# epilogue address arithmetic + first load group of P4/P6/P7/P9/P11/P15 moved above the ALIGN_EPI barrier (leading half's requests fly while it waits for the trailing half)
# speedup vs baseline: 1.0006x; 1.0006x over previous
.LBB0_384:
	ds_read_b128 v[148:151], v155
	ds_read_b128 v[160:163], v155 offset:1024
	ds_read_b128 v[164:167], v155 offset:2048
	ds_read_b128 v[168:171], v155 offset:3072
	ds_read_b128 v[172:175], v156
	ds_read_b128 v[176:179], v156 offset:1024
	ds_read_b128 v[180:183], v156 offset:2048
	ds_read_b128 v[184:187], v156 offset:3072
	s_add_u32 s30, s28, 0xfff80080
	s_addc_u32 s31, s29, -1
	s_cmp_eq_u32 s59, 28
	s_cselect_b32 s35, s19, s31
	s_cselect_b32 s34, s25, s30
	s_cselect_b32 s31, s17, s58
	s_cselect_b32 s30, s56, s57
	v_lshl_add_u64 v[220:221], s[28:29], 0, v[138:139]
	s_add_i32 m0, s27, 0xc000
	ds_read_b128 v[188:191], v157
	ds_read_b128 v[192:195], v157 offset:1024
	ds_read_b128 v[196:199], v157 offset:2048
	ds_read_b128 v[200:203], v157 offset:3072
	ds_read_b128 v[204:207], v157 offset:4096
	ds_read_b128 v[208:211], v157 offset:5120
	ds_read_b128 v[212:215], v157 offset:6144
	ds_read_b128 v[216:219], v157 offset:7168
	global_load_lds_dwordx4 v[220:221], off
	v_lshl_add_u64 v[220:221], s[28:29], 0, v[140:141]
	s_add_i32 m0, s27, 0xe000
	s_nop 0
	global_load_lds_dwordx4 v[220:221], off
	s_waitcnt vmcnt(8)
	s_waitcnt lgkmcnt(0)
	s_barrier
	s_setprio 1
	s_waitcnt lgkmcnt(0)
	v_mfma_f32_16x16x32_bf16 v[126:129], v[148:151], v[188:191], v[126:129]
	v_mfma_f32_16x16x32_bf16 v[122:125], v[164:167], v[188:191], v[122:125]
	v_mfma_f32_16x16x32_bf16 v[110:113], v[148:151], v[196:199], v[110:113]
	v_mfma_f32_16x16x32_bf16 v[106:109], v[164:167], v[196:199], v[106:109]
	v_mfma_f32_16x16x32_bf16 v[94:97], v[148:151], v[204:207], v[94:97]
	v_mfma_f32_16x16x32_bf16 v[90:93], v[164:167], v[204:207], v[90:93]
	v_mfma_f32_16x16x32_bf16 v[78:81], v[148:151], v[212:215], v[78:81]
	v_mfma_f32_16x16x32_bf16 v[74:77], v[164:167], v[212:215], v[74:77]
	v_mfma_f32_16x16x32_bf16 v[126:129], v[160:163], v[192:195], v[126:129]
	v_mfma_f32_16x16x32_bf16 v[122:125], v[168:171], v[192:195], v[122:125]
	v_mfma_f32_16x16x32_bf16 v[110:113], v[160:163], v[200:203], v[110:113]
	v_mfma_f32_16x16x32_bf16 v[106:109], v[168:171], v[200:203], v[106:109]
	v_mfma_f32_16x16x32_bf16 v[94:97], v[160:163], v[208:211], v[94:97]
	v_mfma_f32_16x16x32_bf16 v[90:93], v[168:171], v[208:211], v[90:93]
	v_mfma_f32_16x16x32_bf16 v[78:81], v[160:163], v[216:219], v[78:81]
	v_mfma_f32_16x16x32_bf16 v[74:77], v[168:171], v[216:219], v[74:77]
	s_setprio 0
	s_setprio 1
	v_mfma_f32_16x16x32_bf16 v[118:121], v[172:175], v[188:191], v[118:121]
	v_mfma_f32_16x16x32_bf16 v[114:117], v[180:183], v[188:191], v[114:117]
	v_mfma_f32_16x16x32_bf16 v[102:105], v[172:175], v[196:199], v[102:105]
	v_mfma_f32_16x16x32_bf16 v[98:101], v[180:183], v[196:199], v[98:101]
	v_mfma_f32_16x16x32_bf16 v[86:89], v[172:175], v[204:207], v[86:89]
	v_mfma_f32_16x16x32_bf16 v[82:85], v[180:183], v[204:207], v[82:85]
	v_mfma_f32_16x16x32_bf16 v[70:73], v[172:175], v[212:215], v[70:73]
	v_mfma_f32_16x16x32_bf16 v[66:69], v[180:183], v[212:215], v[66:69]
	v_mfma_f32_16x16x32_bf16 v[118:121], v[176:179], v[192:195], v[118:121]
	v_mfma_f32_16x16x32_bf16 v[114:117], v[184:187], v[192:195], v[114:117]
	v_mfma_f32_16x16x32_bf16 v[102:105], v[176:179], v[200:203], v[102:105]
	v_mfma_f32_16x16x32_bf16 v[98:101], v[184:187], v[200:203], v[98:101]
	v_mfma_f32_16x16x32_bf16 v[86:89], v[176:179], v[208:211], v[86:89]
	v_mfma_f32_16x16x32_bf16 v[82:85], v[184:187], v[208:211], v[82:85]
	v_mfma_f32_16x16x32_bf16 v[70:73], v[176:179], v[216:219], v[70:73]
	v_mfma_f32_16x16x32_bf16 v[66:69], v[184:187], v[216:219], v[66:69]
	s_setprio 0
	s_barrier
	s_add_i32 s60, s45, s36
	v_lshl_add_u64 v[220:221], s[30:31], 0, v[132:133]
	s_mov_b32 m0, s60
	ds_read_b128 v[188:191], v157 offset:16384
	ds_read_b128 v[192:195], v157 offset:17408
	ds_read_b128 v[196:199], v157 offset:18432
	ds_read_b128 v[200:203], v157 offset:19456
	ds_read_b128 v[204:207], v157 offset:20480
	ds_read_b128 v[208:211], v157 offset:21504
	ds_read_b128 v[212:215], v157 offset:22528
	ds_read_b128 v[216:219], v157 offset:23552
	global_load_lds_dwordx4 v[220:221], off
	s_add_i32 m0, s60, 0x2000
	s_add_u32 s60, s30, 0x80000
	v_lshl_add_u64 v[222:223], s[30:31], 0, v[136:137]
	s_addc_u32 s61, s31, 0
	s_add_i32 s62, s54, s36
	global_load_lds_dwordx4 v[222:223], off
	v_lshl_add_u64 v[224:225], s[60:61], 0, v[132:133]
	s_mov_b32 m0, s62
	v_lshl_add_u64 v[226:227], s[34:35], 0, v[134:135]
	global_load_lds_dwordx4 v[224:225], off
	v_lshl_add_u64 v[224:225], s[60:61], 0, v[136:137]
	s_add_i32 m0, s62, 0x2000
	s_nop 0
	global_load_lds_dwordx4 v[224:225], off
	v_lshl_add_u64 v[224:225], s[34:35], 0, v[130:131]
	s_mov_b32 m0, s27
	s_nop 0
	global_load_lds_dwordx4 v[224:225], off
	s_mov_b32 m0, s37
	s_nop 0
	global_load_lds_dwordx4 v[226:227], off
	s_waitcnt vmcnt(8)
	s_waitcnt lgkmcnt(0)
	s_barrier
	s_setprio 1
	s_waitcnt lgkmcnt(0)
	v_mfma_f32_16x16x32_bf16 v[62:65], v[148:151], v[188:191], v[62:65]
	v_mfma_f32_16x16x32_bf16 v[58:61], v[164:167], v[188:191], v[58:61]
	v_mfma_f32_16x16x32_bf16 v[46:49], v[148:151], v[196:199], v[46:49]
	v_mfma_f32_16x16x32_bf16 v[42:45], v[164:167], v[196:199], v[42:45]
	v_mfma_f32_16x16x32_bf16 v[30:33], v[148:151], v[204:207], v[30:33]
	v_mfma_f32_16x16x32_bf16 v[26:29], v[164:167], v[204:207], v[26:29]
	v_mfma_f32_16x16x32_bf16 v[14:17], v[148:151], v[212:215], v[14:17]
	v_mfma_f32_16x16x32_bf16 v[10:13], v[164:167], v[212:215], v[10:13]
	v_mfma_f32_16x16x32_bf16 v[62:65], v[160:163], v[192:195], v[62:65]
	v_mfma_f32_16x16x32_bf16 v[58:61], v[168:171], v[192:195], v[58:61]
	v_mfma_f32_16x16x32_bf16 v[46:49], v[160:163], v[200:203], v[46:49]
	v_mfma_f32_16x16x32_bf16 v[42:45], v[168:171], v[200:203], v[42:45]
	v_mfma_f32_16x16x32_bf16 v[30:33], v[160:163], v[208:211], v[30:33]
	v_mfma_f32_16x16x32_bf16 v[26:29], v[168:171], v[208:211], v[26:29]
	v_mfma_f32_16x16x32_bf16 v[14:17], v[160:163], v[216:219], v[14:17]
	v_mfma_f32_16x16x32_bf16 v[10:13], v[168:171], v[216:219], v[10:13]
	s_setprio 0
	s_setprio 1
	v_mfma_f32_16x16x32_bf16 v[54:57], v[172:175], v[188:191], v[54:57]
	v_mfma_f32_16x16x32_bf16 v[50:53], v[180:183], v[188:191], v[50:53]
	v_mfma_f32_16x16x32_bf16 v[38:41], v[172:175], v[196:199], v[38:41]
	v_mfma_f32_16x16x32_bf16 v[34:37], v[180:183], v[196:199], v[34:37]
	v_mfma_f32_16x16x32_bf16 v[22:25], v[172:175], v[204:207], v[22:25]
	v_mfma_f32_16x16x32_bf16 v[18:21], v[180:183], v[204:207], v[18:21]
	v_mfma_f32_16x16x32_bf16 v[6:9], v[172:175], v[212:215], v[6:9]
	v_mfma_f32_16x16x32_bf16 v[2:5], v[180:183], v[212:215], v[2:5]
	v_mfma_f32_16x16x32_bf16 v[54:57], v[176:179], v[192:195], v[54:57]
	v_mfma_f32_16x16x32_bf16 v[50:53], v[184:187], v[192:195], v[50:53]
	v_mfma_f32_16x16x32_bf16 v[38:41], v[176:179], v[200:203], v[38:41]
	v_mfma_f32_16x16x32_bf16 v[34:37], v[184:187], v[200:203], v[34:37]
	v_mfma_f32_16x16x32_bf16 v[22:25], v[176:179], v[208:211], v[22:25]
	v_mfma_f32_16x16x32_bf16 v[18:21], v[184:187], v[208:211], v[18:21]
	v_mfma_f32_16x16x32_bf16 v[6:9], v[176:179], v[216:219], v[6:9]
	v_mfma_f32_16x16x32_bf16 v[2:5], v[184:187], v[216:219], v[2:5]
	s_setprio 0
	s_barrier
	s_add_i32 s60, 0, 0x18000
	s_add_i32 s61, 0, 0x1c000
	v_add_u32_e32 v168, s60, v153
	v_add_u32_e32 v184, s61, v153
	ds_read_b128 v[148:151], v168
	ds_read_b128 v[160:163], v168 offset:1024
	ds_read_b128 v[164:167], v168 offset:2048
	ds_read_b128 v[168:171], v168 offset:3072
	ds_read_b128 v[172:175], v184
	ds_read_b128 v[176:179], v184 offset:1024
	ds_read_b128 v[180:183], v184 offset:2048
	ds_read_b128 v[184:187], v184 offset:3072
	s_add_u32 s34, s34, 0x80000
	s_addc_u32 s35, s35, 0
	s_mov_b32 m0, s38
	v_lshl_add_u64 v[228:229], s[34:35], 0, v[130:131]
	ds_read_b128 v[188:191], v157 offset:32768
	ds_read_b128 v[192:195], v157 offset:33792
	ds_read_b128 v[196:199], v157 offset:34816
	ds_read_b128 v[200:203], v157 offset:35840
	ds_read_b128 v[204:207], v157 offset:36864
	ds_read_b128 v[208:211], v157 offset:37888
	ds_read_b128 v[212:215], v157 offset:38912
	ds_read_b128 v[216:219], v157 offset:39936
	global_load_lds_dwordx4 v[228:229], off
	v_lshl_add_u64 v[228:229], s[34:35], 0, v[134:135]
	s_mov_b32 m0, s39
	s_nop 0
	global_load_lds_dwordx4 v[228:229], off
	s_waitcnt vmcnt(8)
	s_waitcnt lgkmcnt(0)
	s_barrier
	s_setprio 1
	s_waitcnt lgkmcnt(0)
	v_mfma_f32_16x16x32_bf16 v[126:129], v[148:151], v[188:191], v[126:129]
	v_mfma_f32_16x16x32_bf16 v[122:125], v[164:167], v[188:191], v[122:125]
	v_mfma_f32_16x16x32_bf16 v[110:113], v[148:151], v[196:199], v[110:113]
	v_mfma_f32_16x16x32_bf16 v[106:109], v[164:167], v[196:199], v[106:109]
	v_mfma_f32_16x16x32_bf16 v[94:97], v[148:151], v[204:207], v[94:97]
	v_mfma_f32_16x16x32_bf16 v[90:93], v[164:167], v[204:207], v[90:93]
	v_mfma_f32_16x16x32_bf16 v[78:81], v[148:151], v[212:215], v[78:81]
	v_mfma_f32_16x16x32_bf16 v[74:77], v[164:167], v[212:215], v[74:77]
	v_mfma_f32_16x16x32_bf16 v[126:129], v[160:163], v[192:195], v[126:129]
	v_mfma_f32_16x16x32_bf16 v[122:125], v[168:171], v[192:195], v[122:125]
	v_mfma_f32_16x16x32_bf16 v[110:113], v[160:163], v[200:203], v[110:113]
	v_mfma_f32_16x16x32_bf16 v[106:109], v[168:171], v[200:203], v[106:109]
	v_mfma_f32_16x16x32_bf16 v[94:97], v[160:163], v[208:211], v[94:97]
	v_mfma_f32_16x16x32_bf16 v[90:93], v[168:171], v[208:211], v[90:93]
	v_mfma_f32_16x16x32_bf16 v[78:81], v[160:163], v[216:219], v[78:81]
	v_mfma_f32_16x16x32_bf16 v[74:77], v[168:171], v[216:219], v[74:77]
	s_setprio 0
	s_setprio 1
	v_mfma_f32_16x16x32_bf16 v[118:121], v[172:175], v[188:191], v[118:121]
	v_mfma_f32_16x16x32_bf16 v[114:117], v[180:183], v[188:191], v[114:117]
	v_mfma_f32_16x16x32_bf16 v[102:105], v[172:175], v[196:199], v[102:105]
	v_mfma_f32_16x16x32_bf16 v[98:101], v[180:183], v[196:199], v[98:101]
	v_mfma_f32_16x16x32_bf16 v[86:89], v[172:175], v[204:207], v[86:89]
	v_mfma_f32_16x16x32_bf16 v[82:85], v[180:183], v[204:207], v[82:85]
	v_mfma_f32_16x16x32_bf16 v[70:73], v[172:175], v[212:215], v[70:73]
	v_mfma_f32_16x16x32_bf16 v[66:69], v[180:183], v[212:215], v[66:69]
	v_mfma_f32_16x16x32_bf16 v[118:121], v[176:179], v[192:195], v[118:121]
	v_mfma_f32_16x16x32_bf16 v[114:117], v[184:187], v[192:195], v[114:117]
	v_mfma_f32_16x16x32_bf16 v[102:105], v[176:179], v[200:203], v[102:105]
	v_mfma_f32_16x16x32_bf16 v[98:101], v[184:187], v[200:203], v[98:101]
	v_mfma_f32_16x16x32_bf16 v[86:89], v[176:179], v[208:211], v[86:89]
	v_mfma_f32_16x16x32_bf16 v[82:85], v[184:187], v[208:211], v[82:85]
	v_mfma_f32_16x16x32_bf16 v[70:73], v[176:179], v[216:219], v[70:73]
	v_mfma_f32_16x16x32_bf16 v[66:69], v[184:187], v[216:219], v[66:69]
	s_setprio 0
	s_barrier
	s_add_i32 s34, s60, s36
	v_lshl_add_u64 v[220:221], v[220:221], 0, s[12:13]
	s_mov_b32 m0, s34
	ds_read_b128 v[188:191], v157 offset:49152
	ds_read_b128 v[192:195], v157 offset:50176
	ds_read_b128 v[196:199], v157 offset:51200
	ds_read_b128 v[200:203], v157 offset:52224
	ds_read_b128 v[204:207], v157 offset:53248
	ds_read_b128 v[208:211], v157 offset:54272
	ds_read_b128 v[212:215], v157 offset:55296
	ds_read_b128 v[216:219], v157 offset:56320
	global_load_lds_dwordx4 v[220:221], off
	s_add_i32 m0, s34, 0x2000
	s_add_u32 s30, s30, 0x80080
	v_lshl_add_u64 v[220:221], v[222:223], 0, s[12:13]
	s_addc_u32 s31, s31, 0
	s_add_i32 s34, s61, s36
	global_load_lds_dwordx4 v[220:221], off
	v_lshl_add_u64 v[220:221], s[30:31], 0, v[132:133]
	s_mov_b32 m0, s34
	s_nop 0
	global_load_lds_dwordx4 v[220:221], off
	v_lshl_add_u64 v[220:221], s[30:31], 0, v[136:137]
	s_add_i32 m0, s34, 0x2000
	s_nop 0
	global_load_lds_dwordx4 v[220:221], off
	v_lshl_add_u64 v[220:221], v[224:225], 0, s[12:13]
	s_mov_b32 m0, s41
	s_nop 0
	global_load_lds_dwordx4 v[220:221], off
	v_lshl_add_u64 v[220:221], v[226:227], 0, s[12:13]
	s_mov_b32 m0, s42
	s_nop 0
	global_load_lds_dwordx4 v[220:221], off
	s_waitcnt vmcnt(8)
	s_waitcnt lgkmcnt(0)
	s_barrier
	s_setprio 1
	s_waitcnt lgkmcnt(0)
	v_mfma_f32_16x16x32_bf16 v[62:65], v[148:151], v[188:191], v[62:65]
	v_mfma_f32_16x16x32_bf16 v[58:61], v[164:167], v[188:191], v[58:61]
	v_mfma_f32_16x16x32_bf16 v[46:49], v[148:151], v[196:199], v[46:49]
	v_mfma_f32_16x16x32_bf16 v[42:45], v[164:167], v[196:199], v[42:45]
	v_mfma_f32_16x16x32_bf16 v[30:33], v[148:151], v[204:207], v[30:33]
	v_mfma_f32_16x16x32_bf16 v[26:29], v[164:167], v[204:207], v[26:29]
	v_mfma_f32_16x16x32_bf16 v[14:17], v[148:151], v[212:215], v[14:17]
	v_mfma_f32_16x16x32_bf16 v[10:13], v[164:167], v[212:215], v[10:13]
	v_mfma_f32_16x16x32_bf16 v[62:65], v[160:163], v[192:195], v[62:65]
	v_mfma_f32_16x16x32_bf16 v[58:61], v[168:171], v[192:195], v[58:61]
	v_mfma_f32_16x16x32_bf16 v[46:49], v[160:163], v[200:203], v[46:49]
	v_mfma_f32_16x16x32_bf16 v[42:45], v[168:171], v[200:203], v[42:45]
	v_mfma_f32_16x16x32_bf16 v[30:33], v[160:163], v[208:211], v[30:33]
	v_mfma_f32_16x16x32_bf16 v[26:29], v[168:171], v[208:211], v[26:29]
	v_mfma_f32_16x16x32_bf16 v[14:17], v[160:163], v[216:219], v[14:17]
	v_mfma_f32_16x16x32_bf16 v[10:13], v[168:171], v[216:219], v[10:13]
	s_setprio 0
	s_setprio 1
	v_mfma_f32_16x16x32_bf16 v[54:57], v[172:175], v[188:191], v[54:57]
	v_mfma_f32_16x16x32_bf16 v[50:53], v[180:183], v[188:191], v[50:53]
	v_mfma_f32_16x16x32_bf16 v[38:41], v[172:175], v[196:199], v[38:41]
	v_mfma_f32_16x16x32_bf16 v[34:37], v[180:183], v[196:199], v[34:37]
	v_mfma_f32_16x16x32_bf16 v[22:25], v[172:175], v[204:207], v[22:25]
	v_mfma_f32_16x16x32_bf16 v[18:21], v[180:183], v[204:207], v[18:21]
	v_mfma_f32_16x16x32_bf16 v[6:9], v[172:175], v[212:215], v[6:9]
	v_mfma_f32_16x16x32_bf16 v[2:5], v[180:183], v[212:215], v[2:5]
	v_mfma_f32_16x16x32_bf16 v[54:57], v[176:179], v[192:195], v[54:57]
	v_mfma_f32_16x16x32_bf16 v[50:53], v[184:187], v[192:195], v[50:53]
	v_mfma_f32_16x16x32_bf16 v[38:41], v[176:179], v[200:203], v[38:41]
	v_mfma_f32_16x16x32_bf16 v[34:37], v[184:187], v[200:203], v[34:37]
	v_mfma_f32_16x16x32_bf16 v[22:25], v[176:179], v[208:211], v[22:25]
	v_mfma_f32_16x16x32_bf16 v[18:21], v[184:187], v[208:211], v[18:21]
	v_mfma_f32_16x16x32_bf16 v[6:9], v[176:179], v[216:219], v[6:9]
	v_mfma_f32_16x16x32_bf16 v[2:5], v[184:187], v[216:219], v[2:5]
	s_setprio 0
	s_barrier
	s_add_i32 s59, s59, 2
	s_add_u32 s28, s28, 0x100
	s_addc_u32 s29, s29, 0
	s_add_u32 s57, s57, 0x100
	s_addc_u32 s58, s58, 0
	s_cmp_gt_u32 s59, 29
	s_cbranch_scc0 .LBB0_384
	v_lshl_add_u32 v150, s24, 8, v152
	v_lshl_or_b32 v148, s26, 8, v154
	v_ashrrev_i32_e32 v151, 31, v150
	v_ashrrev_i32_e32 v149, 31, v148
	v_lshlrev_b64 v[160:161], 11, v[150:151]
	v_lshl_add_u64 v[168:169], v[160:161], 0, v[148:149]
	v_lshl_add_u64 v[170:171], v[168:169], 2, s[48:49]
	v_mov_b32_e32 v222, v170
	v_mov_b32_e32 v223, v171
	v_mov_b32_e32 v240, 0x20000
	v_mov_b32_e32 v241, 0
	global_load_dwordx4 v[174:177], v[222:223], off
	global_load_dwordx4 v[178:181], v[222:223], off offset:16
	global_load_dwordx4 v[182:185], v[222:223], off offset:512
	global_load_dwordx4 v[190:193], v[222:223], off offset:528
	v_lshl_add_u64 v[222:223], v[240:241], 0, v[222:223]
	global_load_dwordx4 v[194:197], v[222:223], off
	global_load_dwordx4 v[198:201], v[222:223], off offset:16
	global_load_dwordx4 v[202:205], v[222:223], off offset:512
	global_load_dwordx4 v[206:209], v[222:223], off offset:528
	v_lshl_add_u64 v[222:223], v[240:241], 0, v[222:223]
	global_load_dwordx4 v[210:213], v[222:223], off
	global_load_dwordx4 v[214:217], v[222:223], off offset:16
	global_load_dwordx4 v[218:221], v[222:223], off offset:512
	global_load_dwordx4 v[228:231], v[222:223], off offset:528
	s_and_b64 vcc, exec, s[14:15]
	s_cbranch_vccz .LBB0_387
	s_barrier
.LBB0_387:
	s_nop 0
	s_nop 0
	v_lshl_add_u64 v[168:169], v[168:169], 1, s[50:51]
	s_waitcnt vmcnt(8)
	s_nop 1
	v_mov_b32_e32 v160, v174
	v_mov_b32_e32 v161, v175
	v_mov_b32_e32 v162, v176
	v_mov_b32_e32 v163, v177
	v_mov_b32_e32 v164, v178
	v_mov_b32_e32 v165, v179
	v_mov_b32_e32 v166, v180
	v_mov_b32_e32 v167, v181
	v_pk_add_f32 v[128:129], v[128:129], v[162:163]
	v_pk_add_f32 v[172:173], v[126:127], v[160:161]
	v_pk_add_f32 v[166:167], v[124:125], v[166:167]
	v_pk_add_f32 v[164:165], v[122:123], v[164:165]
	v_cvt_pk_bf16_f32 v122, v172, v173
	v_cvt_pk_bf16_f32 v123, v128, v129
	v_mul_f32_e32 v129, v129, v129
	v_cvt_pk_bf16_f32 v124, v164, v165
	v_cvt_pk_bf16_f32 v125, v166, v167
	global_store_dwordx4 v[168:169], v[122:125], off
	s_nop 0
	s_nop 0
	s_nop 0
	v_and_b32_e32 v123, 64, v159
	v_mul_f32_e32 v170, v173, v173
	v_mul_f32_e32 v165, v165, v165
	v_mul_f32_e32 v167, v167, v167
	v_xor_b32_e32 v122, 16, v159
	v_add_u32_e32 v123, 64, v123
	v_fmac_f32_e32 v170, v172, v172
	v_fmac_f32_e32 v129, v128, v128
	v_fmac_f32_e32 v165, v164, v164
	v_fmac_f32_e32 v167, v166, v166
	v_cmp_lt_i32_e32 vcc, v122, v123
	v_add_f32_e32 v128, v170, v129
	v_add_f32_e32 v129, v165, v167
	v_cndmask_b32_e32 v122, v159, v122, vcc
	v_add_f32_e32 v128, v128, v129
	v_lshlrev_b32_e32 v122, 2, v122
	s_nop 1
	v_mov_b32_e32 v124, v182
	v_mov_b32_e32 v125, v183
	v_mov_b32_e32 v126, v184
	v_mov_b32_e32 v127, v185
	v_pk_add_f32 v[120:121], v[120:121], v[126:127]
	v_pk_add_f32 v[118:119], v[118:119], v[124:125]
	s_nop 1
	v_mov_b32_e32 v160, v190
	v_mov_b32_e32 v161, v191
	v_mov_b32_e32 v162, v192
	v_mov_b32_e32 v163, v193
	v_lshl_add_u64 v[222:223], v[240:241], 0, v[222:223]
	global_load_dwordx4 v[174:177], v[222:223], off
	global_load_dwordx4 v[178:181], v[222:223], off offset:16
	global_load_dwordx4 v[182:185], v[222:223], off offset:512
	global_load_dwordx4 v[190:193], v[222:223], off offset:528
	v_pk_add_f32 v[124:125], v[116:117], v[162:163]
	v_pk_add_f32 v[126:127], v[114:115], v[160:161]
	v_mul_f32_e32 v114, v119, v119
	v_mul_f32_e32 v115, v121, v121
	v_mul_f32_e32 v116, v127, v127
	v_mul_f32_e32 v117, v125, v125
	v_fmac_f32_e32 v114, v118, v118
	v_fmac_f32_e32 v115, v120, v120
	v_fmac_f32_e32 v116, v126, v126
	v_fmac_f32_e32 v117, v124, v124
	v_add_f32_e32 v114, v114, v115
	v_add_f32_e32 v115, v116, v117
	v_add_f32_e32 v114, v114, v115
	v_add_f32_e32 v114, v128, v114
	ds_bpermute_b32 v115, v122, v114
	v_xor_b32_e32 v116, 32, v159
	v_cmp_lt_i32_e32 vcc, v116, v123
	v_cvt_pk_bf16_f32 v118, v118, v119
	v_cvt_pk_bf16_f32 v119, v120, v121
	s_waitcnt lgkmcnt(0)
	v_add_f32_e32 v114, v114, v115
	v_cvt_pk_bf16_f32 v120, v126, v127
	v_cvt_pk_bf16_f32 v121, v124, v125
	v_cndmask_b32_e32 v116, v159, v116, vcc
	v_lshlrev_b32_e32 v116, 2, v116
	ds_bpermute_b32 v115, v116, v114
	global_store_dwordx4 v[168:169], v[118:121], off offset:256
	s_and_saveexec_b64 s[24:25], s[4:5]
	s_cbranch_execz .LBB0_389
	s_waitcnt lgkmcnt(0)
	v_add_f32_e32 v114, v114, v115
	v_fma_f32 v114, v114, s55, 0.5
	v_trunc_f32_e32 v114, v114
	v_mul_f32_e32 v115, 0x2f800000, v114
	v_floor_f32_e32 v115, v115
	v_fmac_f32_e32 v114, 0xcf800000, v115
	v_cvt_u32_f32_e32 v114, v114
	v_cvt_u32_f32_e32 v115, v115
	v_lshl_add_u64 v[118:119], v[150:151], 3, s[10:11]
	global_atomic_add_x2 v[118:119], v[114:115], off

.LBB0_471:
	ds_read_b128 v[148:151], v160
	ds_read_b128 v[152:155], v160 offset:1024
	ds_read_b128 v[166:169], v160 offset:2048
	ds_read_b128 v[170:173], v160 offset:3072
	ds_read_b128 v[174:177], v161
	ds_read_b128 v[178:181], v161 offset:1024
	ds_read_b128 v[182:185], v161 offset:2048
	ds_read_b128 v[186:189], v161 offset:3072
	s_add_u32 s28, s26, 0xfff80080
	s_addc_u32 s29, s27, -1
	s_cmp_eq_u32 s59, 28
	s_cselect_b32 s31, s19, s29
	s_cselect_b32 s30, s55, s28
	s_cselect_b32 s29, s17, s58
	s_cselect_b32 s28, s56, s57
	v_lshl_add_u64 v[222:223], s[26:27], 0, v[138:139]
	s_add_i32 m0, s25, 0xc000
	ds_read_b128 v[190:193], v162
	ds_read_b128 v[194:197], v162 offset:1024
	ds_read_b128 v[198:201], v162 offset:2048
	ds_read_b128 v[202:205], v162 offset:3072
	ds_read_b128 v[206:209], v162 offset:4096
	ds_read_b128 v[210:213], v162 offset:5120
	ds_read_b128 v[214:217], v162 offset:6144
	ds_read_b128 v[218:221], v162 offset:7168
	global_load_lds_dwordx4 v[222:223], off
	v_lshl_add_u64 v[222:223], s[26:27], 0, v[140:141]
	s_add_i32 m0, s25, 0xe000
	s_nop 0
	global_load_lds_dwordx4 v[222:223], off
	s_waitcnt vmcnt(8)
	s_waitcnt lgkmcnt(0)
	s_barrier
	s_setprio 1
	s_waitcnt lgkmcnt(0)
	v_mfma_f32_16x16x32_bf16 v[118:121], v[148:151], v[190:193], v[118:121]
	v_mfma_f32_16x16x32_bf16 v[114:117], v[166:169], v[190:193], v[114:117]
	v_mfma_f32_16x16x32_bf16 v[102:105], v[148:151], v[198:201], v[102:105]
	v_mfma_f32_16x16x32_bf16 v[98:101], v[166:169], v[198:201], v[98:101]
	v_mfma_f32_16x16x32_bf16 v[86:89], v[148:151], v[206:209], v[86:89]
	v_mfma_f32_16x16x32_bf16 v[82:85], v[166:169], v[206:209], v[82:85]
	v_mfma_f32_16x16x32_bf16 v[74:77], v[148:151], v[214:217], v[74:77]
	v_mfma_f32_16x16x32_bf16 v[70:73], v[166:169], v[214:217], v[70:73]
	v_mfma_f32_16x16x32_bf16 v[118:121], v[152:155], v[194:197], v[118:121]
	v_mfma_f32_16x16x32_bf16 v[114:117], v[170:173], v[194:197], v[114:117]
	v_mfma_f32_16x16x32_bf16 v[102:105], v[152:155], v[202:205], v[102:105]
	v_mfma_f32_16x16x32_bf16 v[98:101], v[170:173], v[202:205], v[98:101]
	v_mfma_f32_16x16x32_bf16 v[86:89], v[152:155], v[210:213], v[86:89]
	v_mfma_f32_16x16x32_bf16 v[82:85], v[170:173], v[210:213], v[82:85]
	v_mfma_f32_16x16x32_bf16 v[74:77], v[152:155], v[218:221], v[74:77]
	v_mfma_f32_16x16x32_bf16 v[70:73], v[170:173], v[218:221], v[70:73]
	s_setprio 0
	s_setprio 1
	v_mfma_f32_16x16x32_bf16 v[126:129], v[174:177], v[190:193], v[126:129]
	v_mfma_f32_16x16x32_bf16 v[122:125], v[182:185], v[190:193], v[122:125]
	v_mfma_f32_16x16x32_bf16 v[110:113], v[174:177], v[198:201], v[110:113]
	v_mfma_f32_16x16x32_bf16 v[106:109], v[182:185], v[198:201], v[106:109]
	v_mfma_f32_16x16x32_bf16 v[94:97], v[174:177], v[206:209], v[94:97]
	v_mfma_f32_16x16x32_bf16 v[90:93], v[182:185], v[206:209], v[90:93]
	v_mfma_f32_16x16x32_bf16 v[78:81], v[174:177], v[214:217], v[78:81]
	v_mfma_f32_16x16x32_bf16 v[66:69], v[182:185], v[214:217], v[66:69]
	v_mfma_f32_16x16x32_bf16 v[126:129], v[178:181], v[194:197], v[126:129]
	v_mfma_f32_16x16x32_bf16 v[122:125], v[186:189], v[194:197], v[122:125]
	v_mfma_f32_16x16x32_bf16 v[110:113], v[178:181], v[202:205], v[110:113]
	v_mfma_f32_16x16x32_bf16 v[106:109], v[186:189], v[202:205], v[106:109]
	v_mfma_f32_16x16x32_bf16 v[94:97], v[178:181], v[210:213], v[94:97]
	v_mfma_f32_16x16x32_bf16 v[90:93], v[186:189], v[210:213], v[90:93]
	v_mfma_f32_16x16x32_bf16 v[78:81], v[178:181], v[218:221], v[78:81]
	v_mfma_f32_16x16x32_bf16 v[66:69], v[186:189], v[218:221], v[66:69]
	s_setprio 0
	s_barrier
	s_add_i32 s60, s44, s34
	v_lshl_add_u64 v[222:223], s[28:29], 0, v[134:135]
	s_mov_b32 m0, s60
	ds_read_b128 v[190:193], v162 offset:16384
	ds_read_b128 v[194:197], v162 offset:17408
	ds_read_b128 v[198:201], v162 offset:18432
	ds_read_b128 v[202:205], v162 offset:19456
	ds_read_b128 v[206:209], v162 offset:20480
	ds_read_b128 v[210:213], v162 offset:21504
	ds_read_b128 v[214:217], v162 offset:22528
	ds_read_b128 v[218:221], v162 offset:23552
	global_load_lds_dwordx4 v[222:223], off
	s_add_i32 m0, s60, 0x2000
	s_add_u32 s60, s28, 0x80000
	v_lshl_add_u64 v[224:225], s[28:29], 0, v[130:131]
	s_addc_u32 s61, s29, 0
	s_add_i32 s62, s45, s34
	global_load_lds_dwordx4 v[224:225], off
	v_lshl_add_u64 v[226:227], s[60:61], 0, v[134:135]
	s_mov_b32 m0, s62
	v_lshl_add_u64 v[228:229], s[30:31], 0, v[132:133]
	global_load_lds_dwordx4 v[226:227], off
	v_lshl_add_u64 v[226:227], s[60:61], 0, v[130:131]
	s_add_i32 m0, s62, 0x2000
	s_nop 0
	global_load_lds_dwordx4 v[226:227], off
	v_lshl_add_u64 v[226:227], s[30:31], 0, v[136:137]
	s_mov_b32 m0, s25
	s_nop 0
	global_load_lds_dwordx4 v[226:227], off
	s_mov_b32 m0, s37
	s_nop 0
	global_load_lds_dwordx4 v[228:229], off
	s_waitcnt vmcnt(8)
	s_waitcnt lgkmcnt(0)
	s_barrier
	s_setprio 1
	s_waitcnt lgkmcnt(0)
	v_mfma_f32_16x16x32_bf16 v[58:61], v[148:151], v[190:193], v[58:61]
	v_mfma_f32_16x16x32_bf16 v[54:57], v[166:169], v[190:193], v[54:57]
	v_mfma_f32_16x16x32_bf16 v[42:45], v[148:151], v[198:201], v[42:45]
	v_mfma_f32_16x16x32_bf16 v[38:41], v[166:169], v[198:201], v[38:41]
	v_mfma_f32_16x16x32_bf16 v[26:29], v[148:151], v[206:209], v[26:29]
	v_mfma_f32_16x16x32_bf16 v[22:25], v[166:169], v[206:209], v[22:25]
	v_mfma_f32_16x16x32_bf16 v[6:9], v[148:151], v[214:217], v[6:9]
	v_mfma_f32_16x16x32_bf16 v[2:5], v[166:169], v[214:217], v[2:5]
	v_mfma_f32_16x16x32_bf16 v[58:61], v[152:155], v[194:197], v[58:61]
	v_mfma_f32_16x16x32_bf16 v[54:57], v[170:173], v[194:197], v[54:57]
	v_mfma_f32_16x16x32_bf16 v[42:45], v[152:155], v[202:205], v[42:45]
	v_mfma_f32_16x16x32_bf16 v[38:41], v[170:173], v[202:205], v[38:41]
	v_mfma_f32_16x16x32_bf16 v[26:29], v[152:155], v[210:213], v[26:29]
	v_mfma_f32_16x16x32_bf16 v[22:25], v[170:173], v[210:213], v[22:25]
	v_mfma_f32_16x16x32_bf16 v[6:9], v[152:155], v[218:221], v[6:9]
	v_mfma_f32_16x16x32_bf16 v[2:5], v[170:173], v[218:221], v[2:5]
	s_setprio 0
	s_setprio 1
	v_mfma_f32_16x16x32_bf16 v[62:65], v[174:177], v[190:193], v[62:65]
	v_mfma_f32_16x16x32_bf16 v[50:53], v[182:185], v[190:193], v[50:53]
	v_mfma_f32_16x16x32_bf16 v[46:49], v[174:177], v[198:201], v[46:49]
	v_mfma_f32_16x16x32_bf16 v[34:37], v[182:185], v[198:201], v[34:37]
	v_mfma_f32_16x16x32_bf16 v[30:33], v[174:177], v[206:209], v[30:33]
	v_mfma_f32_16x16x32_bf16 v[18:21], v[182:185], v[206:209], v[18:21]
	v_mfma_f32_16x16x32_bf16 v[14:17], v[174:177], v[214:217], v[14:17]
	v_mfma_f32_16x16x32_bf16 v[10:13], v[182:185], v[214:217], v[10:13]
	v_mfma_f32_16x16x32_bf16 v[62:65], v[178:181], v[194:197], v[62:65]
	v_mfma_f32_16x16x32_bf16 v[50:53], v[186:189], v[194:197], v[50:53]
	v_mfma_f32_16x16x32_bf16 v[46:49], v[178:181], v[202:205], v[46:49]
	v_mfma_f32_16x16x32_bf16 v[34:37], v[186:189], v[202:205], v[34:37]
	v_mfma_f32_16x16x32_bf16 v[30:33], v[178:181], v[210:213], v[30:33]
	v_mfma_f32_16x16x32_bf16 v[18:21], v[186:189], v[210:213], v[18:21]
	v_mfma_f32_16x16x32_bf16 v[14:17], v[178:181], v[218:221], v[14:17]
	v_mfma_f32_16x16x32_bf16 v[10:13], v[186:189], v[218:221], v[10:13]
	s_setprio 0
	s_barrier
	s_add_i32 s60, 0, 0x18000
	v_add_u32_e32 v165, s60, v157
	s_add_i32 s61, 0, 0x1c000
	ds_read_b128 v[148:151], v165
	ds_read_b128 v[152:155], v165 offset:1024
	ds_read_b128 v[166:169], v165 offset:2048
	ds_read_b128 v[170:173], v165 offset:3072
	v_add_u32_e32 v165, s61, v157
	ds_read_b128 v[174:177], v165
	ds_read_b128 v[178:181], v165 offset:1024
	ds_read_b128 v[182:185], v165 offset:2048
	ds_read_b128 v[186:189], v165 offset:3072
	s_add_u32 s30, s30, 0x80000
	s_addc_u32 s31, s31, 0
	s_mov_b32 m0, s38
	v_lshl_add_u64 v[230:231], s[30:31], 0, v[136:137]
	ds_read_b128 v[190:193], v162 offset:32768
	ds_read_b128 v[194:197], v162 offset:33792
	ds_read_b128 v[198:201], v162 offset:34816
	ds_read_b128 v[202:205], v162 offset:35840
	ds_read_b128 v[206:209], v162 offset:36864
	ds_read_b128 v[210:213], v162 offset:37888
	ds_read_b128 v[214:217], v162 offset:38912
	ds_read_b128 v[218:221], v162 offset:39936
	global_load_lds_dwordx4 v[230:231], off
	v_lshl_add_u64 v[230:231], s[30:31], 0, v[132:133]
	s_mov_b32 m0, s39
	s_nop 0
	global_load_lds_dwordx4 v[230:231], off
	s_waitcnt vmcnt(8)
	s_waitcnt lgkmcnt(0)
	s_barrier
	s_setprio 1
	s_waitcnt lgkmcnt(0)
	v_mfma_f32_16x16x32_bf16 v[118:121], v[148:151], v[190:193], v[118:121]
	v_mfma_f32_16x16x32_bf16 v[114:117], v[166:169], v[190:193], v[114:117]
	v_mfma_f32_16x16x32_bf16 v[102:105], v[148:151], v[198:201], v[102:105]
	v_mfma_f32_16x16x32_bf16 v[98:101], v[166:169], v[198:201], v[98:101]
	v_mfma_f32_16x16x32_bf16 v[86:89], v[148:151], v[206:209], v[86:89]
	v_mfma_f32_16x16x32_bf16 v[82:85], v[166:169], v[206:209], v[82:85]
	v_mfma_f32_16x16x32_bf16 v[74:77], v[148:151], v[214:217], v[74:77]
	v_mfma_f32_16x16x32_bf16 v[70:73], v[166:169], v[214:217], v[70:73]
	v_mfma_f32_16x16x32_bf16 v[118:121], v[152:155], v[194:197], v[118:121]
	v_mfma_f32_16x16x32_bf16 v[114:117], v[170:173], v[194:197], v[114:117]
	v_mfma_f32_16x16x32_bf16 v[102:105], v[152:155], v[202:205], v[102:105]
	v_mfma_f32_16x16x32_bf16 v[98:101], v[170:173], v[202:205], v[98:101]
	v_mfma_f32_16x16x32_bf16 v[86:89], v[152:155], v[210:213], v[86:89]
	v_mfma_f32_16x16x32_bf16 v[82:85], v[170:173], v[210:213], v[82:85]
	v_mfma_f32_16x16x32_bf16 v[74:77], v[152:155], v[218:221], v[74:77]
	v_mfma_f32_16x16x32_bf16 v[70:73], v[170:173], v[218:221], v[70:73]
	s_setprio 0
	s_setprio 1
	v_mfma_f32_16x16x32_bf16 v[126:129], v[174:177], v[190:193], v[126:129]
	v_mfma_f32_16x16x32_bf16 v[122:125], v[182:185], v[190:193], v[122:125]
	v_mfma_f32_16x16x32_bf16 v[110:113], v[174:177], v[198:201], v[110:113]
	v_mfma_f32_16x16x32_bf16 v[106:109], v[182:185], v[198:201], v[106:109]
	v_mfma_f32_16x16x32_bf16 v[94:97], v[174:177], v[206:209], v[94:97]
	v_mfma_f32_16x16x32_bf16 v[90:93], v[182:185], v[206:209], v[90:93]
	v_mfma_f32_16x16x32_bf16 v[78:81], v[174:177], v[214:217], v[78:81]
	v_mfma_f32_16x16x32_bf16 v[66:69], v[182:185], v[214:217], v[66:69]
	v_mfma_f32_16x16x32_bf16 v[126:129], v[178:181], v[194:197], v[126:129]
	v_mfma_f32_16x16x32_bf16 v[122:125], v[186:189], v[194:197], v[122:125]
	v_mfma_f32_16x16x32_bf16 v[110:113], v[178:181], v[202:205], v[110:113]
	v_mfma_f32_16x16x32_bf16 v[106:109], v[186:189], v[202:205], v[106:109]
	v_mfma_f32_16x16x32_bf16 v[94:97], v[178:181], v[210:213], v[94:97]
	v_mfma_f32_16x16x32_bf16 v[90:93], v[186:189], v[210:213], v[90:93]
	v_mfma_f32_16x16x32_bf16 v[78:81], v[178:181], v[218:221], v[78:81]
	v_mfma_f32_16x16x32_bf16 v[66:69], v[186:189], v[218:221], v[66:69]
	s_setprio 0
	s_barrier
	s_add_i32 s30, s60, s34
	v_lshl_add_u64 v[222:223], v[222:223], 0, s[12:13]
	s_mov_b32 m0, s30
	ds_read_b128 v[190:193], v162 offset:49152
	ds_read_b128 v[194:197], v162 offset:50176
	ds_read_b128 v[198:201], v162 offset:51200
	ds_read_b128 v[202:205], v162 offset:52224
	ds_read_b128 v[206:209], v162 offset:53248
	ds_read_b128 v[210:213], v162 offset:54272
	ds_read_b128 v[214:217], v162 offset:55296
	ds_read_b128 v[218:221], v162 offset:56320
	global_load_lds_dwordx4 v[222:223], off
	s_add_i32 m0, s30, 0x2000
	s_add_u32 s28, s28, 0x80080
	v_lshl_add_u64 v[222:223], v[224:225], 0, s[12:13]
	s_addc_u32 s29, s29, 0
	s_add_i32 s30, s61, s34
	global_load_lds_dwordx4 v[222:223], off
	v_lshl_add_u64 v[222:223], s[28:29], 0, v[134:135]
	s_mov_b32 m0, s30
	s_nop 0
	global_load_lds_dwordx4 v[222:223], off
	v_lshl_add_u64 v[222:223], s[28:29], 0, v[130:131]
	s_add_i32 m0, s30, 0x2000
	s_nop 0
	global_load_lds_dwordx4 v[222:223], off
	v_lshl_add_u64 v[222:223], v[226:227], 0, s[12:13]
	s_mov_b32 m0, s41
	s_nop 0
	global_load_lds_dwordx4 v[222:223], off
	v_lshl_add_u64 v[222:223], v[228:229], 0, s[12:13]
	s_mov_b32 m0, s42
	s_nop 0
	global_load_lds_dwordx4 v[222:223], off
	s_waitcnt vmcnt(8)
	s_waitcnt lgkmcnt(0)
	s_barrier
	s_setprio 1
	s_waitcnt lgkmcnt(0)
	v_mfma_f32_16x16x32_bf16 v[58:61], v[148:151], v[190:193], v[58:61]
	v_mfma_f32_16x16x32_bf16 v[54:57], v[166:169], v[190:193], v[54:57]
	v_mfma_f32_16x16x32_bf16 v[42:45], v[148:151], v[198:201], v[42:45]
	v_mfma_f32_16x16x32_bf16 v[38:41], v[166:169], v[198:201], v[38:41]
	v_mfma_f32_16x16x32_bf16 v[26:29], v[148:151], v[206:209], v[26:29]
	v_mfma_f32_16x16x32_bf16 v[22:25], v[166:169], v[206:209], v[22:25]
	v_mfma_f32_16x16x32_bf16 v[6:9], v[148:151], v[214:217], v[6:9]
	v_mfma_f32_16x16x32_bf16 v[2:5], v[166:169], v[214:217], v[2:5]
	v_mfma_f32_16x16x32_bf16 v[58:61], v[152:155], v[194:197], v[58:61]
	v_mfma_f32_16x16x32_bf16 v[54:57], v[170:173], v[194:197], v[54:57]
	v_mfma_f32_16x16x32_bf16 v[42:45], v[152:155], v[202:205], v[42:45]
	v_mfma_f32_16x16x32_bf16 v[38:41], v[170:173], v[202:205], v[38:41]
	v_mfma_f32_16x16x32_bf16 v[26:29], v[152:155], v[210:213], v[26:29]
	v_mfma_f32_16x16x32_bf16 v[22:25], v[170:173], v[210:213], v[22:25]
	v_mfma_f32_16x16x32_bf16 v[6:9], v[152:155], v[218:221], v[6:9]
	v_mfma_f32_16x16x32_bf16 v[2:5], v[170:173], v[218:221], v[2:5]
	s_setprio 0
	s_setprio 1
	v_mfma_f32_16x16x32_bf16 v[62:65], v[174:177], v[190:193], v[62:65]
	v_mfma_f32_16x16x32_bf16 v[50:53], v[182:185], v[190:193], v[50:53]
	v_mfma_f32_16x16x32_bf16 v[46:49], v[174:177], v[198:201], v[46:49]
	v_mfma_f32_16x16x32_bf16 v[34:37], v[182:185], v[198:201], v[34:37]
	v_mfma_f32_16x16x32_bf16 v[30:33], v[174:177], v[206:209], v[30:33]
	v_mfma_f32_16x16x32_bf16 v[18:21], v[182:185], v[206:209], v[18:21]
	v_mfma_f32_16x16x32_bf16 v[14:17], v[174:177], v[214:217], v[14:17]
	v_mfma_f32_16x16x32_bf16 v[10:13], v[182:185], v[214:217], v[10:13]
	v_mfma_f32_16x16x32_bf16 v[62:65], v[178:181], v[194:197], v[62:65]
	v_mfma_f32_16x16x32_bf16 v[50:53], v[186:189], v[194:197], v[50:53]
	v_mfma_f32_16x16x32_bf16 v[46:49], v[178:181], v[202:205], v[46:49]
	v_mfma_f32_16x16x32_bf16 v[34:37], v[186:189], v[202:205], v[34:37]
	v_mfma_f32_16x16x32_bf16 v[30:33], v[178:181], v[210:213], v[30:33]
	v_mfma_f32_16x16x32_bf16 v[18:21], v[186:189], v[210:213], v[18:21]
	v_mfma_f32_16x16x32_bf16 v[14:17], v[178:181], v[218:221], v[14:17]
	v_mfma_f32_16x16x32_bf16 v[10:13], v[186:189], v[218:221], v[10:13]
	s_setprio 0
	s_barrier
	s_add_i32 s59, s59, 2
	s_add_u32 s26, s26, 0x100
	s_addc_u32 s27, s27, 0
	s_add_u32 s57, s57, 0x100
	s_addc_u32 s58, s58, 0
	s_cmp_gt_u32 s59, 29
	s_cbranch_scc0 .LBB0_471
	v_lshl_add_u32 v152, s24, 8, v156
	v_ashrrev_i32_e32 v153, 31, v152
	v_lshl_add_u64 v[154:155], v[152:153], 3, s[10:11]
	global_load_dwordx2 v[166:167], v[154:155], off
	global_load_dwordx2 v[178:179], v[154:155], off offset:128
	global_load_dwordx2 v[180:181], v[154:155], off offset:256
	global_load_dwordx2 v[182:183], v[154:155], off offset:384
	global_load_dwordx2 v[184:185], v[154:155], off offset:1024
	global_load_dwordx2 v[186:187], v[154:155], off offset:1152
	global_load_dwordx2 v[188:189], v[154:155], off offset:1280
	global_load_dwordx2 v[190:191], v[154:155], off offset:1408
	s_and_b64 vcc, exec, s[14:15]
	s_cbranch_vccz .LBB0_474
	s_barrier
.LBB0_474:
	v_pk_mul_f32 v[126:127], v[118:119], v[126:127]
	v_pk_mul_f32 v[122:123], v[114:115], v[122:123]
	v_pk_mul_f32 v[128:129], v[120:121], v[128:129]
	v_pk_mul_f32 v[124:125], v[116:117], v[124:125]
	v_mov_b32_e32 v168, 0
	v_mov_b32_e32 v169, 0
	v_lshl_or_b32 v148, s54, 7, v159
	v_mov_b64_e32 v[150:151], s[8:9]
	v_or_b32_e32 v170, 16, v152
	v_ashrrev_i32_e32 v171, 31, v170
	v_pk_mul_f32 v[110:111], v[102:103], v[110:111]
	v_pk_mul_f32 v[106:107], v[98:99], v[106:107]
	v_pk_mul_f32 v[112:113], v[104:105], v[112:113]
	v_pk_mul_f32 v[108:109], v[100:101], v[108:109]
	v_pk_mul_f32 v[94:95], v[86:87], v[94:95]
	v_pk_mul_f32 v[90:91], v[82:83], v[90:91]
	v_pk_mul_f32 v[96:97], v[88:89], v[96:97]
	v_pk_mul_f32 v[92:93], v[84:85], v[92:93]
	v_pk_mul_f32 v[78:79], v[74:75], v[78:79]
	v_pk_mul_f32 v[66:67], v[70:71], v[66:67]
	v_pk_mul_f32 v[80:81], v[76:77], v[80:81]
	v_pk_mul_f32 v[68:69], v[72:73], v[68:69]
	v_pk_mul_f32 v[62:63], v[58:59], v[62:63]
	v_pk_mul_f32 v[50:51], v[54:55], v[50:51]
	v_pk_mul_f32 v[64:65], v[60:61], v[64:65]
	v_pk_mul_f32 v[52:53], v[56:57], v[52:53]
	v_pk_mul_f32 v[46:47], v[42:43], v[46:47]
	v_pk_mul_f32 v[34:35], v[38:39], v[34:35]
	v_pk_mul_f32 v[48:49], v[44:45], v[48:49]
	v_pk_mul_f32 v[36:37], v[40:41], v[36:37]
	v_pk_mul_f32 v[30:31], v[26:27], v[30:31]
	v_pk_mul_f32 v[18:19], v[22:23], v[18:19]
	v_pk_mul_f32 v[32:33], v[28:29], v[32:33]
	v_pk_mul_f32 v[20:21], v[24:25], v[20:21]
	v_pk_mul_f32 v[14:15], v[6:7], v[14:15]
	v_pk_mul_f32 v[10:11], v[2:3], v[10:11]
	v_pk_mul_f32 v[16:17], v[8:9], v[16:17]
	v_pk_mul_f32 v[12:13], v[4:5], v[12:13]
	s_andn2_b64 vcc, exec, s[4:5]
	s_mov_b64 s[4:5], -1
	s_waitcnt vmcnt(7)
	v_ffbh_u32_e32 v149, v167
	v_min_u32_e32 v153, 32, v149
	v_lshlrev_b64 v[166:167], v153, v[166:167]
	v_min_u32_e32 v149, 1, v166
	v_or_b32_e32 v149, v167, v149
	v_cvt_f32_u32_e32 v165, v149
	v_sub_u32_e32 v153, 32, v153
	v_ashrrev_i32_e32 v149, 31, v148
	v_mad_i64_i32 v[166:167], s[26:27], v152, s48, v[150:151]
	v_ldexp_f32 v153, v165, v153
	v_fmamk_f32 v153, v153, 0x30000000, v163
	v_rsq_f32_e32 v165, v153
	v_mul_f32_e32 v172, 0x3e000000, v153
	v_mul_f32_e32 v174, 0xbfb8aa3b, v165
	v_pk_mul_f32 v[118:119], v[118:119], v[174:175] op_sel_hi:[1,0]
	v_pk_mul_f32 v[114:115], v[114:115], v[174:175] op_sel_hi:[1,0]
	v_exp_f32_e32 v118, v118
	v_exp_f32_e32 v119, v119
	v_exp_f32_e32 v114, v114
	v_exp_f32_e32 v115, v115
	v_pk_mul_f32 v[120:121], v[120:121], v[174:175] op_sel_hi:[1,0]
	v_pk_mul_f32 v[116:117], v[116:117], v[174:175] op_sel_hi:[1,0]
	v_exp_f32_e32 v120, v120
	v_exp_f32_e32 v121, v121
	v_exp_f32_e32 v116, v116
	v_exp_f32_e32 v117, v117
	v_pk_fma_f32 v[118:119], v[172:173], v[118:119], v[172:173] op_sel_hi:[0,1,0]
	v_pk_fma_f32 v[114:115], v[172:173], v[114:115], v[172:173] op_sel_hi:[0,1,0]
	v_rcp_f32_e32 v118, v118
	v_rcp_f32_e32 v119, v119
	v_rcp_f32_e32 v114, v114
	v_rcp_f32_e32 v115, v115
	v_pk_fma_f32 v[120:121], v[172:173], v[120:121], v[172:173] op_sel_hi:[0,1,0]
	v_pk_fma_f32 v[116:117], v[172:173], v[116:117], v[172:173] op_sel_hi:[0,1,0]
	v_rcp_f32_e32 v120, v120
	v_rcp_f32_e32 v121, v121
	v_rcp_f32_e32 v116, v116
	v_rcp_f32_e32 v117, v117
	v_pk_mul_f32 v[118:119], v[126:127], v[118:119]
	v_pk_mul_f32 v[114:115], v[122:123], v[114:115]
	v_med3_f32 v118, v118, s49, v164
	v_med3_f32 v119, v119, s49, v164
	v_med3_f32 v114, v114, s49, v164
	v_med3_f32 v115, v115, s49, v164
	v_cvt_pk_fp8_f32 v168, v118, v119
	v_cvt_pk_fp8_f32 v169, v114, v115
	v_pk_mul_f32 v[120:121], v[128:129], v[120:121]
	v_pk_mul_f32 v[116:117], v[124:125], v[116:117]
	v_med3_f32 v120, v120, s49, v164
	v_med3_f32 v121, v121, s49, v164
	v_med3_f32 v114, v116, s49, v164
	v_med3_f32 v115, v117, s49, v164
	v_cvt_pk_fp8_f32 v168, v120, v121 op_sel:[0,0,1]
	v_cvt_pk_fp8_f32 v169, v114, v115 op_sel:[0,0,1]
	v_lshl_add_u64 v[114:115], v[166:167], 0, v[148:149]
	v_lshl_add_u64 v[116:117], v[170:171], 3, s[10:11]
	global_store_dwordx2 v[114:115], v[168:169], off
	s_nop 0
	v_mov_b32_e32 v116, 0
	s_waitcnt vmcnt(7)
	v_mov_b32_e32 v114, v178
	v_mov_b32_e32 v115, v179
	v_ffbh_u32_e32 v117, v115
	v_min_u32_e32 v118, 32, v117
	v_lshlrev_b64 v[114:115], v118, v[114:115]
	v_min_u32_e32 v114, 1, v114
	v_or_b32_e32 v114, v115, v114
	v_cvt_f32_u32_e32 v115, v114
	v_sub_u32_e32 v118, 32, v118
	v_mov_b32_e32 v117, 0
	v_or_b32_e32 v114, 32, v152
	v_ldexp_f32 v115, v115, v118
	v_fmamk_f32 v115, v115, 0x30000000, v163
	v_rsq_f32_e32 v121, v115
	v_mul_f32_e32 v120, 0x3e000000, v115
	v_mad_i64_i32 v[118:119], s[26:27], v170, s48, v[150:151]
	v_mul_f32_e32 v122, 0xbfb8aa3b, v121
	v_pk_mul_f32 v[102:103], v[102:103], v[122:123] op_sel_hi:[1,0]
	v_pk_mul_f32 v[98:99], v[98:99], v[122:123] op_sel_hi:[1,0]
	v_exp_f32_e32 v102, v102
	v_exp_f32_e32 v103, v103
	v_exp_f32_e32 v98, v98
	v_exp_f32_e32 v99, v99
	v_pk_mul_f32 v[104:105], v[104:105], v[122:123] op_sel_hi:[1,0]
	v_pk_mul_f32 v[100:101], v[100:101], v[122:123] op_sel_hi:[1,0]
	v_exp_f32_e32 v104, v104
	v_exp_f32_e32 v105, v105
	v_exp_f32_e32 v100, v100
	v_exp_f32_e32 v101, v101
	v_pk_fma_f32 v[102:103], v[120:121], v[102:103], v[120:121] op_sel_hi:[0,1,0]
	v_pk_fma_f32 v[98:99], v[120:121], v[98:99], v[120:121] op_sel_hi:[0,1,0]
	v_rcp_f32_e32 v102, v102
	v_rcp_f32_e32 v103, v103
	v_rcp_f32_e32 v98, v98
	v_rcp_f32_e32 v99, v99
	v_pk_fma_f32 v[104:105], v[120:121], v[104:105], v[120:121] op_sel_hi:[0,1,0]
	v_pk_fma_f32 v[100:101], v[120:121], v[100:101], v[120:121] op_sel_hi:[0,1,0]
	v_rcp_f32_e32 v104, v104
	v_rcp_f32_e32 v105, v105
	v_rcp_f32_e32 v100, v100
	v_rcp_f32_e32 v101, v101
	v_pk_mul_f32 v[102:103], v[110:111], v[102:103]
	v_pk_mul_f32 v[98:99], v[106:107], v[98:99]
	v_med3_f32 v102, v102, s49, v164
	v_med3_f32 v103, v103, s49, v164
	v_med3_f32 v98, v98, s49, v164
	v_med3_f32 v99, v99, s49, v164
	v_cvt_pk_fp8_f32 v116, v102, v103
	v_cvt_pk_fp8_f32 v117, v98, v99
	v_pk_mul_f32 v[104:105], v[112:113], v[104:105]
	v_pk_mul_f32 v[100:101], v[108:109], v[100:101]
	v_med3_f32 v104, v104, s49, v164
	v_med3_f32 v105, v105, s49, v164
	v_med3_f32 v98, v100, s49, v164
	v_med3_f32 v99, v101, s49, v164
	v_cvt_pk_fp8_f32 v116, v104, v105 op_sel:[0,0,1]
	v_cvt_pk_fp8_f32 v117, v98, v99 op_sel:[0,0,1]
	v_ashrrev_i32_e32 v115, 31, v114
	v_lshl_add_u64 v[98:99], v[118:119], 0, v[148:149]
	v_lshl_add_u64 v[100:101], v[114:115], 3, s[10:11]
	global_store_dwordx2 v[98:99], v[116:117], off
	s_nop 0
	v_mov_b32_e32 v100, 0
	s_waitcnt vmcnt(7)
	v_mov_b32_e32 v98, v180
	v_mov_b32_e32 v99, v181
	v_ffbh_u32_e32 v101, v99
	v_min_u32_e32 v102, 32, v101
	v_lshlrev_b64 v[98:99], v102, v[98:99]
	v_min_u32_e32 v98, 1, v98
	v_or_b32_e32 v98, v99, v98
	v_cvt_f32_u32_e32 v99, v98
	v_sub_u32_e32 v102, 32, v102
	v_mov_b32_e32 v101, 0
	v_or_b32_e32 v98, 48, v152
	v_ldexp_f32 v99, v99, v102
	v_fmamk_f32 v99, v99, 0x30000000, v163
	v_rsq_f32_e32 v105, v99
	v_mul_f32_e32 v104, 0x3e000000, v99
	v_mad_i64_i32 v[102:103], s[26:27], v114, s48, v[150:151]
	v_mul_f32_e32 v106, 0xbfb8aa3b, v105
	v_pk_mul_f32 v[86:87], v[86:87], v[106:107] op_sel_hi:[1,0]
	v_pk_mul_f32 v[82:83], v[82:83], v[106:107] op_sel_hi:[1,0]
	v_exp_f32_e32 v86, v86
	v_exp_f32_e32 v87, v87
	v_exp_f32_e32 v82, v82
	v_exp_f32_e32 v83, v83
	v_pk_mul_f32 v[88:89], v[88:89], v[106:107] op_sel_hi:[1,0]
	v_pk_mul_f32 v[84:85], v[84:85], v[106:107] op_sel_hi:[1,0]
	v_exp_f32_e32 v88, v88
	v_exp_f32_e32 v89, v89
	v_exp_f32_e32 v84, v84
	v_exp_f32_e32 v85, v85
	v_pk_fma_f32 v[86:87], v[104:105], v[86:87], v[104:105] op_sel_hi:[0,1,0]
	v_pk_fma_f32 v[82:83], v[104:105], v[82:83], v[104:105] op_sel_hi:[0,1,0]
	v_rcp_f32_e32 v86, v86
	v_rcp_f32_e32 v87, v87
	v_rcp_f32_e32 v82, v82
	v_rcp_f32_e32 v83, v83
	v_pk_fma_f32 v[88:89], v[104:105], v[88:89], v[104:105] op_sel_hi:[0,1,0]
	v_pk_fma_f32 v[84:85], v[104:105], v[84:85], v[104:105] op_sel_hi:[0,1,0]
	v_rcp_f32_e32 v88, v88
	v_rcp_f32_e32 v89, v89
	v_rcp_f32_e32 v84, v84
	v_rcp_f32_e32 v85, v85
	v_pk_mul_f32 v[86:87], v[94:95], v[86:87]
	v_pk_mul_f32 v[82:83], v[90:91], v[82:83]
	v_med3_f32 v86, v86, s49, v164
	v_med3_f32 v87, v87, s49, v164
	v_med3_f32 v82, v82, s49, v164
	v_med3_f32 v83, v83, s49, v164
	v_cvt_pk_fp8_f32 v100, v86, v87
	v_cvt_pk_fp8_f32 v101, v82, v83
	v_pk_mul_f32 v[88:89], v[96:97], v[88:89]
	v_pk_mul_f32 v[84:85], v[92:93], v[84:85]
	v_med3_f32 v88, v88, s49, v164
	v_med3_f32 v89, v89, s49, v164
	v_med3_f32 v82, v84, s49, v164
	v_med3_f32 v83, v85, s49, v164
	v_cvt_pk_fp8_f32 v100, v88, v89 op_sel:[0,0,1]
	v_cvt_pk_fp8_f32 v101, v82, v83 op_sel:[0,0,1]
	v_ashrrev_i32_e32 v99, 31, v98
	v_lshl_add_u64 v[82:83], v[102:103], 0, v[148:149]
	v_lshl_add_u64 v[84:85], v[98:99], 3, s[10:11]
	global_store_dwordx2 v[82:83], v[100:101], off
	s_nop 0
	s_waitcnt vmcnt(7)
	v_mov_b32_e32 v82, v182
	v_mov_b32_e32 v83, v183
	v_ffbh_u32_e32 v84, v83
	v_min_u32_e32 v84, 32, v84
	v_lshlrev_b64 v[82:83], v84, v[82:83]
	v_min_u32_e32 v82, 1, v82
	v_or_b32_e32 v82, v83, v82
	v_cvt_f32_u32_e32 v82, v82
	v_sub_u32_e32 v83, 32, v84
	v_ldexp_f32 v82, v82, v83
	v_fmamk_f32 v84, v82, 0x30000000, v163
	v_rsq_f32_e32 v85, v84
	v_mul_f32_e32 v84, 0x3e000000, v84
	v_mov_b32_e32 v82, 0
	v_mov_b32_e32 v83, 0
	v_mul_f32_e32 v86, 0xbfb8aa3b, v85
	v_pk_mul_f32 v[74:75], v[74:75], v[86:87] op_sel_hi:[1,0]
	v_pk_mul_f32 v[70:71], v[70:71], v[86:87] op_sel_hi:[1,0]
	v_exp_f32_e32 v74, v74
	v_exp_f32_e32 v75, v75
	v_exp_f32_e32 v70, v70
	v_exp_f32_e32 v71, v71
	v_pk_mul_f32 v[76:77], v[76:77], v[86:87] op_sel_hi:[1,0]
	v_pk_mul_f32 v[72:73], v[72:73], v[86:87] op_sel_hi:[1,0]
	v_exp_f32_e32 v76, v76
	v_exp_f32_e32 v77, v77
	v_exp_f32_e32 v72, v72
	v_exp_f32_e32 v73, v73
	v_pk_fma_f32 v[74:75], v[84:85], v[74:75], v[84:85] op_sel_hi:[0,1,0]
	v_pk_fma_f32 v[70:71], v[84:85], v[70:71], v[84:85] op_sel_hi:[0,1,0]
	v_rcp_f32_e32 v74, v74
	v_rcp_f32_e32 v75, v75
	v_rcp_f32_e32 v70, v70
	v_rcp_f32_e32 v71, v71
	v_pk_fma_f32 v[76:77], v[84:85], v[76:77], v[84:85] op_sel_hi:[0,1,0]
	v_pk_fma_f32 v[72:73], v[84:85], v[72:73], v[84:85] op_sel_hi:[0,1,0]
	v_rcp_f32_e32 v76, v76
	v_rcp_f32_e32 v77, v77
	v_rcp_f32_e32 v72, v72
	v_rcp_f32_e32 v73, v73
	v_pk_mul_f32 v[74:75], v[78:79], v[74:75]
	v_pk_mul_f32 v[66:67], v[66:67], v[70:71]
	v_med3_f32 v70, v74, s49, v164
	v_med3_f32 v71, v75, s49, v164
	v_med3_f32 v66, v66, s49, v164
	v_med3_f32 v67, v67, s49, v164
	v_cvt_pk_fp8_f32 v82, v70, v71
	v_cvt_pk_fp8_f32 v83, v66, v67
	v_pk_mul_f32 v[76:77], v[80:81], v[76:77]
	v_pk_mul_f32 v[68:69], v[68:69], v[72:73]
	v_med3_f32 v72, v76, s49, v164
	v_med3_f32 v73, v77, s49, v164
	v_med3_f32 v66, v68, s49, v164
	v_med3_f32 v67, v69, s49, v164
	v_cvt_pk_fp8_f32 v82, v72, v73 op_sel:[0,0,1]
	v_cvt_pk_fp8_f32 v83, v66, v67 op_sel:[0,0,1]
	v_mad_i64_i32 v[66:67], s[26:27], v98, s48, v[150:151]
	v_lshl_add_u64 v[66:67], v[66:67], 0, v[148:149]
	global_store_dwordx2 v[66:67], v[82:83], off
	s_nop 0
	v_add_u32_e32 v71, 0x80, v152
	s_waitcnt vmcnt(7)
	v_mov_b32_e32 v66, v184
	v_mov_b32_e32 v67, v185
	v_ffbh_u32_e32 v68, v67
	v_min_u32_e32 v68, 32, v68
	v_lshlrev_b64 v[66:67], v68, v[66:67]
	v_min_u32_e32 v66, 1, v66
	v_or_b32_e32 v66, v67, v66
	v_cvt_f32_u32_e32 v67, v66
	v_sub_u32_e32 v68, 32, v68
	v_mov_b32_e32 v66, 0
	v_ldexp_f32 v67, v67, v68
	v_fmamk_f32 v68, v67, 0x30000000, v163
	v_rsq_f32_e32 v69, v68
	v_mul_f32_e32 v68, 0x3e000000, v68
	v_mov_b32_e32 v67, 0
	v_mul_f32_e32 v70, 0xbfb8aa3b, v69
	v_pk_mul_f32 v[58:59], v[58:59], v[70:71] op_sel_hi:[1,0]
	v_pk_mul_f32 v[54:55], v[54:55], v[70:71] op_sel_hi:[1,0]
	v_exp_f32_e32 v58, v58
	v_exp_f32_e32 v59, v59
	v_exp_f32_e32 v54, v54
	v_exp_f32_e32 v55, v55
	v_pk_mul_f32 v[60:61], v[60:61], v[70:71] op_sel_hi:[1,0]
	v_pk_mul_f32 v[56:57], v[56:57], v[70:71] op_sel_hi:[1,0]
	v_exp_f32_e32 v60, v60
	v_exp_f32_e32 v61, v61
	v_exp_f32_e32 v56, v56
	v_exp_f32_e32 v57, v57
	v_pk_fma_f32 v[58:59], v[68:69], v[58:59], v[68:69] op_sel_hi:[0,1,0]
	v_pk_fma_f32 v[54:55], v[68:69], v[54:55], v[68:69] op_sel_hi:[0,1,0]
	v_rcp_f32_e32 v58, v58
	v_rcp_f32_e32 v59, v59
	v_rcp_f32_e32 v54, v54
	v_rcp_f32_e32 v55, v55
	v_pk_fma_f32 v[60:61], v[68:69], v[60:61], v[68:69] op_sel_hi:[0,1,0]
	v_pk_fma_f32 v[56:57], v[68:69], v[56:57], v[68:69] op_sel_hi:[0,1,0]
	v_rcp_f32_e32 v60, v60
	v_rcp_f32_e32 v61, v61
	v_rcp_f32_e32 v56, v56
	v_rcp_f32_e32 v57, v57
	v_pk_mul_f32 v[58:59], v[62:63], v[58:59]
	v_pk_mul_f32 v[50:51], v[50:51], v[54:55]
	v_med3_f32 v54, v58, s49, v164
	v_med3_f32 v55, v59, s49, v164
	v_med3_f32 v50, v50, s49, v164
	v_med3_f32 v51, v51, s49, v164
	v_cvt_pk_fp8_f32 v66, v54, v55
	v_cvt_pk_fp8_f32 v67, v50, v51
	v_pk_mul_f32 v[60:61], v[64:65], v[60:61]
	v_pk_mul_f32 v[52:53], v[52:53], v[56:57]
	v_med3_f32 v56, v60, s49, v164
	v_med3_f32 v57, v61, s49, v164
	v_med3_f32 v50, v52, s49, v164
	v_med3_f32 v51, v53, s49, v164
	v_cvt_pk_fp8_f32 v66, v56, v57 op_sel:[0,0,1]
	v_cvt_pk_fp8_f32 v67, v50, v51 op_sel:[0,0,1]
	v_mad_i64_i32 v[50:51], s[26:27], v71, s48, v[150:151]
	v_lshl_add_u64 v[50:51], v[50:51], 0, v[148:149]
	global_store_dwordx2 v[50:51], v[66:67], off
	s_nop 0
	v_add_u32_e32 v55, 0x90, v152
	s_waitcnt vmcnt(7)
	v_mov_b32_e32 v50, v186
	v_mov_b32_e32 v51, v187
	v_ffbh_u32_e32 v52, v51
	v_min_u32_e32 v52, 32, v52
	v_lshlrev_b64 v[50:51], v52, v[50:51]
	v_min_u32_e32 v50, 1, v50
	v_or_b32_e32 v50, v51, v50
	v_cvt_f32_u32_e32 v51, v50
	v_sub_u32_e32 v52, 32, v52
	v_mov_b32_e32 v50, 0
	v_ldexp_f32 v51, v51, v52
	v_fmamk_f32 v52, v51, 0x30000000, v163
	v_rsq_f32_e32 v53, v52
	v_mul_f32_e32 v52, 0x3e000000, v52
	v_mov_b32_e32 v51, 0
	v_mul_f32_e32 v54, 0xbfb8aa3b, v53
	v_pk_mul_f32 v[42:43], v[42:43], v[54:55] op_sel_hi:[1,0]
	v_pk_mul_f32 v[38:39], v[38:39], v[54:55] op_sel_hi:[1,0]
	v_exp_f32_e32 v42, v42
	v_exp_f32_e32 v43, v43
	v_exp_f32_e32 v38, v38
	v_exp_f32_e32 v39, v39
	v_pk_mul_f32 v[44:45], v[44:45], v[54:55] op_sel_hi:[1,0]
	v_pk_mul_f32 v[40:41], v[40:41], v[54:55] op_sel_hi:[1,0]
	v_exp_f32_e32 v44, v44
	v_exp_f32_e32 v45, v45
	v_exp_f32_e32 v40, v40
	v_exp_f32_e32 v41, v41
	v_pk_fma_f32 v[42:43], v[52:53], v[42:43], v[52:53] op_sel_hi:[0,1,0]
	v_pk_fma_f32 v[38:39], v[52:53], v[38:39], v[52:53] op_sel_hi:[0,1,0]
	v_rcp_f32_e32 v42, v42
	v_rcp_f32_e32 v43, v43
	v_rcp_f32_e32 v38, v38
	v_rcp_f32_e32 v39, v39
	v_pk_fma_f32 v[44:45], v[52:53], v[44:45], v[52:53] op_sel_hi:[0,1,0]
	v_pk_fma_f32 v[40:41], v[52:53], v[40:41], v[52:53] op_sel_hi:[0,1,0]
	v_rcp_f32_e32 v44, v44
	v_rcp_f32_e32 v45, v45
	v_rcp_f32_e32 v40, v40
	v_rcp_f32_e32 v41, v41
	v_pk_mul_f32 v[42:43], v[46:47], v[42:43]
	v_pk_mul_f32 v[34:35], v[34:35], v[38:39]
	v_med3_f32 v38, v42, s49, v164
	v_med3_f32 v39, v43, s49, v164
	v_med3_f32 v34, v34, s49, v164
	v_med3_f32 v35, v35, s49, v164
	v_cvt_pk_fp8_f32 v50, v38, v39
	v_cvt_pk_fp8_f32 v51, v34, v35
	v_pk_mul_f32 v[44:45], v[48:49], v[44:45]
	v_pk_mul_f32 v[36:37], v[36:37], v[40:41]
	v_med3_f32 v40, v44, s49, v164
	v_med3_f32 v41, v45, s49, v164
	v_med3_f32 v34, v36, s49, v164
	v_med3_f32 v35, v37, s49, v164
	v_cvt_pk_fp8_f32 v50, v40, v41 op_sel:[0,0,1]
	v_cvt_pk_fp8_f32 v51, v34, v35 op_sel:[0,0,1]
	v_mad_i64_i32 v[34:35], s[26:27], v55, s48, v[150:151]
	v_lshl_add_u64 v[34:35], v[34:35], 0, v[148:149]
	global_store_dwordx2 v[34:35], v[50:51], off
	s_nop 0
	v_add_u32_e32 v39, 0xa0, v152
	s_waitcnt vmcnt(7)
	v_mov_b32_e32 v34, v188
	v_mov_b32_e32 v35, v189
	v_ffbh_u32_e32 v36, v35
	v_min_u32_e32 v36, 32, v36
	v_lshlrev_b64 v[34:35], v36, v[34:35]
	v_min_u32_e32 v34, 1, v34
	v_or_b32_e32 v34, v35, v34
	v_cvt_f32_u32_e32 v35, v34
	v_sub_u32_e32 v36, 32, v36
	v_mov_b32_e32 v34, 0
	v_ldexp_f32 v35, v35, v36
	v_fmamk_f32 v36, v35, 0x30000000, v163
	v_rsq_f32_e32 v37, v36
	v_mul_f32_e32 v36, 0x3e000000, v36
	v_mov_b32_e32 v35, 0
	v_mul_f32_e32 v38, 0xbfb8aa3b, v37
	v_pk_mul_f32 v[26:27], v[26:27], v[38:39] op_sel_hi:[1,0]
	v_pk_mul_f32 v[22:23], v[22:23], v[38:39] op_sel_hi:[1,0]
	v_exp_f32_e32 v26, v26
	v_exp_f32_e32 v27, v27
	v_exp_f32_e32 v22, v22
	v_exp_f32_e32 v23, v23
	v_pk_mul_f32 v[28:29], v[28:29], v[38:39] op_sel_hi:[1,0]
	v_pk_mul_f32 v[24:25], v[24:25], v[38:39] op_sel_hi:[1,0]
	v_exp_f32_e32 v28, v28
	v_exp_f32_e32 v29, v29
	v_exp_f32_e32 v24, v24
	v_exp_f32_e32 v25, v25
	v_pk_fma_f32 v[26:27], v[36:37], v[26:27], v[36:37] op_sel_hi:[0,1,0]
	v_pk_fma_f32 v[22:23], v[36:37], v[22:23], v[36:37] op_sel_hi:[0,1,0]
	v_rcp_f32_e32 v26, v26
	v_rcp_f32_e32 v27, v27
	v_rcp_f32_e32 v22, v22
	v_rcp_f32_e32 v23, v23
	v_pk_fma_f32 v[28:29], v[36:37], v[28:29], v[36:37] op_sel_hi:[0,1,0]
	v_pk_fma_f32 v[24:25], v[36:37], v[24:25], v[36:37] op_sel_hi:[0,1,0]
	v_rcp_f32_e32 v28, v28
	v_rcp_f32_e32 v29, v29
	v_rcp_f32_e32 v24, v24
	v_rcp_f32_e32 v25, v25
	v_pk_mul_f32 v[26:27], v[30:31], v[26:27]
	v_pk_mul_f32 v[18:19], v[18:19], v[22:23]
	v_med3_f32 v22, v26, s49, v164
	v_med3_f32 v23, v27, s49, v164
	v_med3_f32 v18, v18, s49, v164
	v_med3_f32 v19, v19, s49, v164
	v_cvt_pk_fp8_f32 v34, v22, v23
	v_cvt_pk_fp8_f32 v35, v18, v19
	v_pk_mul_f32 v[28:29], v[32:33], v[28:29]
	v_pk_mul_f32 v[20:21], v[20:21], v[24:25]
	v_med3_f32 v24, v28, s49, v164
	v_med3_f32 v25, v29, s49, v164
	v_med3_f32 v18, v20, s49, v164
	v_med3_f32 v19, v21, s49, v164
	v_cvt_pk_fp8_f32 v34, v24, v25 op_sel:[0,0,1]
	v_cvt_pk_fp8_f32 v35, v18, v19 op_sel:[0,0,1]
	v_mad_i64_i32 v[18:19], s[26:27], v39, s48, v[150:151]
	v_lshl_add_u64 v[18:19], v[18:19], 0, v[148:149]
	global_store_dwordx2 v[18:19], v[34:35], off
	s_nop 0
	v_add_u32_e32 v23, 0xb0, v152
	v_mov_b32_e32 v20, 0
	s_waitcnt vmcnt(7)
	v_mov_b32_e32 v18, v190
	v_mov_b32_e32 v19, v191
	v_ffbh_u32_e32 v21, v19
	v_min_u32_e32 v22, 32, v21
	v_lshlrev_b64 v[18:19], v22, v[18:19]
	v_min_u32_e32 v18, 1, v18
	v_or_b32_e32 v18, v19, v18
	v_cvt_f32_u32_e32 v18, v18
	v_sub_u32_e32 v19, 32, v22
	v_mov_b32_e32 v21, 0
	v_ldexp_f32 v18, v18, v19
	v_fmamk_f32 v18, v18, 0x30000000, v163
	v_rsq_f32_e32 v19, v18
	v_mul_f32_e32 v18, 0x3e000000, v18
	v_mul_f32_e32 v22, 0xbfb8aa3b, v19
	v_pk_mul_f32 v[6:7], v[6:7], v[22:23] op_sel_hi:[1,0]
	v_pk_mul_f32 v[2:3], v[2:3], v[22:23] op_sel_hi:[1,0]
	v_exp_f32_e32 v6, v6
	v_exp_f32_e32 v7, v7
	v_exp_f32_e32 v2, v2
	v_exp_f32_e32 v3, v3
	v_pk_mul_f32 v[8:9], v[8:9], v[22:23] op_sel_hi:[1,0]
	v_pk_mul_f32 v[4:5], v[4:5], v[22:23] op_sel_hi:[1,0]
	v_exp_f32_e32 v8, v8
	v_exp_f32_e32 v9, v9
	v_exp_f32_e32 v4, v4
	v_exp_f32_e32 v5, v5
	v_pk_fma_f32 v[6:7], v[18:19], v[6:7], v[18:19] op_sel_hi:[0,1,0]
	v_pk_fma_f32 v[2:3], v[18:19], v[2:3], v[18:19] op_sel_hi:[0,1,0]
	v_rcp_f32_e32 v6, v6
	v_rcp_f32_e32 v7, v7
	v_rcp_f32_e32 v2, v2
	v_rcp_f32_e32 v3, v3
	v_pk_fma_f32 v[8:9], v[18:19], v[8:9], v[18:19] op_sel_hi:[0,1,0]
	v_pk_fma_f32 v[4:5], v[18:19], v[4:5], v[18:19] op_sel_hi:[0,1,0]
	v_rcp_f32_e32 v8, v8
	v_rcp_f32_e32 v9, v9
	v_rcp_f32_e32 v4, v4
	v_rcp_f32_e32 v5, v5
	v_pk_mul_f32 v[6:7], v[14:15], v[6:7]
	v_pk_mul_f32 v[2:3], v[10:11], v[2:3]
	v_med3_f32 v6, v6, s49, v164
	v_med3_f32 v7, v7, s49, v164
	v_med3_f32 v2, v2, s49, v164
	v_med3_f32 v3, v3, s49, v164
	v_cvt_pk_fp8_f32 v20, v6, v7
	v_cvt_pk_fp8_f32 v21, v2, v3
	v_pk_mul_f32 v[8:9], v[16:17], v[8:9]
	v_pk_mul_f32 v[4:5], v[12:13], v[4:5]
	v_med3_f32 v8, v8, s49, v164
	v_med3_f32 v9, v9, s49, v164
	v_med3_f32 v2, v4, s49, v164
	v_med3_f32 v3, v5, s49, v164
	v_cvt_pk_fp8_f32 v20, v8, v9 op_sel:[0,0,1]
	v_cvt_pk_fp8_f32 v21, v2, v3 op_sel:[0,0,1]
	v_mad_i64_i32 v[2:3], s[26:27], v23, s48, v[150:151]
	v_lshl_add_u64 v[2:3], v[2:3], 0, v[148:149]
	global_store_dwordx2 v[2:3], v[20:21], off
	s_cbranch_vccnz .LBB0_467
	s_andn2_b64 vcc, exec, s[6:7]
	s_cbranch_vccnz .LBB0_466
	s_barrier
	s_branch .LBB0_466

.LBB0_556:
	ds_read_b128 v[162:165], v155
	ds_read_b128 v[166:169], v155 offset:1024
	ds_read_b128 v[170:173], v155 offset:2048
	ds_read_b128 v[174:177], v155 offset:3072
	ds_read_b128 v[178:181], v156
	ds_read_b128 v[182:185], v156 offset:1024
	ds_read_b128 v[224:227], v156 offset:2048
	ds_read_b128 v[228:231], v156 offset:3072
	s_add_u32 s22, s20, 0xfff50080
	s_addc_u32 s23, s21, -1
	s_cmp_eq_u32 s55, 40
	s_cselect_b32 s25, s1, s23
	s_cselect_b32 s24, s0, s22
	s_cselect_b32 s23, s19, s54
	s_cselect_b32 s22, s18, s49
	v_lshl_add_u64 v[148:149], s[20:21], 0, v[138:139]
	s_add_i32 m0, s30, 0xc000
	ds_read_b128 v[192:195], v157
	ds_read_b128 v[196:199], v157 offset:1024
	ds_read_b128 v[200:203], v157 offset:2048
	ds_read_b128 v[204:207], v157 offset:3072
	ds_read_b128 v[208:211], v157 offset:4096
	ds_read_b128 v[212:215], v157 offset:5120
	ds_read_b128 v[216:219], v157 offset:6144
	ds_read_b128 v[220:223], v157 offset:7168
	global_load_lds_dwordx4 v[148:149], off
	v_lshl_add_u64 v[148:149], s[20:21], 0, v[140:141]
	s_add_i32 m0, s30, 0xe000
	s_nop 0
	global_load_lds_dwordx4 v[148:149], off
	s_waitcnt vmcnt(8)
	s_waitcnt lgkmcnt(0)
	s_barrier
	s_setprio 1
	s_waitcnt lgkmcnt(0)
	s_nop 0
	v_mfma_scale_f32_16x16x128_f8f6f4 v[126:129], v[162:169], v[192:199], v[126:129], v160, v159 op_sel_hi:[0,0,0]
	v_mfma_scale_f32_16x16x128_f8f6f4 v[122:125], v[170:177], v[192:199], v[122:125], v160, v159 op_sel_hi:[0,0,0]
	v_mfma_scale_f32_16x16x128_f8f6f4 v[110:113], v[162:169], v[200:207], v[110:113], v160, v159 op_sel_hi:[0,0,0]
	v_mfma_scale_f32_16x16x128_f8f6f4 v[106:109], v[170:177], v[200:207], v[106:109], v160, v159 op_sel_hi:[0,0,0]
	v_mfma_scale_f32_16x16x128_f8f6f4 v[94:97], v[162:169], v[208:215], v[94:97], v160, v159 op_sel_hi:[0,0,0]
	v_mfma_scale_f32_16x16x128_f8f6f4 v[90:93], v[170:177], v[208:215], v[90:93], v160, v159 op_sel_hi:[0,0,0]
	v_mfma_scale_f32_16x16x128_f8f6f4 v[78:81], v[162:169], v[216:223], v[78:81], v160, v159 op_sel_hi:[0,0,0]
	v_mfma_scale_f32_16x16x128_f8f6f4 v[74:77], v[170:177], v[216:223], v[74:77], v160, v159 op_sel_hi:[0,0,0]
	s_setprio 0
	s_setprio 1
	s_nop 0
	v_mfma_scale_f32_16x16x128_f8f6f4 v[118:121], v[178:185], v[192:199], v[118:121], v160, v159 op_sel_hi:[0,0,0]
	v_mfma_scale_f32_16x16x128_f8f6f4 v[114:117], v[224:231], v[192:199], v[114:117], v160, v159 op_sel_hi:[0,0,0]
	v_mfma_scale_f32_16x16x128_f8f6f4 v[102:105], v[178:185], v[200:207], v[102:105], v160, v159 op_sel_hi:[0,0,0]
	v_mfma_scale_f32_16x16x128_f8f6f4 v[98:101], v[224:231], v[200:207], v[98:101], v160, v159 op_sel_hi:[0,0,0]
	v_mfma_scale_f32_16x16x128_f8f6f4 v[86:89], v[178:185], v[208:215], v[86:89], v160, v159 op_sel_hi:[0,0,0]
	v_mfma_scale_f32_16x16x128_f8f6f4 v[82:85], v[224:231], v[208:215], v[82:85], v160, v159 op_sel_hi:[0,0,0]
	v_mfma_scale_f32_16x16x128_f8f6f4 v[70:73], v[178:185], v[216:223], v[70:73], v160, v159 op_sel_hi:[0,0,0]
	v_mfma_scale_f32_16x16x128_f8f6f4 v[66:69], v[224:231], v[216:223], v[66:69], v160, v159 op_sel_hi:[0,0,0]
	s_setprio 0
	s_barrier
	s_add_i32 s56, s40, s29
	v_lshl_add_u64 v[190:191], s[22:23], 0, v[132:133]
	s_mov_b32 m0, s56
	ds_read_b128 v[192:195], v157 offset:16384
	ds_read_b128 v[196:199], v157 offset:17408
	ds_read_b128 v[200:203], v157 offset:18432
	ds_read_b128 v[204:207], v157 offset:19456
	ds_read_b128 v[208:211], v157 offset:20480
	ds_read_b128 v[212:215], v157 offset:21504
	ds_read_b128 v[216:219], v157 offset:22528
	ds_read_b128 v[220:223], v157 offset:23552
	global_load_lds_dwordx4 v[190:191], off
	s_add_i32 m0, s56, 0x2000
	s_add_u32 s56, s22, 0xb0000
	v_lshl_add_u64 v[232:233], s[22:23], 0, v[136:137]
	s_addc_u32 s57, s23, 0
	s_add_i32 s58, s41, s29
	global_load_lds_dwordx4 v[232:233], off
	v_lshl_add_u64 v[148:149], s[56:57], 0, v[132:133]
	s_mov_b32 m0, s58
	v_lshl_add_u64 v[234:235], s[24:25], 0, v[130:131]
	global_load_lds_dwordx4 v[148:149], off
	v_lshl_add_u64 v[148:149], s[56:57], 0, v[136:137]
	s_add_i32 m0, s58, 0x2000
	v_lshl_add_u64 v[236:237], s[24:25], 0, v[134:135]
	global_load_lds_dwordx4 v[148:149], off
	s_mov_b32 m0, s30
	s_nop 0
	global_load_lds_dwordx4 v[234:235], off
	s_mov_b32 m0, s31
	s_nop 0
	global_load_lds_dwordx4 v[236:237], off
	s_waitcnt vmcnt(8)
	s_waitcnt lgkmcnt(0)
	s_barrier
	s_setprio 1
	s_waitcnt lgkmcnt(0)
	s_nop 0
	v_mfma_scale_f32_16x16x128_f8f6f4 v[62:65], v[162:169], v[192:199], v[62:65], v160, v159 op_sel_hi:[0,0,0]
	v_mfma_scale_f32_16x16x128_f8f6f4 v[58:61], v[170:177], v[192:199], v[58:61], v160, v159 op_sel_hi:[0,0,0]
	v_mfma_scale_f32_16x16x128_f8f6f4 v[46:49], v[162:169], v[200:207], v[46:49], v160, v159 op_sel_hi:[0,0,0]
	v_mfma_scale_f32_16x16x128_f8f6f4 v[42:45], v[170:177], v[200:207], v[42:45], v160, v159 op_sel_hi:[0,0,0]
	v_mfma_scale_f32_16x16x128_f8f6f4 v[30:33], v[162:169], v[208:215], v[30:33], v160, v159 op_sel_hi:[0,0,0]
	v_mfma_scale_f32_16x16x128_f8f6f4 v[26:29], v[170:177], v[208:215], v[26:29], v160, v159 op_sel_hi:[0,0,0]
	v_mfma_scale_f32_16x16x128_f8f6f4 v[14:17], v[162:169], v[216:223], v[14:17], v160, v159 op_sel_hi:[0,0,0]
	v_mfma_scale_f32_16x16x128_f8f6f4 v[10:13], v[170:177], v[216:223], v[10:13], v160, v159 op_sel_hi:[0,0,0]
	s_setprio 0
	s_setprio 1
	s_nop 0
	v_mfma_scale_f32_16x16x128_f8f6f4 v[54:57], v[178:185], v[192:199], v[54:57], v160, v159 op_sel_hi:[0,0,0]
	v_mfma_scale_f32_16x16x128_f8f6f4 v[50:53], v[224:231], v[192:199], v[50:53], v160, v159 op_sel_hi:[0,0,0]
	v_mfma_scale_f32_16x16x128_f8f6f4 v[38:41], v[178:185], v[200:207], v[38:41], v160, v159 op_sel_hi:[0,0,0]
	v_mfma_scale_f32_16x16x128_f8f6f4 v[34:37], v[224:231], v[200:207], v[34:37], v160, v159 op_sel_hi:[0,0,0]
	v_mfma_scale_f32_16x16x128_f8f6f4 v[148:151], v[178:185], v[208:215], v[22:25], v160, v159 op_sel_hi:[0,0,0]
	v_mfma_scale_f32_16x16x128_f8f6f4 v[186:189], v[224:231], v[208:215], v[18:21], v160, v159 op_sel_hi:[0,0,0]
	v_mfma_scale_f32_16x16x128_f8f6f4 v[178:181], v[178:185], v[216:223], v[6:9], v160, v159 op_sel_hi:[0,0,0]
	v_mfma_scale_f32_16x16x128_f8f6f4 v[182:185], v[224:231], v[216:223], v[2:5], v160, v159 op_sel_hi:[0,0,0]
	s_setprio 0
	s_barrier
	s_add_i32 s56, 0, 0x18000
	s_add_i32 s57, 0, 0x1c000
	v_add_u32_e32 v22, s56, v153
	v_add_u32_e32 v174, s57, v153
	s_nop 0
	ds_read_b128 v[2:5], v22
	ds_read_b128 v[6:9], v22 offset:1024
	ds_read_b128 v[18:21], v22 offset:2048
	ds_read_b128 v[22:25], v22 offset:3072
	ds_read_b128 v[162:165], v174
	ds_read_b128 v[166:169], v174 offset:1024
	ds_read_b128 v[170:173], v174 offset:2048
	ds_read_b128 v[174:177], v174 offset:3072
	s_add_u32 s24, s24, 0xb0000
	s_addc_u32 s25, s25, 0
	s_mov_b32 m0, s33
	v_lshl_add_u64 v[224:225], s[24:25], 0, v[130:131]
	ds_read_b128 v[192:195], v157 offset:32768
	ds_read_b128 v[196:199], v157 offset:33792
	ds_read_b128 v[200:203], v157 offset:34816
	ds_read_b128 v[204:207], v157 offset:35840
	ds_read_b128 v[208:211], v157 offset:36864
	ds_read_b128 v[212:215], v157 offset:37888
	ds_read_b128 v[216:219], v157 offset:38912
	ds_read_b128 v[220:223], v157 offset:39936
	global_load_lds_dwordx4 v[224:225], off
	v_lshl_add_u64 v[224:225], s[24:25], 0, v[134:135]
	s_mov_b32 m0, s34
	s_nop 0
	global_load_lds_dwordx4 v[224:225], off
	s_waitcnt vmcnt(8)
	s_waitcnt lgkmcnt(0)
	s_barrier
	s_setprio 1
	s_waitcnt lgkmcnt(0)
	s_nop 0
	v_mfma_scale_f32_16x16x128_f8f6f4 v[126:129], v[2:9], v[192:199], v[126:129], v160, v159 op_sel_hi:[0,0,0]
	v_mfma_scale_f32_16x16x128_f8f6f4 v[122:125], v[18:25], v[192:199], v[122:125], v160, v159 op_sel_hi:[0,0,0]
	v_mfma_scale_f32_16x16x128_f8f6f4 v[110:113], v[2:9], v[200:207], v[110:113], v160, v159 op_sel_hi:[0,0,0]
	v_mfma_scale_f32_16x16x128_f8f6f4 v[106:109], v[18:25], v[200:207], v[106:109], v160, v159 op_sel_hi:[0,0,0]
	v_mfma_scale_f32_16x16x128_f8f6f4 v[94:97], v[2:9], v[208:215], v[94:97], v160, v159 op_sel_hi:[0,0,0]
	v_mfma_scale_f32_16x16x128_f8f6f4 v[90:93], v[18:25], v[208:215], v[90:93], v160, v159 op_sel_hi:[0,0,0]
	v_mfma_scale_f32_16x16x128_f8f6f4 v[78:81], v[2:9], v[216:223], v[78:81], v160, v159 op_sel_hi:[0,0,0]
	v_mfma_scale_f32_16x16x128_f8f6f4 v[74:77], v[18:25], v[216:223], v[74:77], v160, v159 op_sel_hi:[0,0,0]
	s_setprio 0
	s_setprio 1
	s_nop 0
	v_mfma_scale_f32_16x16x128_f8f6f4 v[118:121], v[162:169], v[192:199], v[118:121], v160, v159 op_sel_hi:[0,0,0]
	v_mfma_scale_f32_16x16x128_f8f6f4 v[114:117], v[170:177], v[192:199], v[114:117], v160, v159 op_sel_hi:[0,0,0]
	v_mfma_scale_f32_16x16x128_f8f6f4 v[102:105], v[162:169], v[200:207], v[102:105], v160, v159 op_sel_hi:[0,0,0]
	v_mfma_scale_f32_16x16x128_f8f6f4 v[98:101], v[170:177], v[200:207], v[98:101], v160, v159 op_sel_hi:[0,0,0]
	v_mfma_scale_f32_16x16x128_f8f6f4 v[86:89], v[162:169], v[208:215], v[86:89], v160, v159 op_sel_hi:[0,0,0]
	v_mfma_scale_f32_16x16x128_f8f6f4 v[82:85], v[170:177], v[208:215], v[82:85], v160, v159 op_sel_hi:[0,0,0]
	v_mfma_scale_f32_16x16x128_f8f6f4 v[70:73], v[162:169], v[216:223], v[70:73], v160, v159 op_sel_hi:[0,0,0]
	v_mfma_scale_f32_16x16x128_f8f6f4 v[66:69], v[170:177], v[216:223], v[66:69], v160, v159 op_sel_hi:[0,0,0]
	s_setprio 0
	s_barrier
	s_add_i32 s24, s56, s29
	v_lshl_add_u64 v[190:191], v[190:191], 0, s[14:15]
	s_mov_b32 m0, s24
	ds_read_b128 v[192:195], v157 offset:49152
	ds_read_b128 v[196:199], v157 offset:50176
	ds_read_b128 v[200:203], v157 offset:51200
	ds_read_b128 v[204:207], v157 offset:52224
	ds_read_b128 v[208:211], v157 offset:53248
	ds_read_b128 v[212:215], v157 offset:54272
	ds_read_b128 v[216:219], v157 offset:55296
	ds_read_b128 v[220:223], v157 offset:56320
	global_load_lds_dwordx4 v[190:191], off
	s_add_i32 m0, s24, 0x2000
	s_add_u32 s22, s22, 0xb0080
	v_lshl_add_u64 v[190:191], v[232:233], 0, s[14:15]
	s_addc_u32 s23, s23, 0
	s_add_i32 s24, s57, s29
	global_load_lds_dwordx4 v[190:191], off
	v_lshl_add_u64 v[190:191], s[22:23], 0, v[132:133]
	s_mov_b32 m0, s24
	s_nop 0
	global_load_lds_dwordx4 v[190:191], off
	v_lshl_add_u64 v[190:191], s[22:23], 0, v[136:137]
	s_add_i32 m0, s24, 0x2000
	s_nop 0
	global_load_lds_dwordx4 v[190:191], off
	v_lshl_add_u64 v[190:191], v[234:235], 0, s[14:15]
	s_mov_b32 m0, s36
	s_nop 0
	global_load_lds_dwordx4 v[190:191], off
	v_lshl_add_u64 v[190:191], v[236:237], 0, s[14:15]
	s_mov_b32 m0, s37
	s_nop 0
	global_load_lds_dwordx4 v[190:191], off
	s_waitcnt vmcnt(8)
	s_waitcnt lgkmcnt(0)
	s_barrier
	s_setprio 1
	s_waitcnt lgkmcnt(0)
	s_nop 0
	v_mfma_scale_f32_16x16x128_f8f6f4 v[62:65], v[2:9], v[192:199], v[62:65], v160, v159 op_sel_hi:[0,0,0]
	v_mfma_scale_f32_16x16x128_f8f6f4 v[58:61], v[18:25], v[192:199], v[58:61], v160, v159 op_sel_hi:[0,0,0]
	v_mfma_scale_f32_16x16x128_f8f6f4 v[46:49], v[2:9], v[200:207], v[46:49], v160, v159 op_sel_hi:[0,0,0]
	v_mfma_scale_f32_16x16x128_f8f6f4 v[42:45], v[18:25], v[200:207], v[42:45], v160, v159 op_sel_hi:[0,0,0]
	v_mfma_scale_f32_16x16x128_f8f6f4 v[30:33], v[2:9], v[208:215], v[30:33], v160, v159 op_sel_hi:[0,0,0]
	v_mfma_scale_f32_16x16x128_f8f6f4 v[26:29], v[18:25], v[208:215], v[26:29], v160, v159 op_sel_hi:[0,0,0]
	v_mfma_scale_f32_16x16x128_f8f6f4 v[14:17], v[2:9], v[216:223], v[14:17], v160, v159 op_sel_hi:[0,0,0]
	v_mfma_scale_f32_16x16x128_f8f6f4 v[10:13], v[18:25], v[216:223], v[10:13], v160, v159 op_sel_hi:[0,0,0]
	s_setprio 0
	s_setprio 1
	s_nop 0
	v_mfma_scale_f32_16x16x128_f8f6f4 v[54:57], v[162:169], v[192:199], v[54:57], v160, v159 op_sel_hi:[0,0,0]
	v_mfma_scale_f32_16x16x128_f8f6f4 v[50:53], v[170:177], v[192:199], v[50:53], v160, v159 op_sel_hi:[0,0,0]
	v_mfma_scale_f32_16x16x128_f8f6f4 v[38:41], v[162:169], v[200:207], v[38:41], v160, v159 op_sel_hi:[0,0,0]
	v_mfma_scale_f32_16x16x128_f8f6f4 v[34:37], v[170:177], v[200:207], v[34:37], v160, v159 op_sel_hi:[0,0,0]
	v_mfma_scale_f32_16x16x128_f8f6f4 v[22:25], v[162:169], v[208:215], v[148:151], v160, v159 op_sel_hi:[0,0,0]
	v_mfma_scale_f32_16x16x128_f8f6f4 v[18:21], v[170:177], v[208:215], v[186:189], v160, v159 op_sel_hi:[0,0,0]
	v_mfma_scale_f32_16x16x128_f8f6f4 v[6:9], v[162:169], v[216:223], v[178:181], v160, v159 op_sel_hi:[0,0,0]
	v_mfma_scale_f32_16x16x128_f8f6f4 v[2:5], v[170:177], v[216:223], v[182:185], v160, v159 op_sel_hi:[0,0,0]
	s_setprio 0
	s_barrier
	s_add_i32 s55, s55, 2
	s_add_u32 s20, s20, 0x100
	s_addc_u32 s21, s21, 0
	s_add_u32 s49, s49, 0x100
	s_addc_u32 s54, s54, 0
	s_cmp_gt_u32 s55, 41
	s_cbranch_scc0 .LBB0_556
	v_lshl_add_u32 v150, s45, 8, v152
	v_ashrrev_i32_e32 v151, 31, v150
	v_lshl_or_b32 v148, s48, 8, v154
	v_lshlrev_b64 v[162:163], 12, v[150:151]
	v_ashrrev_i32_e32 v149, 31, v148
	v_lshl_add_u64 v[162:163], s[50:51], 0, v[162:163]
	v_lshl_add_u64 v[166:167], v[148:149], 1, v[162:163]
	v_mov_b32_e32 v184, v166
	v_mov_b32_e32 v185, v167
	v_mov_b32_e32 v222, 0x10000
	v_mov_b32_e32 v223, 0
	global_load_dwordx4 v[176:179], v[184:185], off
	global_load_dwordx4 v[180:183], v[184:185], off offset:256
	v_lshl_add_u64 v[184:185], v[222:223], 0, v[184:185]
	global_load_dwordx4 v[190:193], v[184:185], off
	global_load_dwordx4 v[194:197], v[184:185], off offset:256
	v_lshl_add_u64 v[184:185], v[222:223], 0, v[184:185]
	global_load_dwordx4 v[198:201], v[184:185], off
	global_load_dwordx4 v[202:205], v[184:185], off offset:256
	v_lshl_add_u64 v[184:185], v[222:223], 0, v[184:185]
	global_load_dwordx4 v[206:209], v[184:185], off
	global_load_dwordx4 v[210:213], v[184:185], off offset:256
	v_lshl_add_u64 v[184:185], v[222:223], 2, v[184:185]
	v_lshl_add_u64 v[184:185], v[222:223], 0, v[184:185]
	global_load_dwordx4 v[214:217], v[184:185], off
	global_load_dwordx4 v[218:221], v[184:185], off offset:256
	s_and_b64 vcc, exec, s[16:17]
	s_cbranch_vccz .LBB0_559
	s_barrier
.LBB0_559:
	s_nop 0
	v_xor_b32_e32 v174, 32, v161
	s_waitcnt vmcnt(8)
	s_nop 1
	v_mov_b32_e32 v162, v176
	v_mov_b32_e32 v163, v177
	v_mov_b32_e32 v164, v178
	v_mov_b32_e32 v165, v179
	v_lshlrev_b32_e32 v168, 16, v162
	v_and_b32_e32 v169, 0xffff0000, v162
	v_lshlrev_b32_e32 v162, 16, v163
	v_and_b32_e32 v163, 0xffff0000, v163
	v_lshlrev_b32_e32 v170, 16, v164
	v_and_b32_e32 v171, 0xffff0000, v164
	v_lshlrev_b32_e32 v164, 16, v165
	v_and_b32_e32 v165, 0xffff0000, v165
	v_pk_add_f32 v[128:129], v[128:129], v[162:163]
	v_pk_add_f32 v[168:169], v[126:127], v[168:169]
	v_pk_add_f32 v[172:173], v[124:125], v[164:165]
	v_pk_add_f32 v[170:171], v[122:123], v[170:171]
	v_cvt_pk_bf16_f32 v124, v168, v169
	v_cvt_pk_bf16_f32 v125, v128, v129
	v_mul_f32_e32 v169, v169, v169
	v_cvt_pk_bf16_f32 v126, v170, v171
	v_cvt_pk_bf16_f32 v127, v172, v173
	s_nop 0
	v_mul_f32_e32 v129, v129, v129
	v_mul_f32_e32 v171, v171, v171
	v_mul_f32_e32 v173, v173, v173
	v_fmac_f32_e32 v169, v168, v168
	v_fmac_f32_e32 v129, v128, v128
	v_fmac_f32_e32 v171, v170, v170
	v_fmac_f32_e32 v173, v172, v172
	v_add_f32_e32 v128, v169, v129
	v_add_f32_e32 v129, v171, v173
	v_add_f32_e32 v170, v128, v129
	v_and_b32_e32 v123, 64, v161
	v_xor_b32_e32 v122, 16, v161
	v_add_u32_e32 v123, 64, v123
	v_cmp_lt_i32_e32 vcc, v122, v123
	global_store_dwordx4 v[166:167], v[124:127], off
	s_nop 1
	v_mov_b32_e32 v162, v180
	v_mov_b32_e32 v163, v181
	v_mov_b32_e32 v164, v182
	v_mov_b32_e32 v165, v183
	v_lshl_add_u64 v[184:185], v[222:223], 0, v[184:185]
	global_load_dwordx4 v[176:179], v[184:185], off
	global_load_dwordx4 v[180:183], v[184:185], off offset:256
	v_lshlrev_b32_e32 v128, 16, v162
	v_and_b32_e32 v129, 0xffff0000, v162
	v_lshlrev_b32_e32 v162, 16, v163
	v_and_b32_e32 v163, 0xffff0000, v163
	v_lshlrev_b32_e32 v168, 16, v164
	v_and_b32_e32 v169, 0xffff0000, v164
	v_lshlrev_b32_e32 v164, 16, v165
	v_and_b32_e32 v165, 0xffff0000, v165
	v_pk_add_f32 v[120:121], v[120:121], v[162:163]
	v_pk_add_f32 v[118:119], v[118:119], v[128:129]
	v_pk_add_f32 v[128:129], v[116:117], v[164:165]
	v_pk_add_f32 v[162:163], v[114:115], v[168:169]
	v_mul_f32_e32 v114, v119, v119
	v_mul_f32_e32 v115, v121, v121
	v_mul_f32_e32 v116, v163, v163
	v_mul_f32_e32 v117, v129, v129
	v_fmac_f32_e32 v114, v118, v118
	v_fmac_f32_e32 v115, v120, v120
	v_fmac_f32_e32 v116, v162, v162
	v_fmac_f32_e32 v117, v128, v128
	v_add_f32_e32 v114, v114, v115
	v_add_f32_e32 v115, v116, v117
	v_cndmask_b32_e32 v122, v161, v122, vcc
	v_add_f32_e32 v114, v114, v115
	v_lshlrev_b32_e32 v122, 2, v122
	v_add_f32_e32 v114, v170, v114
	ds_bpermute_b32 v115, v122, v114
	v_cmp_lt_i32_e32 vcc, v174, v123
	v_cvt_pk_bf16_f32 v118, v118, v119
	v_cvt_pk_bf16_f32 v119, v120, v121
	v_cvt_pk_bf16_f32 v120, v162, v163
	s_waitcnt lgkmcnt(0)
	v_add_f32_e32 v114, v114, v115
	v_cvt_pk_bf16_f32 v121, v128, v129
	v_cndmask_b32_e32 v116, v161, v174, vcc
	v_lshlrev_b32_e32 v116, 2, v116
	ds_bpermute_b32 v115, v116, v114
	global_store_dwordx4 v[166:167], v[118:121], off offset:256
	s_and_saveexec_b64 s[20:21], s[4:5]
	s_cbranch_execz .LBB0_561
	s_waitcnt lgkmcnt(0)
	v_add_f32_e32 v114, v114, v115
	v_fma_f32 v114, v114, s42, 0.5
	v_trunc_f32_e32 v114, v114
	v_mul_f32_e32 v115, 0x2f800000, v114
	v_floor_f32_e32 v115, v115
	v_fmac_f32_e32 v114, 0xcf800000, v115
	v_cvt_u32_f32_e32 v114, v114
	v_cvt_u32_f32_e32 v115, v115
	v_lshl_add_u64 v[118:119], v[150:151], 3, s[12:13]
	global_atomic_add_x2 v[118:119], v[114:115], off

.LBB0_651:
	ds_read_b128 v[148:151], v157
	ds_read_b128 v[162:165], v157 offset:1024
	ds_read_b128 v[166:169], v157 offset:2048
	ds_read_b128 v[170:173], v157 offset:3072
	ds_read_b128 v[174:177], v159
	ds_read_b128 v[178:181], v159 offset:1024
	ds_read_b128 v[182:185], v159 offset:2048
	ds_read_b128 v[186:189], v159 offset:3072
	s_add_u32 s36, s34, 0xfff80080
	s_addc_u32 s37, s35, -1
	s_cmp_eq_u32 s66, 28
	s_cselect_b32 s39, s27, s37
	s_cselect_b32 s38, s62, s36
	s_cselect_b32 s37, s25, s65
	s_cselect_b32 s36, s63, s64
	v_lshl_add_u64 v[152:153], s[34:35], 0, v[138:139]
	s_add_i32 m0, s42, 0xc000
	ds_read_b128 v[190:193], v160
	ds_read_b128 v[194:197], v160 offset:1024
	ds_read_b128 v[198:201], v160 offset:2048
	ds_read_b128 v[202:205], v160 offset:3072
	ds_read_b128 v[206:209], v160 offset:4096
	ds_read_b128 v[210:213], v160 offset:5120
	ds_read_b128 v[214:217], v160 offset:6144
	ds_read_b128 v[218:221], v160 offset:7168
	global_load_lds_dwordx4 v[152:153], off
	v_lshl_add_u64 v[152:153], s[34:35], 0, v[140:141]
	s_add_i32 m0, s42, 0xe000
	s_nop 0
	global_load_lds_dwordx4 v[152:153], off
	s_waitcnt vmcnt(8)
	s_waitcnt lgkmcnt(0)
	s_barrier
	s_setprio 1
	s_waitcnt lgkmcnt(0)
	v_mfma_f32_16x16x32_bf16 v[126:129], v[148:151], v[190:193], v[126:129]
	v_mfma_f32_16x16x32_bf16 v[122:125], v[166:169], v[190:193], v[122:125]
	v_mfma_f32_16x16x32_bf16 v[110:113], v[148:151], v[198:201], v[110:113]
	v_mfma_f32_16x16x32_bf16 v[106:109], v[166:169], v[198:201], v[106:109]
	v_mfma_f32_16x16x32_bf16 v[94:97], v[148:151], v[206:209], v[94:97]
	v_mfma_f32_16x16x32_bf16 v[90:93], v[166:169], v[206:209], v[90:93]
	v_mfma_f32_16x16x32_bf16 v[78:81], v[148:151], v[214:217], v[78:81]
	v_mfma_f32_16x16x32_bf16 v[74:77], v[166:169], v[214:217], v[74:77]
	v_mfma_f32_16x16x32_bf16 v[126:129], v[162:165], v[194:197], v[126:129]
	v_mfma_f32_16x16x32_bf16 v[122:125], v[170:173], v[194:197], v[122:125]
	v_mfma_f32_16x16x32_bf16 v[110:113], v[162:165], v[202:205], v[110:113]
	v_mfma_f32_16x16x32_bf16 v[106:109], v[170:173], v[202:205], v[106:109]
	v_mfma_f32_16x16x32_bf16 v[94:97], v[162:165], v[210:213], v[94:97]
	v_mfma_f32_16x16x32_bf16 v[90:93], v[170:173], v[210:213], v[90:93]
	v_mfma_f32_16x16x32_bf16 v[78:81], v[162:165], v[218:221], v[78:81]
	v_mfma_f32_16x16x32_bf16 v[74:77], v[170:173], v[218:221], v[74:77]
	s_setprio 0
	s_setprio 1
	v_mfma_f32_16x16x32_bf16 v[118:121], v[174:177], v[190:193], v[118:121]
	v_mfma_f32_16x16x32_bf16 v[114:117], v[182:185], v[190:193], v[114:117]
	v_mfma_f32_16x16x32_bf16 v[102:105], v[174:177], v[198:201], v[102:105]
	v_mfma_f32_16x16x32_bf16 v[98:101], v[182:185], v[198:201], v[98:101]
	v_mfma_f32_16x16x32_bf16 v[86:89], v[174:177], v[206:209], v[86:89]
	v_mfma_f32_16x16x32_bf16 v[82:85], v[182:185], v[206:209], v[82:85]
	v_mfma_f32_16x16x32_bf16 v[70:73], v[174:177], v[214:217], v[70:73]
	v_mfma_f32_16x16x32_bf16 v[66:69], v[182:185], v[214:217], v[66:69]
	v_mfma_f32_16x16x32_bf16 v[118:121], v[178:181], v[194:197], v[118:121]
	v_mfma_f32_16x16x32_bf16 v[114:117], v[186:189], v[194:197], v[114:117]
	v_mfma_f32_16x16x32_bf16 v[102:105], v[178:181], v[202:205], v[102:105]
	v_mfma_f32_16x16x32_bf16 v[98:101], v[186:189], v[202:205], v[98:101]
	v_mfma_f32_16x16x32_bf16 v[86:89], v[178:181], v[210:213], v[86:89]
	v_mfma_f32_16x16x32_bf16 v[82:85], v[186:189], v[210:213], v[82:85]
	v_mfma_f32_16x16x32_bf16 v[70:73], v[178:181], v[218:221], v[70:73]
	v_mfma_f32_16x16x32_bf16 v[66:69], v[186:189], v[218:221], v[66:69]
	s_setprio 0
	s_barrier
	s_add_i32 s67, s56, s41
	v_lshl_add_u64 v[152:153], s[36:37], 0, v[132:133]
	s_mov_b32 m0, s67
	ds_read_b128 v[190:193], v160 offset:16384
	ds_read_b128 v[194:197], v160 offset:17408
	ds_read_b128 v[198:201], v160 offset:18432
	ds_read_b128 v[202:205], v160 offset:19456
	ds_read_b128 v[206:209], v160 offset:20480
	ds_read_b128 v[210:213], v160 offset:21504
	ds_read_b128 v[214:217], v160 offset:22528
	ds_read_b128 v[218:221], v160 offset:23552
	global_load_lds_dwordx4 v[152:153], off
	s_add_i32 m0, s67, 0x2000
	s_add_u32 s68, s36, 0x80000
	v_lshl_add_u64 v[222:223], s[36:37], 0, v[136:137]
	s_addc_u32 s69, s37, 0
	s_add_i32 s67, s57, s41
	global_load_lds_dwordx4 v[222:223], off
	v_lshl_add_u64 v[224:225], s[68:69], 0, v[132:133]
	s_mov_b32 m0, s67
	v_lshl_add_u64 v[226:227], s[38:39], 0, v[134:135]
	global_load_lds_dwordx4 v[224:225], off
	v_lshl_add_u64 v[224:225], s[68:69], 0, v[136:137]
	s_add_i32 m0, s67, 0x2000
	s_nop 0
	global_load_lds_dwordx4 v[224:225], off
	v_lshl_add_u64 v[224:225], s[38:39], 0, v[130:131]
	s_mov_b32 m0, s42
	s_nop 0
	global_load_lds_dwordx4 v[224:225], off
	s_mov_b32 m0, s43
	s_nop 0
	global_load_lds_dwordx4 v[226:227], off
	s_waitcnt vmcnt(8)
	s_waitcnt lgkmcnt(0)
	s_barrier
	s_setprio 1
	s_waitcnt lgkmcnt(0)
	v_mfma_f32_16x16x32_bf16 v[62:65], v[148:151], v[190:193], v[62:65]
	v_mfma_f32_16x16x32_bf16 v[58:61], v[166:169], v[190:193], v[58:61]
	v_mfma_f32_16x16x32_bf16 v[46:49], v[148:151], v[198:201], v[46:49]
	v_mfma_f32_16x16x32_bf16 v[42:45], v[166:169], v[198:201], v[42:45]
	v_mfma_f32_16x16x32_bf16 v[30:33], v[148:151], v[206:209], v[30:33]
	v_mfma_f32_16x16x32_bf16 v[26:29], v[166:169], v[206:209], v[26:29]
	v_mfma_f32_16x16x32_bf16 v[14:17], v[148:151], v[214:217], v[14:17]
	v_mfma_f32_16x16x32_bf16 v[10:13], v[166:169], v[214:217], v[10:13]
	v_mfma_f32_16x16x32_bf16 v[62:65], v[162:165], v[194:197], v[62:65]
	v_mfma_f32_16x16x32_bf16 v[58:61], v[170:173], v[194:197], v[58:61]
	v_mfma_f32_16x16x32_bf16 v[46:49], v[162:165], v[202:205], v[46:49]
	v_mfma_f32_16x16x32_bf16 v[42:45], v[170:173], v[202:205], v[42:45]
	v_mfma_f32_16x16x32_bf16 v[30:33], v[162:165], v[210:213], v[30:33]
	v_mfma_f32_16x16x32_bf16 v[26:29], v[170:173], v[210:213], v[26:29]
	v_mfma_f32_16x16x32_bf16 v[14:17], v[162:165], v[218:221], v[14:17]
	v_mfma_f32_16x16x32_bf16 v[10:13], v[170:173], v[218:221], v[10:13]
	s_setprio 0
	s_setprio 1
	v_mfma_f32_16x16x32_bf16 v[54:57], v[174:177], v[190:193], v[54:57]
	v_mfma_f32_16x16x32_bf16 v[50:53], v[182:185], v[190:193], v[50:53]
	v_mfma_f32_16x16x32_bf16 v[38:41], v[174:177], v[198:201], v[38:41]
	v_mfma_f32_16x16x32_bf16 v[34:37], v[182:185], v[198:201], v[34:37]
	v_mfma_f32_16x16x32_bf16 v[22:25], v[174:177], v[206:209], v[22:25]
	v_mfma_f32_16x16x32_bf16 v[18:21], v[182:185], v[206:209], v[18:21]
	v_mfma_f32_16x16x32_bf16 v[6:9], v[174:177], v[214:217], v[6:9]
	v_mfma_f32_16x16x32_bf16 v[2:5], v[182:185], v[214:217], v[2:5]
	v_mfma_f32_16x16x32_bf16 v[54:57], v[178:181], v[194:197], v[54:57]
	v_mfma_f32_16x16x32_bf16 v[50:53], v[186:189], v[194:197], v[50:53]
	v_mfma_f32_16x16x32_bf16 v[38:41], v[178:181], v[202:205], v[38:41]
	v_mfma_f32_16x16x32_bf16 v[34:37], v[186:189], v[202:205], v[34:37]
	v_mfma_f32_16x16x32_bf16 v[22:25], v[178:181], v[210:213], v[22:25]
	v_mfma_f32_16x16x32_bf16 v[18:21], v[186:189], v[210:213], v[18:21]
	v_mfma_f32_16x16x32_bf16 v[6:9], v[178:181], v[218:221], v[6:9]
	v_mfma_f32_16x16x32_bf16 v[2:5], v[186:189], v[218:221], v[2:5]
	s_setprio 0
	s_barrier
	s_add_i32 s67, 0, 0x18000
	s_add_i32 s68, 0, 0x1c000
	v_add_u32_e32 v170, s67, v155
	v_add_u32_e32 v186, s68, v155
	ds_read_b128 v[148:151], v170
	ds_read_b128 v[162:165], v170 offset:1024
	ds_read_b128 v[166:169], v170 offset:2048
	ds_read_b128 v[170:173], v170 offset:3072
	ds_read_b128 v[174:177], v186
	ds_read_b128 v[178:181], v186 offset:1024
	ds_read_b128 v[182:185], v186 offset:2048
	ds_read_b128 v[186:189], v186 offset:3072
	s_add_u32 s38, s38, 0x80000
	s_addc_u32 s39, s39, 0
	s_mov_b32 m0, s44
	v_lshl_add_u64 v[228:229], s[38:39], 0, v[130:131]
	ds_read_b128 v[190:193], v160 offset:32768
	ds_read_b128 v[194:197], v160 offset:33792
	ds_read_b128 v[198:201], v160 offset:34816
	ds_read_b128 v[202:205], v160 offset:35840
	ds_read_b128 v[206:209], v160 offset:36864
	ds_read_b128 v[210:213], v160 offset:37888
	ds_read_b128 v[214:217], v160 offset:38912
	ds_read_b128 v[218:221], v160 offset:39936
	global_load_lds_dwordx4 v[228:229], off
	v_lshl_add_u64 v[228:229], s[38:39], 0, v[134:135]
	s_mov_b32 m0, s45
	s_nop 0
	global_load_lds_dwordx4 v[228:229], off
	s_waitcnt vmcnt(8)
	s_waitcnt lgkmcnt(0)
	s_barrier
	s_setprio 1
	s_waitcnt lgkmcnt(0)
	v_mfma_f32_16x16x32_bf16 v[126:129], v[148:151], v[190:193], v[126:129]
	v_mfma_f32_16x16x32_bf16 v[122:125], v[166:169], v[190:193], v[122:125]
	v_mfma_f32_16x16x32_bf16 v[110:113], v[148:151], v[198:201], v[110:113]
	v_mfma_f32_16x16x32_bf16 v[106:109], v[166:169], v[198:201], v[106:109]
	v_mfma_f32_16x16x32_bf16 v[94:97], v[148:151], v[206:209], v[94:97]
	v_mfma_f32_16x16x32_bf16 v[90:93], v[166:169], v[206:209], v[90:93]
	v_mfma_f32_16x16x32_bf16 v[78:81], v[148:151], v[214:217], v[78:81]
	v_mfma_f32_16x16x32_bf16 v[74:77], v[166:169], v[214:217], v[74:77]
	v_mfma_f32_16x16x32_bf16 v[126:129], v[162:165], v[194:197], v[126:129]
	v_mfma_f32_16x16x32_bf16 v[122:125], v[170:173], v[194:197], v[122:125]
	v_mfma_f32_16x16x32_bf16 v[110:113], v[162:165], v[202:205], v[110:113]
	v_mfma_f32_16x16x32_bf16 v[106:109], v[170:173], v[202:205], v[106:109]
	v_mfma_f32_16x16x32_bf16 v[94:97], v[162:165], v[210:213], v[94:97]
	v_mfma_f32_16x16x32_bf16 v[90:93], v[170:173], v[210:213], v[90:93]
	v_mfma_f32_16x16x32_bf16 v[78:81], v[162:165], v[218:221], v[78:81]
	v_mfma_f32_16x16x32_bf16 v[74:77], v[170:173], v[218:221], v[74:77]
	s_setprio 0
	s_setprio 1
	v_mfma_f32_16x16x32_bf16 v[118:121], v[174:177], v[190:193], v[118:121]
	v_mfma_f32_16x16x32_bf16 v[114:117], v[182:185], v[190:193], v[114:117]
	v_mfma_f32_16x16x32_bf16 v[102:105], v[174:177], v[198:201], v[102:105]
	v_mfma_f32_16x16x32_bf16 v[98:101], v[182:185], v[198:201], v[98:101]
	v_mfma_f32_16x16x32_bf16 v[86:89], v[174:177], v[206:209], v[86:89]
	v_mfma_f32_16x16x32_bf16 v[82:85], v[182:185], v[206:209], v[82:85]
	v_mfma_f32_16x16x32_bf16 v[70:73], v[174:177], v[214:217], v[70:73]
	v_mfma_f32_16x16x32_bf16 v[66:69], v[182:185], v[214:217], v[66:69]
	v_mfma_f32_16x16x32_bf16 v[118:121], v[178:181], v[194:197], v[118:121]
	v_mfma_f32_16x16x32_bf16 v[114:117], v[186:189], v[194:197], v[114:117]
	v_mfma_f32_16x16x32_bf16 v[102:105], v[178:181], v[202:205], v[102:105]
	v_mfma_f32_16x16x32_bf16 v[98:101], v[186:189], v[202:205], v[98:101]
	v_mfma_f32_16x16x32_bf16 v[86:89], v[178:181], v[210:213], v[86:89]
	v_mfma_f32_16x16x32_bf16 v[82:85], v[186:189], v[210:213], v[82:85]
	v_mfma_f32_16x16x32_bf16 v[70:73], v[178:181], v[218:221], v[70:73]
	v_mfma_f32_16x16x32_bf16 v[66:69], v[186:189], v[218:221], v[66:69]
	s_setprio 0
	s_barrier
	s_add_i32 s38, s67, s41
	v_lshl_add_u64 v[152:153], v[152:153], 0, s[14:15]
	s_mov_b32 m0, s38
	ds_read_b128 v[190:193], v160 offset:49152
	ds_read_b128 v[194:197], v160 offset:50176
	ds_read_b128 v[198:201], v160 offset:51200
	ds_read_b128 v[202:205], v160 offset:52224
	ds_read_b128 v[206:209], v160 offset:53248
	ds_read_b128 v[210:213], v160 offset:54272
	ds_read_b128 v[214:217], v160 offset:55296
	ds_read_b128 v[218:221], v160 offset:56320
	global_load_lds_dwordx4 v[152:153], off
	s_add_i32 m0, s38, 0x2000
	s_add_u32 s36, s36, 0x80080
	v_lshl_add_u64 v[152:153], v[222:223], 0, s[14:15]
	s_addc_u32 s37, s37, 0
	s_add_i32 s38, s68, s41
	global_load_lds_dwordx4 v[152:153], off
	v_lshl_add_u64 v[152:153], s[36:37], 0, v[132:133]
	s_mov_b32 m0, s38
	s_nop 0
	global_load_lds_dwordx4 v[152:153], off
	v_lshl_add_u64 v[152:153], s[36:37], 0, v[136:137]
	s_add_i32 m0, s38, 0x2000
	s_nop 0
	global_load_lds_dwordx4 v[152:153], off
	v_lshl_add_u64 v[152:153], v[224:225], 0, s[14:15]
	s_mov_b32 m0, s49
	s_nop 0
	global_load_lds_dwordx4 v[152:153], off
	v_lshl_add_u64 v[152:153], v[226:227], 0, s[14:15]
	s_mov_b32 m0, s54
	s_nop 0
	global_load_lds_dwordx4 v[152:153], off
	s_waitcnt vmcnt(8)
	s_waitcnt lgkmcnt(0)
	s_barrier
	s_setprio 1
	s_waitcnt lgkmcnt(0)
	v_mfma_f32_16x16x32_bf16 v[62:65], v[148:151], v[190:193], v[62:65]
	v_mfma_f32_16x16x32_bf16 v[58:61], v[166:169], v[190:193], v[58:61]
	v_mfma_f32_16x16x32_bf16 v[46:49], v[148:151], v[198:201], v[46:49]
	v_mfma_f32_16x16x32_bf16 v[42:45], v[166:169], v[198:201], v[42:45]
	v_mfma_f32_16x16x32_bf16 v[30:33], v[148:151], v[206:209], v[30:33]
	v_mfma_f32_16x16x32_bf16 v[26:29], v[166:169], v[206:209], v[26:29]
	v_mfma_f32_16x16x32_bf16 v[14:17], v[148:151], v[214:217], v[14:17]
	v_mfma_f32_16x16x32_bf16 v[10:13], v[166:169], v[214:217], v[10:13]
	v_mfma_f32_16x16x32_bf16 v[62:65], v[162:165], v[194:197], v[62:65]
	v_mfma_f32_16x16x32_bf16 v[58:61], v[170:173], v[194:197], v[58:61]
	v_mfma_f32_16x16x32_bf16 v[46:49], v[162:165], v[202:205], v[46:49]
	v_mfma_f32_16x16x32_bf16 v[42:45], v[170:173], v[202:205], v[42:45]
	v_mfma_f32_16x16x32_bf16 v[30:33], v[162:165], v[210:213], v[30:33]
	v_mfma_f32_16x16x32_bf16 v[26:29], v[170:173], v[210:213], v[26:29]
	v_mfma_f32_16x16x32_bf16 v[14:17], v[162:165], v[218:221], v[14:17]
	v_mfma_f32_16x16x32_bf16 v[10:13], v[170:173], v[218:221], v[10:13]
	s_setprio 0
	s_setprio 1
	v_mfma_f32_16x16x32_bf16 v[54:57], v[174:177], v[190:193], v[54:57]
	v_mfma_f32_16x16x32_bf16 v[50:53], v[182:185], v[190:193], v[50:53]
	v_mfma_f32_16x16x32_bf16 v[38:41], v[174:177], v[198:201], v[38:41]
	v_mfma_f32_16x16x32_bf16 v[34:37], v[182:185], v[198:201], v[34:37]
	v_mfma_f32_16x16x32_bf16 v[22:25], v[174:177], v[206:209], v[22:25]
	v_mfma_f32_16x16x32_bf16 v[18:21], v[182:185], v[206:209], v[18:21]
	v_mfma_f32_16x16x32_bf16 v[6:9], v[174:177], v[214:217], v[6:9]
	v_mfma_f32_16x16x32_bf16 v[2:5], v[182:185], v[214:217], v[2:5]
	v_mfma_f32_16x16x32_bf16 v[54:57], v[178:181], v[194:197], v[54:57]
	v_mfma_f32_16x16x32_bf16 v[50:53], v[186:189], v[194:197], v[50:53]
	v_mfma_f32_16x16x32_bf16 v[38:41], v[178:181], v[202:205], v[38:41]
	v_mfma_f32_16x16x32_bf16 v[34:37], v[186:189], v[202:205], v[34:37]
	v_mfma_f32_16x16x32_bf16 v[22:25], v[178:181], v[210:213], v[22:25]
	v_mfma_f32_16x16x32_bf16 v[18:21], v[186:189], v[210:213], v[18:21]
	v_mfma_f32_16x16x32_bf16 v[6:9], v[178:181], v[218:221], v[6:9]
	v_mfma_f32_16x16x32_bf16 v[2:5], v[186:189], v[218:221], v[2:5]
	s_setprio 0
	s_barrier
	s_add_i32 s66, s66, 2
	s_add_u32 s34, s34, 0x100
	s_addc_u32 s35, s35, 0
	s_add_u32 s64, s64, 0x100
	s_addc_u32 s65, s65, 0
	s_cmp_gt_u32 s66, 29
	s_cbranch_scc0 .LBB0_651
	v_lshl_add_u32 v152, s0, 8, v154
	v_ashrrev_i32_e32 v153, 31, v152
	v_lshl_add_u64 v[148:149], v[152:153], 3, s[12:13]
	global_load_dwordx2 v[150:151], v[148:149], off
	global_load_dwordx2 v[178:179], v[148:149], off offset:128
	global_load_dwordx2 v[180:181], v[148:149], off offset:256
	global_load_dwordx2 v[182:183], v[148:149], off offset:384
	global_load_dwordx2 v[184:185], v[148:149], off offset:1024
	global_load_dwordx2 v[186:187], v[148:149], off offset:1152
	global_load_dwordx2 v[188:189], v[148:149], off offset:1280
	global_load_dwordx2 v[190:191], v[148:149], off offset:1408
	s_and_b64 vcc, exec, s[16:17]
	s_cbranch_vccz .LBB0_654
	s_barrier
.LBB0_654:
	v_lshlrev_b64 v[166:167], 14, v[152:153]
	v_lshl_or_b32 v162, s1, 8, v156
	v_ashrrev_i32_e32 v163, 31, v162
	v_or_b32_e32 v164, 16, v152
	v_lshlrev_b64 v[162:163], 1, v[162:163]
	v_ashrrev_i32_e32 v165, 31, v164
	s_mov_b64 s[0:1], 0x200000
	s_waitcnt vmcnt(7)
	v_ffbh_u32_e32 v153, v151
	v_min_u32_e32 v153, 32, v153
	v_lshlrev_b64 v[150:151], v153, v[150:151]
	v_min_u32_e32 v150, 1, v150
	v_or_b32_e32 v150, v151, v150
	v_cvt_f32_u32_e32 v150, v150
	v_sub_u32_e32 v151, 32, v153
	v_ldexp_f32 v150, v150, v151
	v_fmamk_f32 v150, v150, 0x30000000, v161
	v_rsq_f32_e32 v168, v150
	v_lshl_add_u64 v[150:151], s[10:11], 0, v[166:167]
	v_lshl_add_u64 v[150:151], v[150:151], 0, v[162:163]
	v_lshl_add_u64 v[166:167], v[164:165], 3, s[12:13]
	v_pk_mul_f32 v[128:129], v[128:129], v[168:169] op_sel_hi:[1,0]
	v_pk_mul_f32 v[126:127], v[126:127], v[168:169] op_sel_hi:[1,0]
	v_pk_mul_f32 v[124:125], v[124:125], v[168:169] op_sel_hi:[1,0]
	v_pk_mul_f32 v[122:123], v[122:123], v[168:169] op_sel_hi:[1,0]
	v_pk_mul_f32 v[120:121], v[120:121], v[168:169] op_sel_hi:[1,0]
	v_pk_mul_f32 v[118:119], v[118:119], v[168:169] op_sel_hi:[1,0]
	v_pk_mul_f32 v[170:171], v[116:117], v[168:169] op_sel_hi:[1,0]
	v_pk_mul_f32 v[168:169], v[114:115], v[168:169] op_sel_hi:[1,0]
	v_cvt_pk_bf16_f32 v114, v126, v127
	v_cvt_pk_bf16_f32 v115, v128, v129
	v_cvt_pk_bf16_f32 v116, v122, v123
	v_cvt_pk_bf16_f32 v117, v124, v125
	global_store_dwordx4 v[150:151], v[114:117], off
	s_nop 1
	v_cvt_pk_bf16_f32 v114, v118, v119
	v_cvt_pk_bf16_f32 v115, v120, v121
	v_cvt_pk_bf16_f32 v116, v168, v169
	v_cvt_pk_bf16_f32 v117, v170, v171
	global_store_dwordx4 v[150:151], v[114:117], off offset:256
	s_nop 0
	s_nop 0
	v_or_b32_e32 v116, 32, v152
	s_waitcnt vmcnt(8)
	v_mov_b32_e32 v114, v178
	v_mov_b32_e32 v115, v179
	v_ffbh_u32_e32 v117, v115
	v_min_u32_e32 v118, 32, v117
	v_lshlrev_b64 v[114:115], v118, v[114:115]
	v_min_u32_e32 v114, 1, v114
	v_or_b32_e32 v114, v115, v114
	v_cvt_f32_u32_e32 v119, v114
	v_sub_u32_e32 v118, 32, v118
	v_lshlrev_b64 v[114:115], 14, v[164:165]
	v_lshl_add_u64 v[114:115], s[10:11], 0, v[114:115]
	v_ldexp_f32 v118, v119, v118
	v_fmamk_f32 v118, v118, 0x30000000, v161
	v_rsq_f32_e32 v118, v118
	v_ashrrev_i32_e32 v117, 31, v116
	v_lshl_add_u64 v[114:115], v[114:115], 0, v[162:163]
	v_lshl_add_u64 v[120:121], v[116:117], 3, s[12:13]
	v_pk_mul_f32 v[112:113], v[112:113], v[118:119] op_sel_hi:[1,0]
	v_pk_mul_f32 v[110:111], v[110:111], v[118:119] op_sel_hi:[1,0]
	v_pk_mul_f32 v[108:109], v[108:109], v[118:119] op_sel_hi:[1,0]
	v_pk_mul_f32 v[106:107], v[106:107], v[118:119] op_sel_hi:[1,0]
	v_pk_mul_f32 v[104:105], v[104:105], v[118:119] op_sel_hi:[1,0]
	v_pk_mul_f32 v[102:103], v[102:103], v[118:119] op_sel_hi:[1,0]
	v_pk_mul_f32 v[122:123], v[100:101], v[118:119] op_sel_hi:[1,0]
	v_pk_mul_f32 v[118:119], v[98:99], v[118:119] op_sel_hi:[1,0]
	v_cvt_pk_bf16_f32 v98, v110, v111
	v_cvt_pk_bf16_f32 v99, v112, v113
	v_cvt_pk_bf16_f32 v100, v106, v107
	v_cvt_pk_bf16_f32 v101, v108, v109
	global_store_dwordx4 v[114:115], v[98:101], off
	s_nop 1
	v_cvt_pk_bf16_f32 v98, v102, v103
	v_cvt_pk_bf16_f32 v99, v104, v105
	v_cvt_pk_bf16_f32 v100, v118, v119
	v_cvt_pk_bf16_f32 v101, v122, v123
	global_store_dwordx4 v[114:115], v[98:101], off offset:256
	s_nop 0
	s_nop 0
	v_or_b32_e32 v100, 48, v152
	s_waitcnt vmcnt(9)
	v_mov_b32_e32 v98, v180
	v_mov_b32_e32 v99, v181
	v_ffbh_u32_e32 v101, v99
	v_min_u32_e32 v102, 32, v101
	v_lshlrev_b64 v[98:99], v102, v[98:99]
	v_min_u32_e32 v98, 1, v98
	v_or_b32_e32 v98, v99, v98
	v_cvt_f32_u32_e32 v103, v98
	v_sub_u32_e32 v102, 32, v102
	v_lshlrev_b64 v[98:99], 14, v[116:117]
	v_lshl_add_u64 v[98:99], s[10:11], 0, v[98:99]
	v_ldexp_f32 v102, v103, v102
	v_fmamk_f32 v102, v102, 0x30000000, v161
	v_rsq_f32_e32 v102, v102
	v_ashrrev_i32_e32 v101, 31, v100
	v_lshl_add_u64 v[98:99], v[98:99], 0, v[162:163]
	v_lshl_add_u64 v[104:105], v[100:101], 3, s[12:13]
	v_pk_mul_f32 v[96:97], v[96:97], v[102:103] op_sel_hi:[1,0]
	v_pk_mul_f32 v[94:95], v[94:95], v[102:103] op_sel_hi:[1,0]
	v_pk_mul_f32 v[92:93], v[92:93], v[102:103] op_sel_hi:[1,0]
	v_pk_mul_f32 v[90:91], v[90:91], v[102:103] op_sel_hi:[1,0]
	v_pk_mul_f32 v[88:89], v[88:89], v[102:103] op_sel_hi:[1,0]
	v_pk_mul_f32 v[86:87], v[86:87], v[102:103] op_sel_hi:[1,0]
	v_pk_mul_f32 v[106:107], v[84:85], v[102:103] op_sel_hi:[1,0]
	v_pk_mul_f32 v[102:103], v[82:83], v[102:103] op_sel_hi:[1,0]
	v_cvt_pk_bf16_f32 v82, v94, v95
	v_cvt_pk_bf16_f32 v83, v96, v97
	v_cvt_pk_bf16_f32 v84, v90, v91
	v_cvt_pk_bf16_f32 v85, v92, v93
	global_store_dwordx4 v[98:99], v[82:85], off
	s_nop 1
	v_cvt_pk_bf16_f32 v82, v86, v87
	v_cvt_pk_bf16_f32 v83, v88, v89
	v_cvt_pk_bf16_f32 v84, v102, v103
	v_cvt_pk_bf16_f32 v85, v106, v107
	global_store_dwordx4 v[98:99], v[82:85], off offset:256
	s_nop 0
	s_waitcnt vmcnt(10)
	v_mov_b32_e32 v82, v182
	v_mov_b32_e32 v83, v183
	v_ffbh_u32_e32 v84, v83
	v_min_u32_e32 v84, 32, v84
	v_lshlrev_b64 v[82:83], v84, v[82:83]
	v_min_u32_e32 v82, 1, v82
	v_or_b32_e32 v82, v83, v82
	v_cvt_f32_u32_e32 v82, v82
	v_sub_u32_e32 v83, 32, v84
	v_lshlrev_b64 v[84:85], 14, v[100:101]
	v_lshl_add_u64 v[84:85], s[10:11], 0, v[84:85]
	v_ldexp_f32 v82, v82, v83
	v_fmamk_f32 v82, v82, 0x30000000, v161
	v_rsq_f32_e32 v82, v82
	v_lshl_add_u64 v[84:85], v[84:85], 0, v[162:163]
	v_pk_mul_f32 v[80:81], v[80:81], v[82:83] op_sel_hi:[1,0]
	v_pk_mul_f32 v[78:79], v[78:79], v[82:83] op_sel_hi:[1,0]
	v_pk_mul_f32 v[76:77], v[76:77], v[82:83] op_sel_hi:[1,0]
	v_pk_mul_f32 v[74:75], v[74:75], v[82:83] op_sel_hi:[1,0]
	v_pk_mul_f32 v[72:73], v[72:73], v[82:83] op_sel_hi:[1,0]
	v_pk_mul_f32 v[70:71], v[70:71], v[82:83] op_sel_hi:[1,0]
	v_pk_mul_f32 v[86:87], v[68:69], v[82:83] op_sel_hi:[1,0]
	v_pk_mul_f32 v[82:83], v[66:67], v[82:83] op_sel_hi:[1,0]
	v_cvt_pk_bf16_f32 v66, v78, v79
	v_cvt_pk_bf16_f32 v67, v80, v81
	v_cvt_pk_bf16_f32 v68, v74, v75
	v_cvt_pk_bf16_f32 v69, v76, v77
	global_store_dwordx4 v[84:85], v[66:69], off
	s_nop 1
	v_cvt_pk_bf16_f32 v66, v70, v71
	v_cvt_pk_bf16_f32 v67, v72, v73
	v_cvt_pk_bf16_f32 v68, v82, v83
	v_cvt_pk_bf16_f32 v69, v86, v87
	global_store_dwordx4 v[84:85], v[66:69], off offset:256
	s_nop 0
	v_add_co_u32_e32 v70, vcc, s58, v150
	s_waitcnt vmcnt(11)
	v_mov_b32_e32 v66, v184
	v_mov_b32_e32 v67, v185
	v_ffbh_u32_e32 v68, v67
	v_min_u32_e32 v68, 32, v68
	v_lshlrev_b64 v[66:67], v68, v[66:67]
	v_min_u32_e32 v66, 1, v66
	v_or_b32_e32 v66, v67, v66
	v_cvt_f32_u32_e32 v69, v66
	v_sub_u32_e32 v68, 32, v68
	v_lshl_add_u64 v[66:67], v[150:151], 0, s[0:1]
	v_addc_co_u32_e32 v71, vcc, 0, v151, vcc
	v_ldexp_f32 v68, v69, v68
	v_fmamk_f32 v68, v68, 0x30000000, v161
	v_rsq_f32_e32 v68, v68
	s_nop 0
	v_pk_mul_f32 v[64:65], v[64:65], v[68:69] op_sel_hi:[1,0]
	v_pk_mul_f32 v[62:63], v[62:63], v[68:69] op_sel_hi:[1,0]
	v_pk_mul_f32 v[60:61], v[60:61], v[68:69] op_sel_hi:[1,0]
	v_pk_mul_f32 v[58:59], v[58:59], v[68:69] op_sel_hi:[1,0]
	v_pk_mul_f32 v[56:57], v[56:57], v[68:69] op_sel_hi:[1,0]
	v_pk_mul_f32 v[54:55], v[54:55], v[68:69] op_sel_hi:[1,0]
	v_pk_mul_f32 v[72:73], v[52:53], v[68:69] op_sel_hi:[1,0]
	v_pk_mul_f32 v[68:69], v[50:51], v[68:69] op_sel_hi:[1,0]
	v_cvt_pk_bf16_f32 v50, v62, v63
	v_cvt_pk_bf16_f32 v51, v64, v65
	v_cvt_pk_bf16_f32 v52, v58, v59
	v_cvt_pk_bf16_f32 v53, v60, v61
	global_store_dwordx4 v[70:71], v[50:53], off
	s_nop 1
	v_cvt_pk_bf16_f32 v50, v54, v55
	v_cvt_pk_bf16_f32 v51, v56, v57
	v_cvt_pk_bf16_f32 v52, v68, v69
	v_cvt_pk_bf16_f32 v53, v72, v73
	global_store_dwordx4 v[66:67], v[50:53], off offset:256
	s_nop 0
	v_add_co_u32_e32 v54, vcc, s59, v150
	s_waitcnt vmcnt(12)
	v_mov_b32_e32 v50, v186
	v_mov_b32_e32 v51, v187
	v_ffbh_u32_e32 v52, v51
	v_min_u32_e32 v52, 32, v52
	v_lshlrev_b64 v[50:51], v52, v[50:51]
	v_min_u32_e32 v50, 1, v50
	v_or_b32_e32 v50, v51, v50
	v_cvt_f32_u32_e32 v53, v50
	v_sub_u32_e32 v52, 32, v52
	v_lshl_add_u64 v[50:51], v[150:151], 0, s[18:19]
	v_addc_co_u32_e32 v55, vcc, 0, v151, vcc
	v_ldexp_f32 v52, v53, v52
	v_fmamk_f32 v52, v52, 0x30000000, v161
	v_rsq_f32_e32 v52, v52
	s_nop 0
	v_pk_mul_f32 v[48:49], v[48:49], v[52:53] op_sel_hi:[1,0]
	v_pk_mul_f32 v[46:47], v[46:47], v[52:53] op_sel_hi:[1,0]
	v_pk_mul_f32 v[44:45], v[44:45], v[52:53] op_sel_hi:[1,0]
	v_pk_mul_f32 v[42:43], v[42:43], v[52:53] op_sel_hi:[1,0]
	v_pk_mul_f32 v[40:41], v[40:41], v[52:53] op_sel_hi:[1,0]
	v_pk_mul_f32 v[38:39], v[38:39], v[52:53] op_sel_hi:[1,0]
	v_pk_mul_f32 v[56:57], v[36:37], v[52:53] op_sel_hi:[1,0]
	v_pk_mul_f32 v[52:53], v[34:35], v[52:53] op_sel_hi:[1,0]
	v_cvt_pk_bf16_f32 v34, v46, v47
	v_cvt_pk_bf16_f32 v35, v48, v49
	v_cvt_pk_bf16_f32 v36, v42, v43
	v_cvt_pk_bf16_f32 v37, v44, v45
	global_store_dwordx4 v[54:55], v[34:37], off
	s_nop 1
	v_cvt_pk_bf16_f32 v34, v38, v39
	v_cvt_pk_bf16_f32 v35, v40, v41
	v_cvt_pk_bf16_f32 v36, v52, v53
	v_cvt_pk_bf16_f32 v37, v56, v57
	global_store_dwordx4 v[50:51], v[34:37], off offset:256
	s_nop 0
	v_add_co_u32_e32 v38, vcc, s60, v150
	s_waitcnt vmcnt(13)
	v_mov_b32_e32 v34, v188
	v_mov_b32_e32 v35, v189
	v_ffbh_u32_e32 v36, v35
	v_min_u32_e32 v36, 32, v36
	v_lshlrev_b64 v[34:35], v36, v[34:35]
	v_min_u32_e32 v34, 1, v34
	v_or_b32_e32 v34, v35, v34
	v_cvt_f32_u32_e32 v37, v34
	v_sub_u32_e32 v36, 32, v36
	v_lshl_add_u64 v[34:35], v[150:151], 0, s[20:21]
	v_addc_co_u32_e32 v39, vcc, 0, v151, vcc
	v_ldexp_f32 v36, v37, v36
	v_fmamk_f32 v36, v36, 0x30000000, v161
	v_rsq_f32_e32 v36, v36
	s_andn2_b64 vcc, exec, s[4:5]
	v_pk_mul_f32 v[32:33], v[32:33], v[36:37] op_sel_hi:[1,0]
	v_pk_mul_f32 v[30:31], v[30:31], v[36:37] op_sel_hi:[1,0]
	v_pk_mul_f32 v[28:29], v[28:29], v[36:37] op_sel_hi:[1,0]
	v_pk_mul_f32 v[26:27], v[26:27], v[36:37] op_sel_hi:[1,0]
	v_pk_mul_f32 v[24:25], v[24:25], v[36:37] op_sel_hi:[1,0]
	v_pk_mul_f32 v[22:23], v[22:23], v[36:37] op_sel_hi:[1,0]
	v_pk_mul_f32 v[40:41], v[20:21], v[36:37] op_sel_hi:[1,0]
	v_pk_mul_f32 v[36:37], v[18:19], v[36:37] op_sel_hi:[1,0]
	v_cvt_pk_bf16_f32 v18, v30, v31
	v_cvt_pk_bf16_f32 v19, v32, v33
	v_cvt_pk_bf16_f32 v20, v26, v27
	v_cvt_pk_bf16_f32 v21, v28, v29
	global_store_dwordx4 v[38:39], v[18:21], off
	s_nop 1
	v_cvt_pk_bf16_f32 v18, v22, v23
	v_cvt_pk_bf16_f32 v19, v24, v25
	v_cvt_pk_bf16_f32 v20, v36, v37
	v_cvt_pk_bf16_f32 v21, v40, v41
	global_store_dwordx4 v[34:35], v[18:21], off offset:256
	s_nop 0
	v_add_co_u32_e64 v22, s[0:1], s61, v150
	s_waitcnt vmcnt(14)
	v_mov_b32_e32 v18, v190
	v_mov_b32_e32 v19, v191
	v_ffbh_u32_e32 v20, v19
	v_min_u32_e32 v20, 32, v20
	v_lshlrev_b64 v[18:19], v20, v[18:19]
	v_min_u32_e32 v18, 1, v18
	v_or_b32_e32 v18, v19, v18
	v_cvt_f32_u32_e32 v21, v18
	v_sub_u32_e32 v20, 32, v20
	v_addc_co_u32_e64 v23, s[0:1], 0, v151, s[0:1]
	v_ldexp_f32 v20, v21, v20
	v_fmamk_f32 v20, v20, 0x30000000, v161
	v_rsq_f32_e32 v20, v20
	v_lshl_add_u64 v[18:19], v[150:151], 0, s[22:23]
	s_mov_b64 s[0:1], -1
	v_pk_mul_f32 v[16:17], v[16:17], v[20:21] op_sel_hi:[1,0]
	v_pk_mul_f32 v[14:15], v[14:15], v[20:21] op_sel_hi:[1,0]
	v_pk_mul_f32 v[12:13], v[12:13], v[20:21] op_sel_hi:[1,0]
	v_pk_mul_f32 v[10:11], v[10:11], v[20:21] op_sel_hi:[1,0]
	v_pk_mul_f32 v[8:9], v[8:9], v[20:21] op_sel_hi:[1,0]
	v_pk_mul_f32 v[6:7], v[6:7], v[20:21] op_sel_hi:[1,0]
	v_pk_mul_f32 v[24:25], v[4:5], v[20:21] op_sel_hi:[1,0]
	v_pk_mul_f32 v[20:21], v[2:3], v[20:21] op_sel_hi:[1,0]
	v_cvt_pk_bf16_f32 v2, v14, v15
	v_cvt_pk_bf16_f32 v3, v16, v17
	v_cvt_pk_bf16_f32 v4, v10, v11
	v_cvt_pk_bf16_f32 v5, v12, v13
	global_store_dwordx4 v[22:23], v[2:5], off
	s_nop 1
	v_cvt_pk_bf16_f32 v2, v6, v7
	v_cvt_pk_bf16_f32 v3, v8, v9
	v_cvt_pk_bf16_f32 v4, v20, v21
	v_cvt_pk_bf16_f32 v5, v24, v25
	global_store_dwordx4 v[18:19], v[2:5], off offset:256
	s_cbranch_vccnz .LBB0_643
	s_andn2_b64 vcc, exec, s[8:9]
	s_cbranch_vccnz .LBB0_642
	s_barrier
	s_branch .LBB0_642

.LBB0_848:
	ds_read_b128 v[148:151], v157
	ds_read_b128 v[162:165], v157 offset:1024
	ds_read_b128 v[166:169], v157 offset:2048
	ds_read_b128 v[170:173], v157 offset:3072
	ds_read_b128 v[174:177], v159
	ds_read_b128 v[178:181], v159 offset:1024
	ds_read_b128 v[182:185], v159 offset:2048
	ds_read_b128 v[186:189], v159 offset:3072
	s_add_u32 s36, s34, 0xfff80080
	s_addc_u32 s37, s35, -1
	s_cmp_eq_u32 s62, 28
	s_cselect_b32 s39, s23, s37
	s_cselect_b32 s38, s58, s36
	s_cselect_b32 s37, s21, s61
	s_cselect_b32 s36, s59, s60
	v_lshl_add_u64 v[152:153], s[34:35], 0, v[138:139]
	s_add_i32 m0, s31, 0xc000
	ds_read_b128 v[190:193], v160
	ds_read_b128 v[194:197], v160 offset:1024
	ds_read_b128 v[198:201], v160 offset:2048
	ds_read_b128 v[202:205], v160 offset:3072
	ds_read_b128 v[206:209], v160 offset:4096
	ds_read_b128 v[210:213], v160 offset:5120
	ds_read_b128 v[214:217], v160 offset:6144
	ds_read_b128 v[218:221], v160 offset:7168
	global_load_lds_dwordx4 v[152:153], off
	v_lshl_add_u64 v[152:153], s[34:35], 0, v[140:141]
	s_add_i32 m0, s31, 0xe000
	s_nop 0
	global_load_lds_dwordx4 v[152:153], off
	s_waitcnt vmcnt(8)
	s_waitcnt lgkmcnt(0)
	s_barrier
	s_setprio 1
	s_waitcnt lgkmcnt(0)
	v_mfma_f32_16x16x32_bf16 v[126:129], v[148:151], v[190:193], v[126:129]
	v_mfma_f32_16x16x32_bf16 v[122:125], v[166:169], v[190:193], v[122:125]
	v_mfma_f32_16x16x32_bf16 v[110:113], v[148:151], v[198:201], v[110:113]
	v_mfma_f32_16x16x32_bf16 v[106:109], v[166:169], v[198:201], v[106:109]
	v_mfma_f32_16x16x32_bf16 v[94:97], v[148:151], v[206:209], v[94:97]
	v_mfma_f32_16x16x32_bf16 v[90:93], v[166:169], v[206:209], v[90:93]
	v_mfma_f32_16x16x32_bf16 v[78:81], v[148:151], v[214:217], v[78:81]
	v_mfma_f32_16x16x32_bf16 v[74:77], v[166:169], v[214:217], v[74:77]
	v_mfma_f32_16x16x32_bf16 v[126:129], v[162:165], v[194:197], v[126:129]
	v_mfma_f32_16x16x32_bf16 v[122:125], v[170:173], v[194:197], v[122:125]
	v_mfma_f32_16x16x32_bf16 v[110:113], v[162:165], v[202:205], v[110:113]
	v_mfma_f32_16x16x32_bf16 v[106:109], v[170:173], v[202:205], v[106:109]
	v_mfma_f32_16x16x32_bf16 v[94:97], v[162:165], v[210:213], v[94:97]
	v_mfma_f32_16x16x32_bf16 v[90:93], v[170:173], v[210:213], v[90:93]
	v_mfma_f32_16x16x32_bf16 v[78:81], v[162:165], v[218:221], v[78:81]
	v_mfma_f32_16x16x32_bf16 v[74:77], v[170:173], v[218:221], v[74:77]
	s_setprio 0
	s_setprio 1
	v_mfma_f32_16x16x32_bf16 v[118:121], v[174:177], v[190:193], v[118:121]
	v_mfma_f32_16x16x32_bf16 v[114:117], v[182:185], v[190:193], v[114:117]
	v_mfma_f32_16x16x32_bf16 v[102:105], v[174:177], v[198:201], v[102:105]
	v_mfma_f32_16x16x32_bf16 v[98:101], v[182:185], v[198:201], v[98:101]
	v_mfma_f32_16x16x32_bf16 v[86:89], v[174:177], v[206:209], v[86:89]
	v_mfma_f32_16x16x32_bf16 v[82:85], v[182:185], v[206:209], v[82:85]
	v_mfma_f32_16x16x32_bf16 v[70:73], v[174:177], v[214:217], v[70:73]
	v_mfma_f32_16x16x32_bf16 v[66:69], v[182:185], v[214:217], v[66:69]
	v_mfma_f32_16x16x32_bf16 v[118:121], v[178:181], v[194:197], v[118:121]
	v_mfma_f32_16x16x32_bf16 v[114:117], v[186:189], v[194:197], v[114:117]
	v_mfma_f32_16x16x32_bf16 v[102:105], v[178:181], v[202:205], v[102:105]
	v_mfma_f32_16x16x32_bf16 v[98:101], v[186:189], v[202:205], v[98:101]
	v_mfma_f32_16x16x32_bf16 v[86:89], v[178:181], v[210:213], v[86:89]
	v_mfma_f32_16x16x32_bf16 v[82:85], v[186:189], v[210:213], v[82:85]
	v_mfma_f32_16x16x32_bf16 v[70:73], v[178:181], v[218:221], v[70:73]
	v_mfma_f32_16x16x32_bf16 v[66:69], v[186:189], v[218:221], v[66:69]
	s_setprio 0
	s_barrier
	s_add_i32 s63, s55, s41
	v_lshl_add_u64 v[152:153], s[36:37], 0, v[132:133]
	s_mov_b32 m0, s63
	ds_read_b128 v[190:193], v160 offset:16384
	ds_read_b128 v[194:197], v160 offset:17408
	ds_read_b128 v[198:201], v160 offset:18432
	ds_read_b128 v[202:205], v160 offset:19456
	ds_read_b128 v[206:209], v160 offset:20480
	ds_read_b128 v[210:213], v160 offset:21504
	ds_read_b128 v[214:217], v160 offset:22528
	ds_read_b128 v[218:221], v160 offset:23552
	global_load_lds_dwordx4 v[152:153], off
	s_add_i32 m0, s63, 0x2000
	s_add_u32 s64, s36, 0x80000
	v_lshl_add_u64 v[222:223], s[36:37], 0, v[136:137]
	s_addc_u32 s65, s37, 0
	s_add_i32 s63, s56, s41
	global_load_lds_dwordx4 v[222:223], off
	v_lshl_add_u64 v[224:225], s[64:65], 0, v[132:133]
	s_mov_b32 m0, s63
	v_lshl_add_u64 v[226:227], s[38:39], 0, v[134:135]
	global_load_lds_dwordx4 v[224:225], off
	v_lshl_add_u64 v[224:225], s[64:65], 0, v[136:137]
	s_add_i32 m0, s63, 0x2000
	s_nop 0
	global_load_lds_dwordx4 v[224:225], off
	v_lshl_add_u64 v[224:225], s[38:39], 0, v[130:131]
	s_mov_b32 m0, s31
	s_nop 0
	global_load_lds_dwordx4 v[224:225], off
	s_mov_b32 m0, s42
	s_nop 0
	global_load_lds_dwordx4 v[226:227], off
	s_waitcnt vmcnt(8)
	s_waitcnt lgkmcnt(0)
	s_barrier
	s_setprio 1
	s_waitcnt lgkmcnt(0)
	v_mfma_f32_16x16x32_bf16 v[62:65], v[148:151], v[190:193], v[62:65]
	v_mfma_f32_16x16x32_bf16 v[58:61], v[166:169], v[190:193], v[58:61]
	v_mfma_f32_16x16x32_bf16 v[46:49], v[148:151], v[198:201], v[46:49]
	v_mfma_f32_16x16x32_bf16 v[42:45], v[166:169], v[198:201], v[42:45]
	v_mfma_f32_16x16x32_bf16 v[30:33], v[148:151], v[206:209], v[30:33]
	v_mfma_f32_16x16x32_bf16 v[26:29], v[166:169], v[206:209], v[26:29]
	v_mfma_f32_16x16x32_bf16 v[14:17], v[148:151], v[214:217], v[14:17]
	v_mfma_f32_16x16x32_bf16 v[10:13], v[166:169], v[214:217], v[10:13]
	v_mfma_f32_16x16x32_bf16 v[62:65], v[162:165], v[194:197], v[62:65]
	v_mfma_f32_16x16x32_bf16 v[58:61], v[170:173], v[194:197], v[58:61]
	v_mfma_f32_16x16x32_bf16 v[46:49], v[162:165], v[202:205], v[46:49]
	v_mfma_f32_16x16x32_bf16 v[42:45], v[170:173], v[202:205], v[42:45]
	v_mfma_f32_16x16x32_bf16 v[30:33], v[162:165], v[210:213], v[30:33]
	v_mfma_f32_16x16x32_bf16 v[26:29], v[170:173], v[210:213], v[26:29]
	v_mfma_f32_16x16x32_bf16 v[14:17], v[162:165], v[218:221], v[14:17]
	v_mfma_f32_16x16x32_bf16 v[10:13], v[170:173], v[218:221], v[10:13]
	s_setprio 0
	s_setprio 1
	v_mfma_f32_16x16x32_bf16 v[54:57], v[174:177], v[190:193], v[54:57]
	v_mfma_f32_16x16x32_bf16 v[50:53], v[182:185], v[190:193], v[50:53]
	v_mfma_f32_16x16x32_bf16 v[38:41], v[174:177], v[198:201], v[38:41]
	v_mfma_f32_16x16x32_bf16 v[34:37], v[182:185], v[198:201], v[34:37]
	v_mfma_f32_16x16x32_bf16 v[22:25], v[174:177], v[206:209], v[22:25]
	v_mfma_f32_16x16x32_bf16 v[18:21], v[182:185], v[206:209], v[18:21]
	v_mfma_f32_16x16x32_bf16 v[6:9], v[174:177], v[214:217], v[6:9]
	v_mfma_f32_16x16x32_bf16 v[2:5], v[182:185], v[214:217], v[2:5]
	v_mfma_f32_16x16x32_bf16 v[54:57], v[178:181], v[194:197], v[54:57]
	v_mfma_f32_16x16x32_bf16 v[50:53], v[186:189], v[194:197], v[50:53]
	v_mfma_f32_16x16x32_bf16 v[38:41], v[178:181], v[202:205], v[38:41]
	v_mfma_f32_16x16x32_bf16 v[34:37], v[186:189], v[202:205], v[34:37]
	v_mfma_f32_16x16x32_bf16 v[22:25], v[178:181], v[210:213], v[22:25]
	v_mfma_f32_16x16x32_bf16 v[18:21], v[186:189], v[210:213], v[18:21]
	v_mfma_f32_16x16x32_bf16 v[6:9], v[178:181], v[218:221], v[6:9]
	v_mfma_f32_16x16x32_bf16 v[2:5], v[186:189], v[218:221], v[2:5]
	s_setprio 0
	s_barrier
	s_add_i32 s63, 0, 0x18000
	v_add_u32_e32 v161, s63, v155
	s_add_i32 s64, 0, 0x1c000
	ds_read_b128 v[148:151], v161
	ds_read_b128 v[162:165], v161 offset:1024
	ds_read_b128 v[166:169], v161 offset:2048
	ds_read_b128 v[170:173], v161 offset:3072
	v_add_u32_e32 v161, s64, v155
	ds_read_b128 v[174:177], v161
	ds_read_b128 v[178:181], v161 offset:1024
	ds_read_b128 v[182:185], v161 offset:2048
	ds_read_b128 v[186:189], v161 offset:3072
	s_add_u32 s38, s38, 0x80000
	s_addc_u32 s39, s39, 0
	s_mov_b32 m0, s43
	v_lshl_add_u64 v[228:229], s[38:39], 0, v[130:131]
	ds_read_b128 v[190:193], v160 offset:32768
	ds_read_b128 v[194:197], v160 offset:33792
	ds_read_b128 v[198:201], v160 offset:34816
	ds_read_b128 v[202:205], v160 offset:35840
	ds_read_b128 v[206:209], v160 offset:36864
	ds_read_b128 v[210:213], v160 offset:37888
	ds_read_b128 v[214:217], v160 offset:38912
	ds_read_b128 v[218:221], v160 offset:39936
	global_load_lds_dwordx4 v[228:229], off
	v_lshl_add_u64 v[228:229], s[38:39], 0, v[134:135]
	s_mov_b32 m0, s44
	s_nop 0
	global_load_lds_dwordx4 v[228:229], off
	s_waitcnt vmcnt(8)
	s_waitcnt lgkmcnt(0)
	s_barrier
	s_setprio 1
	s_waitcnt lgkmcnt(0)
	v_mfma_f32_16x16x32_bf16 v[126:129], v[148:151], v[190:193], v[126:129]
	v_mfma_f32_16x16x32_bf16 v[122:125], v[166:169], v[190:193], v[122:125]
	v_mfma_f32_16x16x32_bf16 v[110:113], v[148:151], v[198:201], v[110:113]
	v_mfma_f32_16x16x32_bf16 v[106:109], v[166:169], v[198:201], v[106:109]
	v_mfma_f32_16x16x32_bf16 v[94:97], v[148:151], v[206:209], v[94:97]
	v_mfma_f32_16x16x32_bf16 v[90:93], v[166:169], v[206:209], v[90:93]
	v_mfma_f32_16x16x32_bf16 v[78:81], v[148:151], v[214:217], v[78:81]
	v_mfma_f32_16x16x32_bf16 v[74:77], v[166:169], v[214:217], v[74:77]
	v_mfma_f32_16x16x32_bf16 v[126:129], v[162:165], v[194:197], v[126:129]
	v_mfma_f32_16x16x32_bf16 v[122:125], v[170:173], v[194:197], v[122:125]
	v_mfma_f32_16x16x32_bf16 v[110:113], v[162:165], v[202:205], v[110:113]
	v_mfma_f32_16x16x32_bf16 v[106:109], v[170:173], v[202:205], v[106:109]
	v_mfma_f32_16x16x32_bf16 v[94:97], v[162:165], v[210:213], v[94:97]
	v_mfma_f32_16x16x32_bf16 v[90:93], v[170:173], v[210:213], v[90:93]
	v_mfma_f32_16x16x32_bf16 v[78:81], v[162:165], v[218:221], v[78:81]
	v_mfma_f32_16x16x32_bf16 v[74:77], v[170:173], v[218:221], v[74:77]
	s_setprio 0
	s_setprio 1
	v_mfma_f32_16x16x32_bf16 v[118:121], v[174:177], v[190:193], v[118:121]
	v_mfma_f32_16x16x32_bf16 v[114:117], v[182:185], v[190:193], v[114:117]
	v_mfma_f32_16x16x32_bf16 v[102:105], v[174:177], v[198:201], v[102:105]
	v_mfma_f32_16x16x32_bf16 v[98:101], v[182:185], v[198:201], v[98:101]
	v_mfma_f32_16x16x32_bf16 v[86:89], v[174:177], v[206:209], v[86:89]
	v_mfma_f32_16x16x32_bf16 v[82:85], v[182:185], v[206:209], v[82:85]
	v_mfma_f32_16x16x32_bf16 v[70:73], v[174:177], v[214:217], v[70:73]
	v_mfma_f32_16x16x32_bf16 v[66:69], v[182:185], v[214:217], v[66:69]
	v_mfma_f32_16x16x32_bf16 v[118:121], v[178:181], v[194:197], v[118:121]
	v_mfma_f32_16x16x32_bf16 v[114:117], v[186:189], v[194:197], v[114:117]
	v_mfma_f32_16x16x32_bf16 v[102:105], v[178:181], v[202:205], v[102:105]
	v_mfma_f32_16x16x32_bf16 v[98:101], v[186:189], v[202:205], v[98:101]
	v_mfma_f32_16x16x32_bf16 v[86:89], v[178:181], v[210:213], v[86:89]
	v_mfma_f32_16x16x32_bf16 v[82:85], v[186:189], v[210:213], v[82:85]
	v_mfma_f32_16x16x32_bf16 v[70:73], v[178:181], v[218:221], v[70:73]
	v_mfma_f32_16x16x32_bf16 v[66:69], v[186:189], v[218:221], v[66:69]
	s_setprio 0
	s_barrier
	s_add_i32 s38, s63, s41
	v_lshl_add_u64 v[152:153], v[152:153], 0, s[8:9]
	s_mov_b32 m0, s38
	ds_read_b128 v[190:193], v160 offset:49152
	ds_read_b128 v[194:197], v160 offset:50176
	ds_read_b128 v[198:201], v160 offset:51200
	ds_read_b128 v[202:205], v160 offset:52224
	ds_read_b128 v[206:209], v160 offset:53248
	ds_read_b128 v[210:213], v160 offset:54272
	ds_read_b128 v[214:217], v160 offset:55296
	ds_read_b128 v[218:221], v160 offset:56320
	global_load_lds_dwordx4 v[152:153], off
	s_add_i32 m0, s38, 0x2000
	s_add_u32 s36, s36, 0x80080
	v_lshl_add_u64 v[152:153], v[222:223], 0, s[8:9]
	s_addc_u32 s37, s37, 0
	s_add_i32 s38, s64, s41
	global_load_lds_dwordx4 v[152:153], off
	v_lshl_add_u64 v[152:153], s[36:37], 0, v[132:133]
	s_mov_b32 m0, s38
	s_nop 0
	global_load_lds_dwordx4 v[152:153], off
	v_lshl_add_u64 v[152:153], s[36:37], 0, v[136:137]
	s_add_i32 m0, s38, 0x2000
	s_nop 0
	global_load_lds_dwordx4 v[152:153], off
	v_lshl_add_u64 v[152:153], v[224:225], 0, s[8:9]
	s_mov_b32 m0, s48
	s_nop 0
	global_load_lds_dwordx4 v[152:153], off
	v_lshl_add_u64 v[152:153], v[226:227], 0, s[8:9]
	s_mov_b32 m0, s49
	s_nop 0
	global_load_lds_dwordx4 v[152:153], off
	s_waitcnt vmcnt(8)
	s_waitcnt lgkmcnt(0)
	s_barrier
	s_setprio 1
	s_waitcnt lgkmcnt(0)
	v_mfma_f32_16x16x32_bf16 v[62:65], v[148:151], v[190:193], v[62:65]
	v_mfma_f32_16x16x32_bf16 v[58:61], v[166:169], v[190:193], v[58:61]
	v_mfma_f32_16x16x32_bf16 v[46:49], v[148:151], v[198:201], v[46:49]
	v_mfma_f32_16x16x32_bf16 v[42:45], v[166:169], v[198:201], v[42:45]
	v_mfma_f32_16x16x32_bf16 v[30:33], v[148:151], v[206:209], v[30:33]
	v_mfma_f32_16x16x32_bf16 v[26:29], v[166:169], v[206:209], v[26:29]
	v_mfma_f32_16x16x32_bf16 v[14:17], v[148:151], v[214:217], v[14:17]
	v_mfma_f32_16x16x32_bf16 v[10:13], v[166:169], v[214:217], v[10:13]
	v_mfma_f32_16x16x32_bf16 v[62:65], v[162:165], v[194:197], v[62:65]
	v_mfma_f32_16x16x32_bf16 v[58:61], v[170:173], v[194:197], v[58:61]
	v_mfma_f32_16x16x32_bf16 v[46:49], v[162:165], v[202:205], v[46:49]
	v_mfma_f32_16x16x32_bf16 v[42:45], v[170:173], v[202:205], v[42:45]
	v_mfma_f32_16x16x32_bf16 v[30:33], v[162:165], v[210:213], v[30:33]
	v_mfma_f32_16x16x32_bf16 v[26:29], v[170:173], v[210:213], v[26:29]
	v_mfma_f32_16x16x32_bf16 v[14:17], v[162:165], v[218:221], v[14:17]
	v_mfma_f32_16x16x32_bf16 v[10:13], v[170:173], v[218:221], v[10:13]
	s_setprio 0
	s_setprio 1
	v_mfma_f32_16x16x32_bf16 v[54:57], v[174:177], v[190:193], v[54:57]
	v_mfma_f32_16x16x32_bf16 v[50:53], v[182:185], v[190:193], v[50:53]
	v_mfma_f32_16x16x32_bf16 v[38:41], v[174:177], v[198:201], v[38:41]
	v_mfma_f32_16x16x32_bf16 v[34:37], v[182:185], v[198:201], v[34:37]
	v_mfma_f32_16x16x32_bf16 v[22:25], v[174:177], v[206:209], v[22:25]
	v_mfma_f32_16x16x32_bf16 v[18:21], v[182:185], v[206:209], v[18:21]
	v_mfma_f32_16x16x32_bf16 v[6:9], v[174:177], v[214:217], v[6:9]
	v_mfma_f32_16x16x32_bf16 v[2:5], v[182:185], v[214:217], v[2:5]
	v_mfma_f32_16x16x32_bf16 v[54:57], v[178:181], v[194:197], v[54:57]
	v_mfma_f32_16x16x32_bf16 v[50:53], v[186:189], v[194:197], v[50:53]
	v_mfma_f32_16x16x32_bf16 v[38:41], v[178:181], v[202:205], v[38:41]
	v_mfma_f32_16x16x32_bf16 v[34:37], v[186:189], v[202:205], v[34:37]
	v_mfma_f32_16x16x32_bf16 v[22:25], v[178:181], v[210:213], v[22:25]
	v_mfma_f32_16x16x32_bf16 v[18:21], v[186:189], v[210:213], v[18:21]
	v_mfma_f32_16x16x32_bf16 v[6:9], v[178:181], v[218:221], v[6:9]
	v_mfma_f32_16x16x32_bf16 v[2:5], v[186:189], v[218:221], v[2:5]
	s_setprio 0
	s_barrier
	s_add_i32 s62, s62, 2
	s_add_u32 s34, s34, 0x100
	s_addc_u32 s35, s35, 0
	s_add_u32 s60, s60, 0x100
	s_addc_u32 s61, s61, 0
	s_cmp_gt_u32 s62, 29
	s_cbranch_scc0 .LBB0_848
	v_lshl_add_u32 v152, s30, 8, v154
	v_lshl_or_b32 v150, s57, 8, v156
	v_ashrrev_i32_e32 v153, 31, v152
	v_ashrrev_i32_e32 v151, 31, v150
	v_lshlrev_b64 v[148:149], 11, v[152:153]
	v_lshl_add_u64 v[148:149], v[148:149], 0, v[150:151]
	v_lshl_add_u64 v[166:167], v[148:149], 1, s[50:51]
	v_mov_b32_e32 v222, v166
	v_mov_b32_e32 v223, v167
	v_mov_b32_e32 v240, 0x10000
	v_mov_b32_e32 v241, 0
	global_load_dwordx4 v[174:177], v[222:223], off
	global_load_dwordx4 v[178:181], v[222:223], off offset:256
	v_lshl_add_u64 v[222:223], v[240:241], 0, v[222:223]
	global_load_dwordx4 v[182:185], v[222:223], off
	global_load_dwordx4 v[186:189], v[222:223], off offset:256
	v_lshl_add_u64 v[222:223], v[240:241], 0, v[222:223]
	global_load_dwordx4 v[190:193], v[222:223], off
	global_load_dwordx4 v[194:197], v[222:223], off offset:256
	v_lshl_add_u64 v[222:223], v[240:241], 0, v[222:223]
	global_load_dwordx4 v[198:201], v[222:223], off
	global_load_dwordx4 v[202:205], v[222:223], off offset:256
	v_lshl_add_u64 v[222:223], v[240:241], 2, v[222:223]
	v_lshl_add_u64 v[222:223], v[240:241], 0, v[222:223]
	global_load_dwordx4 v[206:209], v[222:223], off
	global_load_dwordx4 v[210:213], v[222:223], off offset:256
	v_lshl_add_u64 v[222:223], v[240:241], 0, v[222:223]
	global_load_dwordx4 v[214:217], v[222:223], off
	global_load_dwordx4 v[218:221], v[222:223], off offset:256
	s_and_b64 vcc, exec, s[10:11]
	s_cbranch_vccz .LBB0_851
	s_barrier
.LBB0_851:
	s_nop 0
	v_lshl_add_u64 v[168:169], v[148:149], 2, s[28:29]
	s_andn2_b64 vcc, exec, s[4:5]
	s_mov_b64 s[4:5], -1
	s_waitcnt vmcnt(10)
	s_nop 1
	v_mov_b32_e32 v162, v174
	v_mov_b32_e32 v163, v175
	v_mov_b32_e32 v164, v176
	v_mov_b32_e32 v165, v177
	v_lshlrev_b32_e32 v170, 16, v162
	v_and_b32_e32 v171, 0xffff0000, v162
	v_lshlrev_b32_e32 v162, 16, v163
	v_and_b32_e32 v163, 0xffff0000, v163
	v_lshlrev_b32_e32 v172, 16, v164
	v_and_b32_e32 v173, 0xffff0000, v164
	v_lshlrev_b32_e32 v164, 16, v165
	v_and_b32_e32 v165, 0xffff0000, v165
	v_pk_add_f32 v[128:129], v[128:129], v[162:163]
	v_pk_add_f32 v[126:127], v[126:127], v[170:171]
	v_pk_add_f32 v[124:125], v[124:125], v[164:165]
	v_pk_add_f32 v[122:123], v[122:123], v[172:173]
	global_store_dwordx4 v[168:169], v[126:129], off
	global_store_dwordx4 v[168:169], v[122:125], off offset:16
	s_nop 0
	v_or_b32_e32 v126, 16, v152
	v_ashrrev_i32_e32 v127, 31, v126
	v_lshlrev_b64 v[126:127], 11, v[126:127]
	v_lshl_add_u64 v[126:127], v[126:127], 0, v[150:151]
	v_lshl_add_u64 v[128:129], v[126:127], 1, s[50:51]
	s_nop 1
	v_mov_b32_e32 v122, v178
	v_mov_b32_e32 v123, v179
	v_mov_b32_e32 v124, v180
	v_mov_b32_e32 v125, v181
	v_lshl_add_u64 v[222:223], v[240:241], 0, v[222:223]
	global_load_dwordx4 v[174:177], v[222:223], off
	global_load_dwordx4 v[178:181], v[222:223], off offset:256
	v_lshlrev_b32_e32 v162, 16, v122
	v_and_b32_e32 v163, 0xffff0000, v122
	v_lshlrev_b32_e32 v122, 16, v123
	v_and_b32_e32 v123, 0xffff0000, v123
	v_lshlrev_b32_e32 v164, 16, v124
	v_and_b32_e32 v165, 0xffff0000, v124
	v_lshlrev_b32_e32 v124, 16, v125
	v_and_b32_e32 v125, 0xffff0000, v125
	v_pk_add_f32 v[120:121], v[120:121], v[122:123]
	v_pk_add_f32 v[118:119], v[118:119], v[162:163]
	v_pk_add_f32 v[116:117], v[116:117], v[124:125]
	v_pk_add_f32 v[114:115], v[114:115], v[164:165]
	global_store_dwordx4 v[168:169], v[118:121], off offset:512
	global_store_dwordx4 v[168:169], v[114:117], off offset:528
	s_nop 0
	v_lshl_add_u64 v[118:119], v[126:127], 2, s[28:29]
	s_waitcnt vmcnt(14)
	s_nop 1
	v_mov_b32_e32 v114, v182
	v_mov_b32_e32 v115, v183
	v_mov_b32_e32 v116, v184
	v_mov_b32_e32 v117, v185
	v_lshlrev_b32_e32 v120, 16, v114
	v_and_b32_e32 v121, 0xffff0000, v114
	v_lshlrev_b32_e32 v114, 16, v115
	v_and_b32_e32 v115, 0xffff0000, v115
	v_lshlrev_b32_e32 v122, 16, v116
	v_and_b32_e32 v123, 0xffff0000, v116
	v_lshlrev_b32_e32 v116, 16, v117
	v_and_b32_e32 v117, 0xffff0000, v117
	v_pk_add_f32 v[112:113], v[112:113], v[114:115]
	v_pk_add_f32 v[110:111], v[110:111], v[120:121]
	v_pk_add_f32 v[108:109], v[108:109], v[116:117]
	v_pk_add_f32 v[106:107], v[106:107], v[122:123]
	global_store_dwordx4 v[118:119], v[110:113], off
	global_store_dwordx4 v[118:119], v[106:109], off offset:16
	s_nop 0
	v_or_b32_e32 v110, 32, v152
	v_ashrrev_i32_e32 v111, 31, v110
	v_lshlrev_b64 v[110:111], 11, v[110:111]
	v_lshl_add_u64 v[110:111], v[110:111], 0, v[150:151]
	v_lshl_add_u64 v[112:113], v[110:111], 1, s[50:51]
	s_nop 1
	v_mov_b32_e32 v106, v186
	v_mov_b32_e32 v107, v187
	v_mov_b32_e32 v108, v188
	v_mov_b32_e32 v109, v189
	v_lshl_add_u64 v[222:223], v[240:241], 0, v[222:223]
	global_load_dwordx4 v[182:185], v[222:223], off
	global_load_dwordx4 v[186:189], v[222:223], off offset:256
	v_lshlrev_b32_e32 v114, 16, v106
	v_and_b32_e32 v115, 0xffff0000, v106
	v_lshlrev_b32_e32 v106, 16, v107
	v_and_b32_e32 v107, 0xffff0000, v107
	v_lshlrev_b32_e32 v116, 16, v108
	v_and_b32_e32 v117, 0xffff0000, v108
	v_lshlrev_b32_e32 v108, 16, v109
	v_and_b32_e32 v109, 0xffff0000, v109
	v_pk_add_f32 v[104:105], v[104:105], v[106:107]
	v_pk_add_f32 v[102:103], v[102:103], v[114:115]
	v_pk_add_f32 v[100:101], v[100:101], v[108:109]
	v_pk_add_f32 v[98:99], v[98:99], v[116:117]
	global_store_dwordx4 v[118:119], v[102:105], off offset:512
	global_store_dwordx4 v[118:119], v[98:101], off offset:528
	s_nop 0
	v_lshl_add_u64 v[102:103], v[110:111], 2, s[28:29]
	s_waitcnt vmcnt(18)
	s_nop 1
	v_mov_b32_e32 v98, v190
	v_mov_b32_e32 v99, v191
	v_mov_b32_e32 v100, v192
	v_mov_b32_e32 v101, v193
	v_lshlrev_b32_e32 v104, 16, v98
	v_and_b32_e32 v105, 0xffff0000, v98
	v_lshlrev_b32_e32 v98, 16, v99
	v_and_b32_e32 v99, 0xffff0000, v99
	v_lshlrev_b32_e32 v106, 16, v100
	v_and_b32_e32 v107, 0xffff0000, v100
	v_lshlrev_b32_e32 v100, 16, v101
	v_and_b32_e32 v101, 0xffff0000, v101
	v_pk_add_f32 v[96:97], v[96:97], v[98:99]
	v_pk_add_f32 v[94:95], v[94:95], v[104:105]
	v_pk_add_f32 v[92:93], v[92:93], v[100:101]
	v_pk_add_f32 v[90:91], v[90:91], v[106:107]
	global_store_dwordx4 v[102:103], v[94:97], off
	global_store_dwordx4 v[102:103], v[90:93], off offset:16
	s_nop 0
	v_or_b32_e32 v94, 48, v152
	v_ashrrev_i32_e32 v95, 31, v94
	v_lshlrev_b64 v[94:95], 11, v[94:95]
	v_lshl_add_u64 v[94:95], v[94:95], 0, v[150:151]
	v_lshl_add_u64 v[96:97], v[94:95], 1, s[50:51]
	s_nop 1
	v_mov_b32_e32 v90, v194
	v_mov_b32_e32 v91, v195
	v_mov_b32_e32 v92, v196
	v_mov_b32_e32 v93, v197
	v_lshlrev_b32_e32 v98, 16, v90
	v_and_b32_e32 v99, 0xffff0000, v90
	v_lshlrev_b32_e32 v90, 16, v91
	v_and_b32_e32 v91, 0xffff0000, v91
	v_lshlrev_b32_e32 v100, 16, v92
	v_and_b32_e32 v101, 0xffff0000, v92
	v_lshlrev_b32_e32 v92, 16, v93
	v_and_b32_e32 v93, 0xffff0000, v93
	v_pk_add_f32 v[88:89], v[88:89], v[90:91]
	v_pk_add_f32 v[86:87], v[86:87], v[98:99]
	v_pk_add_f32 v[84:85], v[84:85], v[92:93]
	v_pk_add_f32 v[82:83], v[82:83], v[100:101]
	global_store_dwordx4 v[102:103], v[86:89], off offset:512
	global_store_dwordx4 v[102:103], v[82:85], off offset:528
	s_nop 0
	v_lshl_add_u64 v[86:87], v[94:95], 2, s[28:29]
	s_waitcnt vmcnt(20)
	s_nop 1
	v_mov_b32_e32 v82, v198
	v_mov_b32_e32 v83, v199
	v_mov_b32_e32 v84, v200
	v_mov_b32_e32 v85, v201
	v_lshlrev_b32_e32 v88, 16, v82
	v_and_b32_e32 v89, 0xffff0000, v82
	v_lshlrev_b32_e32 v82, 16, v83
	v_and_b32_e32 v83, 0xffff0000, v83
	v_lshlrev_b32_e32 v90, 16, v84
	v_and_b32_e32 v91, 0xffff0000, v84
	v_lshlrev_b32_e32 v84, 16, v85
	v_and_b32_e32 v85, 0xffff0000, v85
	v_pk_add_f32 v[80:81], v[80:81], v[82:83]
	v_pk_add_f32 v[78:79], v[78:79], v[88:89]
	v_pk_add_f32 v[76:77], v[76:77], v[84:85]
	v_pk_add_f32 v[74:75], v[74:75], v[90:91]
	global_store_dwordx4 v[86:87], v[78:81], off
	global_store_dwordx4 v[86:87], v[74:77], off offset:16
	s_nop 0
	v_lshl_add_u64 v[78:79], v[148:149], 0, s[12:13]
	v_lshl_add_u64 v[80:81], v[78:79], 1, s[50:51]
	s_nop 1
	v_mov_b32_e32 v74, v202
	v_mov_b32_e32 v75, v203
	v_mov_b32_e32 v76, v204
	v_mov_b32_e32 v77, v205
	v_lshlrev_b32_e32 v82, 16, v74
	v_and_b32_e32 v83, 0xffff0000, v74
	v_lshlrev_b32_e32 v74, 16, v75
	v_and_b32_e32 v75, 0xffff0000, v75
	v_lshlrev_b32_e32 v84, 16, v76
	v_and_b32_e32 v85, 0xffff0000, v76
	v_lshlrev_b32_e32 v76, 16, v77
	v_and_b32_e32 v77, 0xffff0000, v77
	v_pk_add_f32 v[72:73], v[72:73], v[74:75]
	v_pk_add_f32 v[70:71], v[70:71], v[82:83]
	v_pk_add_f32 v[68:69], v[68:69], v[76:77]
	v_pk_add_f32 v[66:67], v[66:67], v[84:85]
	global_store_dwordx4 v[86:87], v[70:73], off offset:512
	global_store_dwordx4 v[86:87], v[66:69], off offset:528
	s_nop 0
	v_lshl_add_u64 v[70:71], v[78:79], 2, s[28:29]
	s_waitcnt vmcnt(22)
	s_nop 1
	v_mov_b32_e32 v66, v206
	v_mov_b32_e32 v67, v207
	v_mov_b32_e32 v68, v208
	v_mov_b32_e32 v69, v209
	v_lshlrev_b32_e32 v72, 16, v66
	v_and_b32_e32 v73, 0xffff0000, v66
	v_lshlrev_b32_e32 v66, 16, v67
	v_and_b32_e32 v67, 0xffff0000, v67
	v_lshlrev_b32_e32 v74, 16, v68
	v_and_b32_e32 v75, 0xffff0000, v68
	v_lshlrev_b32_e32 v68, 16, v69
	v_and_b32_e32 v69, 0xffff0000, v69
	v_pk_add_f32 v[64:65], v[64:65], v[66:67]
	v_pk_add_f32 v[62:63], v[62:63], v[72:73]
	v_pk_add_f32 v[60:61], v[60:61], v[68:69]
	v_pk_add_f32 v[58:59], v[58:59], v[74:75]
	global_store_dwordx4 v[70:71], v[62:65], off
	global_store_dwordx4 v[70:71], v[58:61], off offset:16
	s_nop 0
	v_lshl_add_u64 v[62:63], v[148:149], 0, s[14:15]
	v_lshl_add_u64 v[64:65], v[62:63], 1, s[50:51]
	s_nop 1
	v_mov_b32_e32 v58, v210
	v_mov_b32_e32 v59, v211
	v_mov_b32_e32 v60, v212
	v_mov_b32_e32 v61, v213
	v_lshlrev_b32_e32 v66, 16, v58
	v_and_b32_e32 v67, 0xffff0000, v58
	v_lshlrev_b32_e32 v58, 16, v59
	v_and_b32_e32 v59, 0xffff0000, v59
	v_lshlrev_b32_e32 v68, 16, v60
	v_and_b32_e32 v69, 0xffff0000, v60
	v_lshlrev_b32_e32 v60, 16, v61
	v_and_b32_e32 v61, 0xffff0000, v61
	v_pk_add_f32 v[56:57], v[56:57], v[58:59]
	v_pk_add_f32 v[54:55], v[54:55], v[66:67]
	v_pk_add_f32 v[52:53], v[52:53], v[60:61]
	v_pk_add_f32 v[50:51], v[50:51], v[68:69]
	global_store_dwordx4 v[70:71], v[54:57], off offset:512
	global_store_dwordx4 v[70:71], v[50:53], off offset:528
	s_nop 0
	v_lshl_add_u64 v[54:55], v[62:63], 2, s[28:29]
	s_waitcnt vmcnt(24)
	s_nop 1
	v_mov_b32_e32 v50, v214
	v_mov_b32_e32 v51, v215
	v_mov_b32_e32 v52, v216
	v_mov_b32_e32 v53, v217
	v_lshlrev_b32_e32 v56, 16, v50
	v_and_b32_e32 v57, 0xffff0000, v50
	v_lshlrev_b32_e32 v50, 16, v51
	v_and_b32_e32 v51, 0xffff0000, v51
	v_lshlrev_b32_e32 v58, 16, v52
	v_and_b32_e32 v59, 0xffff0000, v52
	v_lshlrev_b32_e32 v52, 16, v53
	v_and_b32_e32 v53, 0xffff0000, v53
	v_pk_add_f32 v[48:49], v[48:49], v[50:51]
	v_pk_add_f32 v[46:47], v[46:47], v[56:57]
	v_pk_add_f32 v[44:45], v[44:45], v[52:53]
	v_pk_add_f32 v[42:43], v[42:43], v[58:59]
	global_store_dwordx4 v[54:55], v[46:49], off
	global_store_dwordx4 v[54:55], v[42:45], off offset:16
	s_nop 0
	v_lshl_add_u64 v[46:47], v[148:149], 0, s[16:17]
	v_lshl_add_u64 v[48:49], v[46:47], 1, s[50:51]
	s_nop 1
	v_mov_b32_e32 v42, v218
	v_mov_b32_e32 v43, v219
	v_mov_b32_e32 v44, v220
	v_mov_b32_e32 v45, v221
	v_lshlrev_b32_e32 v50, 16, v42
	v_and_b32_e32 v51, 0xffff0000, v42
	v_lshlrev_b32_e32 v42, 16, v43
	v_and_b32_e32 v43, 0xffff0000, v43
	v_lshlrev_b32_e32 v52, 16, v44
	v_and_b32_e32 v53, 0xffff0000, v44
	v_lshlrev_b32_e32 v44, 16, v45
	v_and_b32_e32 v45, 0xffff0000, v45
	v_pk_add_f32 v[40:41], v[40:41], v[42:43]
	v_pk_add_f32 v[38:39], v[38:39], v[50:51]
	v_pk_add_f32 v[36:37], v[36:37], v[44:45]
	v_pk_add_f32 v[34:35], v[34:35], v[52:53]
	global_store_dwordx4 v[54:55], v[38:41], off offset:512
	global_store_dwordx4 v[54:55], v[34:37], off offset:528
	s_nop 0
	v_lshl_add_u64 v[38:39], v[46:47], 2, s[28:29]
	s_waitcnt vmcnt(24)
	s_nop 1
	v_mov_b32_e32 v34, v174
	v_mov_b32_e32 v35, v175
	v_mov_b32_e32 v36, v176
	v_mov_b32_e32 v37, v177
	v_lshlrev_b32_e32 v40, 16, v34
	v_and_b32_e32 v41, 0xffff0000, v34
	v_lshlrev_b32_e32 v34, 16, v35
	v_and_b32_e32 v35, 0xffff0000, v35
	v_lshlrev_b32_e32 v42, 16, v36
	v_and_b32_e32 v43, 0xffff0000, v36
	v_lshlrev_b32_e32 v36, 16, v37
	v_and_b32_e32 v37, 0xffff0000, v37
	v_pk_add_f32 v[32:33], v[32:33], v[34:35]
	v_pk_add_f32 v[30:31], v[30:31], v[40:41]
	v_pk_add_f32 v[28:29], v[28:29], v[36:37]
	v_pk_add_f32 v[26:27], v[26:27], v[42:43]
	global_store_dwordx4 v[38:39], v[30:33], off
	global_store_dwordx4 v[38:39], v[26:29], off offset:16
	s_nop 0
	v_lshl_add_u64 v[30:31], v[148:149], 0, s[18:19]
	v_lshl_add_u64 v[32:33], v[30:31], 1, s[50:51]
	s_nop 1
	v_mov_b32_e32 v26, v178
	v_mov_b32_e32 v27, v179
	v_mov_b32_e32 v28, v180
	v_mov_b32_e32 v29, v181
	v_lshlrev_b32_e32 v34, 16, v26
	v_and_b32_e32 v35, 0xffff0000, v26
	v_lshlrev_b32_e32 v26, 16, v27
	v_and_b32_e32 v27, 0xffff0000, v27
	v_lshlrev_b32_e32 v36, 16, v28
	v_and_b32_e32 v37, 0xffff0000, v28
	v_lshlrev_b32_e32 v28, 16, v29
	v_and_b32_e32 v29, 0xffff0000, v29
	v_pk_add_f32 v[24:25], v[24:25], v[26:27]
	v_pk_add_f32 v[22:23], v[22:23], v[34:35]
	v_pk_add_f32 v[20:21], v[20:21], v[28:29]
	v_pk_add_f32 v[18:19], v[18:19], v[36:37]
	global_store_dwordx4 v[38:39], v[22:25], off offset:512
	global_store_dwordx4 v[38:39], v[18:21], off offset:528
	s_nop 0
	v_lshl_add_u64 v[22:23], v[30:31], 2, s[28:29]
	s_waitcnt vmcnt(22)
	s_nop 1
	v_mov_b32_e32 v18, v182
	v_mov_b32_e32 v19, v183
	v_mov_b32_e32 v20, v184
	v_mov_b32_e32 v21, v185
	v_lshlrev_b32_e32 v24, 16, v18
	v_and_b32_e32 v25, 0xffff0000, v18
	v_lshlrev_b32_e32 v18, 16, v19
	v_and_b32_e32 v19, 0xffff0000, v19
	v_lshlrev_b32_e32 v26, 16, v20
	v_and_b32_e32 v27, 0xffff0000, v20
	v_lshlrev_b32_e32 v20, 16, v21
	v_and_b32_e32 v21, 0xffff0000, v21
	v_pk_add_f32 v[16:17], v[16:17], v[18:19]
	v_pk_add_f32 v[14:15], v[14:15], v[24:25]
	v_pk_add_f32 v[12:13], v[12:13], v[20:21]
	v_pk_add_f32 v[10:11], v[10:11], v[26:27]
	global_store_dwordx4 v[22:23], v[14:17], off
	global_store_dwordx4 v[22:23], v[10:13], off offset:16
	s_nop 0
	s_nop 1
	v_mov_b32_e32 v10, v186
	v_mov_b32_e32 v11, v187
	v_mov_b32_e32 v12, v188
	v_mov_b32_e32 v13, v189
	v_lshlrev_b32_e32 v14, 16, v10
	v_and_b32_e32 v15, 0xffff0000, v10
	v_lshlrev_b32_e32 v10, 16, v11
	v_and_b32_e32 v11, 0xffff0000, v11
	v_lshlrev_b32_e32 v16, 16, v12
	v_and_b32_e32 v17, 0xffff0000, v12
	v_lshlrev_b32_e32 v12, 16, v13
	v_and_b32_e32 v13, 0xffff0000, v13
	v_pk_add_f32 v[8:9], v[8:9], v[10:11]
	v_pk_add_f32 v[6:7], v[6:7], v[14:15]
	v_pk_add_f32 v[4:5], v[4:5], v[12:13]
	v_pk_add_f32 v[2:3], v[2:3], v[16:17]
	global_store_dwordx4 v[22:23], v[6:9], off offset:512
	global_store_dwordx4 v[22:23], v[2:5], off offset:528
	s_cbranch_vccnz .LBB0_840
	s_andn2_b64 vcc, exec, s[6:7]
	s_cbranch_vccnz .LBB0_839
	s_barrier
	s_branch .LBB0_839

.LBB0_1159:
	ds_read_b128 v[166:169], v160
	ds_read_b128 v[170:173], v160 offset:1024
	ds_read_b128 v[174:177], v160 offset:2048
	ds_read_b128 v[178:181], v160 offset:3072
	ds_read_b128 v[182:185], v161
	ds_read_b128 v[186:189], v161 offset:1024
	ds_read_b128 v[224:227], v161 offset:2048
	ds_read_b128 v[228:231], v161 offset:3072
	s_add_u32 s38, s36, 0xfff20080
	s_addc_u32 s39, s37, -1
	s_cmp_eq_u32 s69, 52
	s_cselect_b32 s41, s31, s39
	s_cselect_b32 s40, s30, s38
	s_cselect_b32 s39, s35, s68
	s_cselect_b32 s38, s34, s1
	s_mov_b32 m0, s64
	v_lshl_add_u64 v[144:145], s[36:37], 0, v[140:141]
	ds_read_b128 v[192:195], v162
	ds_read_b128 v[196:199], v162 offset:1024
	ds_read_b128 v[200:203], v162 offset:2048
	ds_read_b128 v[204:207], v162 offset:3072
	ds_read_b128 v[208:211], v162 offset:4096
	ds_read_b128 v[212:215], v162 offset:5120
	ds_read_b128 v[216:219], v162 offset:6144
	ds_read_b128 v[220:223], v162 offset:7168
	global_load_lds_dwordx4 v[144:145], off
	v_lshl_add_u64 v[144:145], s[36:37], 0, v[142:143]
	s_mov_b32 m0, s65
	s_nop 0
	global_load_lds_dwordx4 v[144:145], off
	s_waitcnt vmcnt(8)
	s_waitcnt lgkmcnt(0)
	s_barrier
	s_setprio 1
	s_waitcnt lgkmcnt(0)
	s_nop 0
	v_mfma_scale_f32_16x16x128_f8f6f4 v[126:129], v[166:173], v[192:199], v[126:129], v165, v164 op_sel_hi:[0,0,0]
	v_mfma_scale_f32_16x16x128_f8f6f4 v[122:125], v[174:181], v[192:199], v[122:125], v165, v164 op_sel_hi:[0,0,0]
	v_mfma_scale_f32_16x16x128_f8f6f4 v[110:113], v[166:173], v[200:207], v[110:113], v165, v164 op_sel_hi:[0,0,0]
	v_mfma_scale_f32_16x16x128_f8f6f4 v[106:109], v[174:181], v[200:207], v[106:109], v165, v164 op_sel_hi:[0,0,0]
	v_mfma_scale_f32_16x16x128_f8f6f4 v[94:97], v[166:173], v[208:215], v[94:97], v165, v164 op_sel_hi:[0,0,0]
	v_mfma_scale_f32_16x16x128_f8f6f4 v[90:93], v[174:181], v[208:215], v[90:93], v165, v164 op_sel_hi:[0,0,0]
	v_mfma_scale_f32_16x16x128_f8f6f4 v[86:89], v[166:173], v[216:223], v[86:89], v165, v164 op_sel_hi:[0,0,0]
	v_mfma_scale_f32_16x16x128_f8f6f4 v[78:81], v[174:181], v[216:223], v[78:81], v165, v164 op_sel_hi:[0,0,0]
	s_setprio 0
	s_setprio 1
	s_nop 0
	v_mfma_scale_f32_16x16x128_f8f6f4 v[118:121], v[182:189], v[192:199], v[118:121], v165, v164 op_sel_hi:[0,0,0]
	v_mfma_scale_f32_16x16x128_f8f6f4 v[114:117], v[224:231], v[192:199], v[114:117], v165, v164 op_sel_hi:[0,0,0]
	v_mfma_scale_f32_16x16x128_f8f6f4 v[102:105], v[182:189], v[200:207], v[102:105], v165, v164 op_sel_hi:[0,0,0]
	v_mfma_scale_f32_16x16x128_f8f6f4 v[98:101], v[224:231], v[200:207], v[98:101], v165, v164 op_sel_hi:[0,0,0]
	v_mfma_scale_f32_16x16x128_f8f6f4 v[82:85], v[182:189], v[208:215], v[82:85], v165, v164 op_sel_hi:[0,0,0]
	v_mfma_scale_f32_16x16x128_f8f6f4 v[74:77], v[224:231], v[208:215], v[74:77], v165, v164 op_sel_hi:[0,0,0]
	v_mfma_scale_f32_16x16x128_f8f6f4 v[70:73], v[182:189], v[216:223], v[70:73], v165, v164 op_sel_hi:[0,0,0]
	v_mfma_scale_f32_16x16x128_f8f6f4 v[66:69], v[224:231], v[216:223], v[66:69], v165, v164 op_sel_hi:[0,0,0]
	s_setprio 0
	s_barrier
	s_add_i32 s70, s58, s50
	v_lshl_add_u64 v[144:145], s[38:39], 0, v[130:131]
	s_mov_b32 m0, s70
	ds_read_b128 v[192:195], v162 offset:16384
	ds_read_b128 v[196:199], v162 offset:17408
	ds_read_b128 v[200:203], v162 offset:18432
	ds_read_b128 v[204:207], v162 offset:19456
	ds_read_b128 v[208:211], v162 offset:20480
	ds_read_b128 v[212:215], v162 offset:21504
	ds_read_b128 v[216:219], v162 offset:22528
	ds_read_b128 v[220:223], v162 offset:23552
	global_load_lds_dwordx4 v[144:145], off
	s_add_i32 m0, s70, 0x2000
	s_add_u32 s70, s38, 0xe0000
	v_lshl_add_u64 v[148:149], s[38:39], 0, v[138:139]
	s_addc_u32 s71, s39, 0
	s_add_i32 s72, s59, s50
	global_load_lds_dwordx4 v[148:149], off
	v_lshl_add_u64 v[190:191], s[70:71], 0, v[130:131]
	s_mov_b32 m0, s72
	v_lshl_add_u64 v[240:241], s[40:41], 0, v[132:133]
	global_load_lds_dwordx4 v[190:191], off
	v_lshl_add_u64 v[190:191], s[70:71], 0, v[138:139]
	s_add_i32 m0, s72, 0x2000
	s_nop 0
	global_load_lds_dwordx4 v[190:191], off
	v_lshl_add_u64 v[190:191], s[40:41], 0, v[136:137]
	s_mov_b32 m0, s51
	s_nop 0
	global_load_lds_dwordx4 v[190:191], off
	s_mov_b32 m0, s52
	s_nop 0
	global_load_lds_dwordx4 v[240:241], off
	s_waitcnt vmcnt(8)
	s_waitcnt lgkmcnt(0)
	s_barrier
	s_setprio 1
	s_waitcnt lgkmcnt(0)
	s_nop 0
	v_mfma_scale_f32_16x16x128_f8f6f4 v[62:65], v[166:173], v[192:199], v[62:65], v165, v164 op_sel_hi:[0,0,0]
	v_mfma_scale_f32_16x16x128_f8f6f4 v[58:61], v[174:181], v[192:199], v[58:61], v165, v164 op_sel_hi:[0,0,0]
	v_mfma_scale_f32_16x16x128_f8f6f4 v[46:49], v[166:173], v[200:207], v[46:49], v165, v164 op_sel_hi:[0,0,0]
	v_mfma_scale_f32_16x16x128_f8f6f4 v[42:45], v[174:181], v[200:207], v[42:45], v165, v164 op_sel_hi:[0,0,0]
	v_mfma_scale_f32_16x16x128_f8f6f4 v[30:33], v[166:173], v[208:215], v[30:33], v165, v164 op_sel_hi:[0,0,0]
	v_mfma_scale_f32_16x16x128_f8f6f4 v[26:29], v[174:181], v[208:215], v[26:29], v165, v164 op_sel_hi:[0,0,0]
	v_mfma_scale_f32_16x16x128_f8f6f4 v[14:17], v[166:173], v[216:223], v[14:17], v165, v164 op_sel_hi:[0,0,0]
	v_mfma_scale_f32_16x16x128_f8f6f4 v[10:13], v[174:181], v[216:223], v[10:13], v165, v164 op_sel_hi:[0,0,0]
	s_setprio 0
	s_setprio 1
	s_nop 0
	v_mfma_scale_f32_16x16x128_f8f6f4 v[54:57], v[182:189], v[192:199], v[54:57], v165, v164 op_sel_hi:[0,0,0]
	v_mfma_scale_f32_16x16x128_f8f6f4 v[50:53], v[224:231], v[192:199], v[50:53], v165, v164 op_sel_hi:[0,0,0]
	v_mfma_scale_f32_16x16x128_f8f6f4 v[38:41], v[182:189], v[200:207], v[38:41], v165, v164 op_sel_hi:[0,0,0]
	v_mfma_scale_f32_16x16x128_f8f6f4 v[34:37], v[224:231], v[200:207], v[34:37], v165, v164 op_sel_hi:[0,0,0]
	v_mfma_scale_f32_16x16x128_f8f6f4 v[232:235], v[182:189], v[208:215], v[22:25], v165, v164 op_sel_hi:[0,0,0]
	v_mfma_scale_f32_16x16x128_f8f6f4 v[236:239], v[224:231], v[208:215], v[18:21], v165, v164 op_sel_hi:[0,0,0]
	v_mfma_scale_f32_16x16x128_f8f6f4 v[182:185], v[182:189], v[216:223], v[6:9], v165, v164 op_sel_hi:[0,0,0]
	v_mfma_scale_f32_16x16x128_f8f6f4 v[186:189], v[224:231], v[216:223], v[2:5], v165, v164 op_sel_hi:[0,0,0]
	s_setprio 0
	s_barrier
	s_add_i32 s70, 0, 0x18000
	s_add_i32 s71, 0, 0x1c000
	v_add_u32_e32 v22, s70, v158
	v_add_u32_e32 v178, s71, v158
	s_nop 0
	ds_read_b128 v[2:5], v22
	ds_read_b128 v[6:9], v22 offset:1024
	ds_read_b128 v[18:21], v22 offset:2048
	ds_read_b128 v[22:25], v22 offset:3072
	ds_read_b128 v[166:169], v178
	ds_read_b128 v[170:173], v178 offset:1024
	ds_read_b128 v[174:177], v178 offset:2048
	ds_read_b128 v[178:181], v178 offset:3072
	s_add_u32 s40, s40, 0xe0000
	s_addc_u32 s41, s41, 0
	s_mov_b32 m0, s53
	v_lshl_add_u64 v[224:225], s[40:41], 0, v[136:137]
	ds_read_b128 v[192:195], v162 offset:32768
	ds_read_b128 v[196:199], v162 offset:33792
	ds_read_b128 v[200:203], v162 offset:34816
	ds_read_b128 v[204:207], v162 offset:35840
	ds_read_b128 v[208:211], v162 offset:36864
	ds_read_b128 v[212:215], v162 offset:37888
	ds_read_b128 v[216:219], v162 offset:38912
	ds_read_b128 v[220:223], v162 offset:39936
	global_load_lds_dwordx4 v[224:225], off
	v_lshl_add_u64 v[224:225], s[40:41], 0, v[132:133]
	s_mov_b32 m0, s54
	s_nop 0
	global_load_lds_dwordx4 v[224:225], off
	s_waitcnt vmcnt(8)
	s_waitcnt lgkmcnt(0)
	s_barrier
	s_setprio 1
	s_waitcnt lgkmcnt(0)
	s_nop 0
	v_mfma_scale_f32_16x16x128_f8f6f4 v[126:129], v[2:9], v[192:199], v[126:129], v165, v164 op_sel_hi:[0,0,0]
	v_mfma_scale_f32_16x16x128_f8f6f4 v[122:125], v[18:25], v[192:199], v[122:125], v165, v164 op_sel_hi:[0,0,0]
	v_mfma_scale_f32_16x16x128_f8f6f4 v[110:113], v[2:9], v[200:207], v[110:113], v165, v164 op_sel_hi:[0,0,0]
	v_mfma_scale_f32_16x16x128_f8f6f4 v[106:109], v[18:25], v[200:207], v[106:109], v165, v164 op_sel_hi:[0,0,0]
	v_mfma_scale_f32_16x16x128_f8f6f4 v[94:97], v[2:9], v[208:215], v[94:97], v165, v164 op_sel_hi:[0,0,0]
	v_mfma_scale_f32_16x16x128_f8f6f4 v[90:93], v[18:25], v[208:215], v[90:93], v165, v164 op_sel_hi:[0,0,0]
	v_mfma_scale_f32_16x16x128_f8f6f4 v[86:89], v[2:9], v[216:223], v[86:89], v165, v164 op_sel_hi:[0,0,0]
	v_mfma_scale_f32_16x16x128_f8f6f4 v[78:81], v[18:25], v[216:223], v[78:81], v165, v164 op_sel_hi:[0,0,0]
	s_setprio 0
	s_setprio 1
	s_nop 0
	v_mfma_scale_f32_16x16x128_f8f6f4 v[118:121], v[166:173], v[192:199], v[118:121], v165, v164 op_sel_hi:[0,0,0]
	v_mfma_scale_f32_16x16x128_f8f6f4 v[114:117], v[174:181], v[192:199], v[114:117], v165, v164 op_sel_hi:[0,0,0]
	v_mfma_scale_f32_16x16x128_f8f6f4 v[102:105], v[166:173], v[200:207], v[102:105], v165, v164 op_sel_hi:[0,0,0]
	v_mfma_scale_f32_16x16x128_f8f6f4 v[98:101], v[174:181], v[200:207], v[98:101], v165, v164 op_sel_hi:[0,0,0]
	v_mfma_scale_f32_16x16x128_f8f6f4 v[82:85], v[166:173], v[208:215], v[82:85], v165, v164 op_sel_hi:[0,0,0]
	v_mfma_scale_f32_16x16x128_f8f6f4 v[74:77], v[174:181], v[208:215], v[74:77], v165, v164 op_sel_hi:[0,0,0]
	v_mfma_scale_f32_16x16x128_f8f6f4 v[70:73], v[166:173], v[216:223], v[70:73], v165, v164 op_sel_hi:[0,0,0]
	v_mfma_scale_f32_16x16x128_f8f6f4 v[66:69], v[174:181], v[216:223], v[66:69], v165, v164 op_sel_hi:[0,0,0]
	s_setprio 0
	s_barrier
	s_add_i32 s40, s70, s50
	v_lshl_add_u64 v[144:145], v[144:145], 0, s[14:15]
	s_mov_b32 m0, s40
	ds_read_b128 v[192:195], v162 offset:49152
	ds_read_b128 v[196:199], v162 offset:50176
	ds_read_b128 v[200:203], v162 offset:51200
	ds_read_b128 v[204:207], v162 offset:52224
	ds_read_b128 v[208:211], v162 offset:53248
	ds_read_b128 v[212:215], v162 offset:54272
	ds_read_b128 v[216:219], v162 offset:55296
	ds_read_b128 v[220:223], v162 offset:56320
	global_load_lds_dwordx4 v[144:145], off
	s_add_i32 m0, s40, 0x2000
	s_add_u32 s38, s38, 0xe0080
	v_lshl_add_u64 v[144:145], v[148:149], 0, s[14:15]
	s_addc_u32 s39, s39, 0
	s_add_i32 s40, s71, s50
	global_load_lds_dwordx4 v[144:145], off
	v_lshl_add_u64 v[144:145], s[38:39], 0, v[130:131]
	s_mov_b32 m0, s40
	s_nop 0
	global_load_lds_dwordx4 v[144:145], off
	v_lshl_add_u64 v[144:145], s[38:39], 0, v[138:139]
	s_add_i32 m0, s40, 0x2000
	s_nop 0
	global_load_lds_dwordx4 v[144:145], off
	v_lshl_add_u64 v[144:145], v[190:191], 0, s[14:15]
	s_mov_b32 m0, s56
	s_nop 0
	global_load_lds_dwordx4 v[144:145], off
	v_lshl_add_u64 v[144:145], v[240:241], 0, s[14:15]
	s_mov_b32 m0, s57
	s_nop 0
	global_load_lds_dwordx4 v[144:145], off
	s_waitcnt vmcnt(8)
	s_waitcnt lgkmcnt(0)
	s_barrier
	s_setprio 1
	s_waitcnt lgkmcnt(0)
	s_nop 0
	v_mfma_scale_f32_16x16x128_f8f6f4 v[62:65], v[2:9], v[192:199], v[62:65], v165, v164 op_sel_hi:[0,0,0]
	v_mfma_scale_f32_16x16x128_f8f6f4 v[58:61], v[18:25], v[192:199], v[58:61], v165, v164 op_sel_hi:[0,0,0]
	v_mfma_scale_f32_16x16x128_f8f6f4 v[46:49], v[2:9], v[200:207], v[46:49], v165, v164 op_sel_hi:[0,0,0]
	v_mfma_scale_f32_16x16x128_f8f6f4 v[42:45], v[18:25], v[200:207], v[42:45], v165, v164 op_sel_hi:[0,0,0]
	v_mfma_scale_f32_16x16x128_f8f6f4 v[30:33], v[2:9], v[208:215], v[30:33], v165, v164 op_sel_hi:[0,0,0]
	v_mfma_scale_f32_16x16x128_f8f6f4 v[26:29], v[18:25], v[208:215], v[26:29], v165, v164 op_sel_hi:[0,0,0]
	v_mfma_scale_f32_16x16x128_f8f6f4 v[14:17], v[2:9], v[216:223], v[14:17], v165, v164 op_sel_hi:[0,0,0]
	v_mfma_scale_f32_16x16x128_f8f6f4 v[10:13], v[18:25], v[216:223], v[10:13], v165, v164 op_sel_hi:[0,0,0]
	s_setprio 0
	s_setprio 1
	s_nop 0
	v_mfma_scale_f32_16x16x128_f8f6f4 v[54:57], v[166:173], v[192:199], v[54:57], v165, v164 op_sel_hi:[0,0,0]
	v_mfma_scale_f32_16x16x128_f8f6f4 v[50:53], v[174:181], v[192:199], v[50:53], v165, v164 op_sel_hi:[0,0,0]
	v_mfma_scale_f32_16x16x128_f8f6f4 v[38:41], v[166:173], v[200:207], v[38:41], v165, v164 op_sel_hi:[0,0,0]
	v_mfma_scale_f32_16x16x128_f8f6f4 v[34:37], v[174:181], v[200:207], v[34:37], v165, v164 op_sel_hi:[0,0,0]
	v_mfma_scale_f32_16x16x128_f8f6f4 v[22:25], v[166:173], v[208:215], v[232:235], v165, v164 op_sel_hi:[0,0,0]
	v_mfma_scale_f32_16x16x128_f8f6f4 v[18:21], v[174:181], v[208:215], v[236:239], v165, v164 op_sel_hi:[0,0,0]
	v_mfma_scale_f32_16x16x128_f8f6f4 v[6:9], v[166:173], v[216:223], v[182:185], v165, v164 op_sel_hi:[0,0,0]
	v_mfma_scale_f32_16x16x128_f8f6f4 v[2:5], v[174:181], v[216:223], v[186:189], v165, v164 op_sel_hi:[0,0,0]
	s_setprio 0
	s_barrier
	s_add_i32 s69, s69, 2
	s_add_u32 s36, s36, 0x100
	s_addc_u32 s37, s37, 0
	s_add_u32 s1, s1, 0x100
	s_addc_u32 s68, s68, 0
	s_cmp_gt_u32 s69, 53
	s_cbranch_scc0 .LBB0_1159
	v_lshl_add_u32 v166, s0, 8, v157
	v_ashrrev_i32_e32 v167, 31, v166
	v_lshl_add_u64 v[144:145], v[166:167], 2, s[6:7]
	global_load_dword v168, v[144:145], off
	global_load_dword v178, v[144:145], off offset:64
	global_load_dword v179, v[144:145], off offset:128
	global_load_dword v180, v[144:145], off offset:192
	global_load_dword v181, v[144:145], off offset:512
	global_load_dword v182, v[144:145], off offset:576
	global_load_dword v183, v[144:145], off offset:640
	global_load_dword v184, v[144:145], off offset:704
	s_and_b64 vcc, exec, s[16:17]
	s_cbranch_vccz .LBB0_1162
	s_barrier
.LBB0_1162:
	v_lshl_or_b32 v148, s67, 8, v159
	v_ashrrev_i32_e32 v149, 31, v148
	v_lshlrev_b64 v[172:173], 12, v[166:167]
	v_or_b32_e32 v170, 16, v166
	v_lshlrev_b64 v[174:175], 1, v[148:149]
	v_lshl_add_u64 v[148:149], s[12:13], 0, v[172:173]
	v_ashrrev_i32_e32 v171, 31, v170
	v_lshl_add_u64 v[148:149], v[148:149], 0, v[174:175]
	v_lshl_add_u64 v[172:173], v[170:171], 2, s[6:7]
	s_waitcnt vmcnt(7)
	v_pk_mul_f32 v[128:129], v[128:129], v[168:169] op_sel_hi:[1,0]
	v_pk_mul_f32 v[126:127], v[126:127], v[168:169] op_sel_hi:[1,0]
	v_pk_mul_f32 v[124:125], v[124:125], v[168:169] op_sel_hi:[1,0]
	v_pk_mul_f32 v[122:123], v[122:123], v[168:169] op_sel_hi:[1,0]
	v_pk_mul_f32 v[120:121], v[120:121], v[168:169] op_sel_hi:[1,0]
	v_pk_mul_f32 v[118:119], v[118:119], v[168:169] op_sel_hi:[1,0]
	v_pk_mul_f32 v[176:177], v[116:117], v[168:169] op_sel_hi:[1,0]
	v_pk_mul_f32 v[168:169], v[114:115], v[168:169] op_sel_hi:[1,0]
	v_cvt_pk_bf16_f32 v114, v126, v127
	v_cvt_pk_bf16_f32 v115, v128, v129
	v_cvt_pk_bf16_f32 v116, v122, v123
	v_cvt_pk_bf16_f32 v117, v124, v125
	global_store_dwordx4 v[148:149], v[114:117], off
	s_nop 1
	v_cvt_pk_bf16_f32 v114, v118, v119
	v_cvt_pk_bf16_f32 v115, v120, v121
	v_cvt_pk_bf16_f32 v116, v168, v169
	v_cvt_pk_bf16_f32 v117, v176, v177
	global_store_dwordx4 v[148:149], v[114:117], off offset:256
	s_nop 0
	v_lshlrev_b64 v[118:119], 12, v[170:171]
	v_or_b32_e32 v116, 32, v166
	v_lshl_add_u64 v[118:119], s[12:13], 0, v[118:119]
	v_ashrrev_i32_e32 v117, 31, v116
	v_lshl_add_u64 v[118:119], v[118:119], 0, v[174:175]
	v_lshl_add_u64 v[120:121], v[116:117], 2, s[6:7]
	s_waitcnt vmcnt(8)
	v_mov_b32_e32 v114, v178
	v_pk_mul_f32 v[112:113], v[112:113], v[114:115] op_sel_hi:[1,0]
	v_pk_mul_f32 v[110:111], v[110:111], v[114:115] op_sel_hi:[1,0]
	v_pk_mul_f32 v[108:109], v[108:109], v[114:115] op_sel_hi:[1,0]
	v_pk_mul_f32 v[106:107], v[106:107], v[114:115] op_sel_hi:[1,0]
	v_pk_mul_f32 v[104:105], v[104:105], v[114:115] op_sel_hi:[1,0]
	v_pk_mul_f32 v[102:103], v[102:103], v[114:115] op_sel_hi:[1,0]
	v_pk_mul_f32 v[122:123], v[100:101], v[114:115] op_sel_hi:[1,0]
	v_pk_mul_f32 v[114:115], v[98:99], v[114:115] op_sel_hi:[1,0]
	v_cvt_pk_bf16_f32 v98, v110, v111
	v_cvt_pk_bf16_f32 v99, v112, v113
	v_cvt_pk_bf16_f32 v100, v106, v107
	v_cvt_pk_bf16_f32 v101, v108, v109
	global_store_dwordx4 v[118:119], v[98:101], off
	s_nop 1
	v_cvt_pk_bf16_f32 v98, v102, v103
	v_cvt_pk_bf16_f32 v99, v104, v105
	v_cvt_pk_bf16_f32 v100, v114, v115
	v_cvt_pk_bf16_f32 v101, v122, v123
	global_store_dwordx4 v[118:119], v[98:101], off offset:256
	s_nop 0
	v_lshlrev_b64 v[102:103], 12, v[116:117]
	v_or_b32_e32 v100, 48, v166
	v_lshl_add_u64 v[102:103], s[12:13], 0, v[102:103]
	v_ashrrev_i32_e32 v101, 31, v100
	v_lshl_add_u64 v[102:103], v[102:103], 0, v[174:175]
	v_lshl_add_u64 v[104:105], v[100:101], 2, s[6:7]
	s_waitcnt vmcnt(9)
	v_mov_b32_e32 v98, v179
	v_pk_mul_f32 v[96:97], v[96:97], v[98:99] op_sel_hi:[1,0]
	v_pk_mul_f32 v[94:95], v[94:95], v[98:99] op_sel_hi:[1,0]
	v_pk_mul_f32 v[92:93], v[92:93], v[98:99] op_sel_hi:[1,0]
	v_pk_mul_f32 v[90:91], v[90:91], v[98:99] op_sel_hi:[1,0]
	v_pk_mul_f32 v[84:85], v[84:85], v[98:99] op_sel_hi:[1,0]
	v_pk_mul_f32 v[82:83], v[82:83], v[98:99] op_sel_hi:[1,0]
	v_pk_mul_f32 v[106:107], v[76:77], v[98:99] op_sel_hi:[1,0]
	v_pk_mul_f32 v[98:99], v[74:75], v[98:99] op_sel_hi:[1,0]
	v_cvt_pk_bf16_f32 v74, v94, v95
	v_cvt_pk_bf16_f32 v75, v96, v97
	v_cvt_pk_bf16_f32 v76, v90, v91
	v_cvt_pk_bf16_f32 v77, v92, v93
	global_store_dwordx4 v[102:103], v[74:77], off
	s_nop 1
	v_cvt_pk_bf16_f32 v74, v82, v83
	v_cvt_pk_bf16_f32 v75, v84, v85
	v_cvt_pk_bf16_f32 v76, v98, v99
	v_cvt_pk_bf16_f32 v77, v106, v107
	global_store_dwordx4 v[102:103], v[74:77], off offset:256
	s_nop 0
	s_waitcnt vmcnt(10)
	v_mov_b32_e32 v74, v180
	v_pk_mul_f32 v[82:83], v[88:89], v[74:75] op_sel_hi:[1,0]
	v_lshlrev_b64 v[76:77], 12, v[100:101]
	v_lshl_add_u64 v[76:77], s[12:13], 0, v[76:77]
	v_lshl_add_u64 v[76:77], v[76:77], 0, v[174:175]
	v_pk_mul_f32 v[84:85], v[86:87], v[74:75] op_sel_hi:[1,0]
	v_pk_mul_f32 v[80:81], v[80:81], v[74:75] op_sel_hi:[1,0]
	v_pk_mul_f32 v[78:79], v[78:79], v[74:75] op_sel_hi:[1,0]
	v_pk_mul_f32 v[72:73], v[72:73], v[74:75] op_sel_hi:[1,0]
	v_pk_mul_f32 v[70:71], v[70:71], v[74:75] op_sel_hi:[1,0]
	v_pk_mul_f32 v[86:87], v[68:69], v[74:75] op_sel_hi:[1,0]
	v_pk_mul_f32 v[74:75], v[66:67], v[74:75] op_sel_hi:[1,0]
	v_cvt_pk_bf16_f32 v66, v84, v85
	v_cvt_pk_bf16_f32 v67, v82, v83
	v_cvt_pk_bf16_f32 v68, v78, v79
	v_cvt_pk_bf16_f32 v69, v80, v81
	global_store_dwordx4 v[76:77], v[66:69], off
	s_nop 1
	v_cvt_pk_bf16_f32 v66, v70, v71
	v_cvt_pk_bf16_f32 v67, v72, v73
	v_cvt_pk_bf16_f32 v68, v74, v75
	v_cvt_pk_bf16_f32 v69, v86, v87
	global_store_dwordx4 v[76:77], v[66:69], off offset:256
	s_nop 0
	v_add_co_u32_e32 v70, vcc, s60, v148
	v_lshl_add_u64 v[68:69], v[148:149], 0, s[18:19]
	s_nop 0
	v_addc_co_u32_e32 v71, vcc, 0, v149, vcc
	s_waitcnt vmcnt(11)
	v_mov_b32_e32 v66, v181
	v_pk_mul_f32 v[64:65], v[64:65], v[66:67] op_sel_hi:[1,0]
	v_pk_mul_f32 v[62:63], v[62:63], v[66:67] op_sel_hi:[1,0]
	v_pk_mul_f32 v[60:61], v[60:61], v[66:67] op_sel_hi:[1,0]
	v_pk_mul_f32 v[58:59], v[58:59], v[66:67] op_sel_hi:[1,0]
	v_pk_mul_f32 v[56:57], v[56:57], v[66:67] op_sel_hi:[1,0]
	v_pk_mul_f32 v[54:55], v[54:55], v[66:67] op_sel_hi:[1,0]
	v_pk_mul_f32 v[72:73], v[52:53], v[66:67] op_sel_hi:[1,0]
	v_pk_mul_f32 v[66:67], v[50:51], v[66:67] op_sel_hi:[1,0]
	v_cvt_pk_bf16_f32 v50, v62, v63
	v_cvt_pk_bf16_f32 v51, v64, v65
	v_cvt_pk_bf16_f32 v52, v58, v59
	v_cvt_pk_bf16_f32 v53, v60, v61
	global_store_dwordx4 v[70:71], v[50:53], off
	s_nop 1
	v_cvt_pk_bf16_f32 v50, v54, v55
	v_cvt_pk_bf16_f32 v51, v56, v57
	v_cvt_pk_bf16_f32 v52, v66, v67
	v_cvt_pk_bf16_f32 v53, v72, v73
	global_store_dwordx4 v[68:69], v[50:53], off offset:256
	s_nop 0
	v_add_co_u32_e32 v54, vcc, s61, v148
	v_lshl_add_u64 v[52:53], v[148:149], 0, s[20:21]
	s_nop 0
	v_addc_co_u32_e32 v55, vcc, 0, v149, vcc
	s_waitcnt vmcnt(12)
	v_mov_b32_e32 v50, v182
	v_pk_mul_f32 v[48:49], v[48:49], v[50:51] op_sel_hi:[1,0]
	v_pk_mul_f32 v[46:47], v[46:47], v[50:51] op_sel_hi:[1,0]
	v_pk_mul_f32 v[44:45], v[44:45], v[50:51] op_sel_hi:[1,0]
	v_pk_mul_f32 v[42:43], v[42:43], v[50:51] op_sel_hi:[1,0]
	v_pk_mul_f32 v[40:41], v[40:41], v[50:51] op_sel_hi:[1,0]
	v_pk_mul_f32 v[38:39], v[38:39], v[50:51] op_sel_hi:[1,0]
	v_pk_mul_f32 v[56:57], v[36:37], v[50:51] op_sel_hi:[1,0]
	v_pk_mul_f32 v[50:51], v[34:35], v[50:51] op_sel_hi:[1,0]
	v_cvt_pk_bf16_f32 v34, v46, v47
	v_cvt_pk_bf16_f32 v35, v48, v49
	v_cvt_pk_bf16_f32 v36, v42, v43
	v_cvt_pk_bf16_f32 v37, v44, v45
	global_store_dwordx4 v[54:55], v[34:37], off
	s_nop 1
	v_cvt_pk_bf16_f32 v34, v38, v39
	v_cvt_pk_bf16_f32 v35, v40, v41
	v_cvt_pk_bf16_f32 v36, v50, v51
	v_cvt_pk_bf16_f32 v37, v56, v57
	global_store_dwordx4 v[52:53], v[34:37], off offset:256
	s_nop 0
	v_add_co_u32_e32 v38, vcc, s62, v148
	v_lshl_add_u64 v[36:37], v[148:149], 0, s[22:23]
	s_nop 0
	v_addc_co_u32_e32 v39, vcc, 0, v149, vcc
	s_and_b64 vcc, exec, s[2:3]
	s_waitcnt vmcnt(13)
	v_mov_b32_e32 v34, v183
	v_pk_mul_f32 v[32:33], v[32:33], v[34:35] op_sel_hi:[1,0]
	v_pk_mul_f32 v[30:31], v[30:31], v[34:35] op_sel_hi:[1,0]
	v_pk_mul_f32 v[28:29], v[28:29], v[34:35] op_sel_hi:[1,0]
	v_pk_mul_f32 v[26:27], v[26:27], v[34:35] op_sel_hi:[1,0]
	v_pk_mul_f32 v[24:25], v[24:25], v[34:35] op_sel_hi:[1,0]
	v_pk_mul_f32 v[22:23], v[22:23], v[34:35] op_sel_hi:[1,0]
	v_pk_mul_f32 v[40:41], v[20:21], v[34:35] op_sel_hi:[1,0]
	v_pk_mul_f32 v[34:35], v[18:19], v[34:35] op_sel_hi:[1,0]
	v_cvt_pk_bf16_f32 v18, v30, v31
	v_cvt_pk_bf16_f32 v19, v32, v33
	v_cvt_pk_bf16_f32 v20, v26, v27
	v_cvt_pk_bf16_f32 v21, v28, v29
	global_store_dwordx4 v[38:39], v[18:21], off
	s_nop 1
	v_cvt_pk_bf16_f32 v18, v22, v23
	v_cvt_pk_bf16_f32 v19, v24, v25
	v_cvt_pk_bf16_f32 v20, v34, v35
	v_cvt_pk_bf16_f32 v21, v40, v41
	global_store_dwordx4 v[36:37], v[18:21], off offset:256
	s_nop 0
	v_add_co_u32_e64 v22, s[0:1], s63, v148
	v_lshl_add_u64 v[20:21], v[148:149], 0, s[24:25]
	s_nop 0
	v_addc_co_u32_e64 v23, s[0:1], 0, v149, s[0:1]
	s_mov_b64 s[0:1], -1
	s_waitcnt vmcnt(14)
	v_mov_b32_e32 v18, v184
	v_pk_mul_f32 v[16:17], v[16:17], v[18:19] op_sel_hi:[1,0]
	v_pk_mul_f32 v[14:15], v[14:15], v[18:19] op_sel_hi:[1,0]
	v_pk_mul_f32 v[12:13], v[12:13], v[18:19] op_sel_hi:[1,0]
	v_pk_mul_f32 v[10:11], v[10:11], v[18:19] op_sel_hi:[1,0]
	v_pk_mul_f32 v[8:9], v[8:9], v[18:19] op_sel_hi:[1,0]
	v_pk_mul_f32 v[6:7], v[6:7], v[18:19] op_sel_hi:[1,0]
	v_pk_mul_f32 v[24:25], v[4:5], v[18:19] op_sel_hi:[1,0]
	v_pk_mul_f32 v[18:19], v[2:3], v[18:19] op_sel_hi:[1,0]
	v_cvt_pk_bf16_f32 v2, v14, v15
	v_cvt_pk_bf16_f32 v3, v16, v17
	v_cvt_pk_bf16_f32 v4, v10, v11
	v_cvt_pk_bf16_f32 v5, v12, v13
	global_store_dwordx4 v[22:23], v[2:5], off
	s_nop 1
	v_cvt_pk_bf16_f32 v2, v6, v7
	v_cvt_pk_bf16_f32 v3, v8, v9
	v_cvt_pk_bf16_f32 v4, v18, v19
	v_cvt_pk_bf16_f32 v5, v24, v25
	global_store_dwordx4 v[20:21], v[2:5], off offset:256
	s_cbranch_vccnz .LBB0_1151
	s_andn2_b64 vcc, exec, s[10:11]
	s_cbranch_vccnz .LBB0_1150
	s_barrier
	s_branch .LBB0_1150

.LBB0_1181:
	v_lshl_add_u32 v148, s20, 8, v147
	v_ashrrev_i32_e32 v149, 31, v148
	v_lshl_add_u64 v[140:141], v[148:149], 2, s[6:7]
	global_load_dword v158, v[140:141], off
	global_load_dword v178, v[140:141], off offset:64
	global_load_dword v179, v[140:141], off offset:128
	global_load_dword v180, v[140:141], off offset:192
	global_load_dword v181, v[140:141], off offset:512
	global_load_dword v182, v[140:141], off offset:576
	global_load_dword v183, v[140:141], off offset:640
	global_load_dword v184, v[140:141], off offset:704
	s_and_b64 vcc, exec, s[12:13]
	s_cbranch_vccz .LBB0_1183
	s_barrier
.LBB0_1183:
	s_abs_i32 s22, s67
	s_mul_hi_u32 s23, s22, s61
	s_mul_i32 s24, s23, s59
	s_ashr_i32 s20, s67, 31
	s_sub_i32 s22, s22, s24
	s_xor_b32 s20, s20, s60
	s_add_i32 s25, s23, 1
	s_sub_i32 s24, s22, s59
	s_cmp_ge_u32 s22, s59
	s_cselect_b32 s23, s25, s23
	s_cselect_b32 s22, s24, s22
	s_add_i32 s24, s23, 1
	s_cmp_ge_u32 s22, s59
	s_cselect_b32 s22, s24, s23
	s_xor_b32 s22, s22, s20
	s_sub_i32 s20, s22, s20
	s_mul_hi_i32 s23, s53, s20
	s_mul_i32 s22, s53, s20
	s_lshl_b64 s[22:23], s[22:23], 1
	v_lshl_or_b32 v144, s66, 8, v151
	v_subrev_u32_e32 v142, s52, v148
	s_add_u32 s22, s50, s22
	v_ashrrev_i32_e32 v145, 31, v144
	v_ashrrev_i32_e32 v143, 31, v142
	s_addc_u32 s23, s51, s23
	v_or_b32_e32 v160, 16, v148
	v_lshlrev_b64 v[162:163], 12, v[142:143]
	v_lshl_add_u64 v[144:145], v[144:145], 1, s[22:23]
	v_ashrrev_i32_e32 v161, 31, v160
	v_lshl_add_u64 v[162:163], v[144:145], 0, v[162:163]
	v_lshl_add_u64 v[164:165], v[160:161], 2, s[6:7]
	s_and_b64 vcc, exec, s[2:3]
	s_mov_b64 s[2:3], -1
	s_waitcnt vmcnt(7)
	v_pk_mul_f32 v[122:123], v[122:123], v[158:159] op_sel_hi:[1,0]
	v_pk_mul_f32 v[120:121], v[120:121], v[158:159] op_sel_hi:[1,0]
	v_pk_mul_f32 v[126:127], v[126:127], v[158:159] op_sel_hi:[1,0]
	v_pk_mul_f32 v[124:125], v[124:125], v[158:159] op_sel_hi:[1,0]
	v_pk_mul_f32 v[118:119], v[118:119], v[158:159] op_sel_hi:[1,0]
	v_pk_mul_f32 v[116:117], v[116:117], v[158:159] op_sel_hi:[1,0]
	v_pk_mul_f32 v[166:167], v[114:115], v[158:159] op_sel_hi:[1,0]
	v_pk_mul_f32 v[158:159], v[112:113], v[158:159] op_sel_hi:[1,0]
	v_cvt_pk_bf16_f32 v112, v120, v121
	v_cvt_pk_bf16_f32 v113, v122, v123
	v_cvt_pk_bf16_f32 v114, v124, v125
	v_cvt_pk_bf16_f32 v115, v126, v127
	global_store_dwordx4 v[162:163], v[112:115], off
	s_nop 1
	v_cvt_pk_bf16_f32 v112, v116, v117
	v_cvt_pk_bf16_f32 v113, v118, v119
	v_cvt_pk_bf16_f32 v114, v158, v159
	v_cvt_pk_bf16_f32 v115, v166, v167
	global_store_dwordx4 v[162:163], v[112:115], off offset:256
	s_nop 0
	v_subrev_u32_e32 v116, s52, v160
	v_ashrrev_i32_e32 v117, 31, v116
	v_or_b32_e32 v114, 32, v148
	v_lshlrev_b64 v[116:117], 12, v[116:117]
	v_ashrrev_i32_e32 v115, 31, v114
	v_lshl_add_u64 v[116:117], v[144:145], 0, v[116:117]
	v_lshl_add_u64 v[118:119], v[114:115], 2, s[6:7]
	s_waitcnt vmcnt(8)
	v_mov_b32_e32 v112, v178
	v_pk_mul_f32 v[110:111], v[110:111], v[112:113] op_sel_hi:[1,0]
	v_pk_mul_f32 v[108:109], v[108:109], v[112:113] op_sel_hi:[1,0]
	v_pk_mul_f32 v[106:107], v[106:107], v[112:113] op_sel_hi:[1,0]
	v_pk_mul_f32 v[104:105], v[104:105], v[112:113] op_sel_hi:[1,0]
	v_pk_mul_f32 v[102:103], v[102:103], v[112:113] op_sel_hi:[1,0]
	v_pk_mul_f32 v[100:101], v[100:101], v[112:113] op_sel_hi:[1,0]
	v_pk_mul_f32 v[120:121], v[98:99], v[112:113] op_sel_hi:[1,0]
	v_pk_mul_f32 v[112:113], v[96:97], v[112:113] op_sel_hi:[1,0]
	v_cvt_pk_bf16_f32 v96, v108, v109
	v_cvt_pk_bf16_f32 v97, v110, v111
	v_cvt_pk_bf16_f32 v98, v104, v105
	v_cvt_pk_bf16_f32 v99, v106, v107
	global_store_dwordx4 v[116:117], v[96:99], off
	s_nop 1
	v_cvt_pk_bf16_f32 v96, v100, v101
	v_cvt_pk_bf16_f32 v97, v102, v103
	v_cvt_pk_bf16_f32 v98, v112, v113
	v_cvt_pk_bf16_f32 v99, v120, v121
	global_store_dwordx4 v[116:117], v[96:99], off offset:256
	s_nop 0
	v_subrev_u32_e32 v100, s52, v114
	v_ashrrev_i32_e32 v101, 31, v100
	v_or_b32_e32 v98, 48, v148
	v_lshlrev_b64 v[100:101], 12, v[100:101]
	v_ashrrev_i32_e32 v99, 31, v98
	v_lshl_add_u64 v[100:101], v[144:145], 0, v[100:101]
	v_lshl_add_u64 v[102:103], v[98:99], 2, s[6:7]
	s_waitcnt vmcnt(9)
	v_mov_b32_e32 v96, v179
	v_pk_mul_f32 v[94:95], v[94:95], v[96:97] op_sel_hi:[1,0]
	v_pk_mul_f32 v[92:93], v[92:93], v[96:97] op_sel_hi:[1,0]
	v_pk_mul_f32 v[90:91], v[90:91], v[96:97] op_sel_hi:[1,0]
	v_pk_mul_f32 v[88:89], v[88:89], v[96:97] op_sel_hi:[1,0]
	v_pk_mul_f32 v[86:87], v[86:87], v[96:97] op_sel_hi:[1,0]
	v_pk_mul_f32 v[84:85], v[84:85], v[96:97] op_sel_hi:[1,0]
	v_pk_mul_f32 v[104:105], v[82:83], v[96:97] op_sel_hi:[1,0]
	v_pk_mul_f32 v[96:97], v[80:81], v[96:97] op_sel_hi:[1,0]
	v_cvt_pk_bf16_f32 v80, v92, v93
	v_cvt_pk_bf16_f32 v81, v94, v95
	v_cvt_pk_bf16_f32 v82, v88, v89
	v_cvt_pk_bf16_f32 v83, v90, v91
	global_store_dwordx4 v[100:101], v[80:83], off
	s_nop 1
	v_cvt_pk_bf16_f32 v80, v84, v85
	v_cvt_pk_bf16_f32 v81, v86, v87
	v_cvt_pk_bf16_f32 v82, v96, v97
	v_cvt_pk_bf16_f32 v83, v104, v105
	global_store_dwordx4 v[100:101], v[80:83], off offset:256
	s_nop 0
	s_waitcnt vmcnt(10)
	v_mov_b32_e32 v80, v180
	v_pk_mul_f32 v[78:79], v[78:79], v[80:81] op_sel_hi:[1,0]
	v_subrev_u32_e32 v82, s52, v98
	v_ashrrev_i32_e32 v83, 31, v82
	v_lshlrev_b64 v[82:83], 12, v[82:83]
	v_lshl_add_u64 v[82:83], v[144:145], 0, v[82:83]
	v_pk_mul_f32 v[76:77], v[76:77], v[80:81] op_sel_hi:[1,0]
	v_pk_mul_f32 v[74:75], v[74:75], v[80:81] op_sel_hi:[1,0]
	v_pk_mul_f32 v[72:73], v[72:73], v[80:81] op_sel_hi:[1,0]
	v_pk_mul_f32 v[70:71], v[70:71], v[80:81] op_sel_hi:[1,0]
	v_pk_mul_f32 v[68:69], v[68:69], v[80:81] op_sel_hi:[1,0]
	v_pk_mul_f32 v[84:85], v[66:67], v[80:81] op_sel_hi:[1,0]
	v_pk_mul_f32 v[80:81], v[64:65], v[80:81] op_sel_hi:[1,0]
	v_cvt_pk_bf16_f32 v64, v76, v77
	v_cvt_pk_bf16_f32 v65, v78, v79
	v_cvt_pk_bf16_f32 v66, v72, v73
	v_cvt_pk_bf16_f32 v67, v74, v75
	global_store_dwordx4 v[82:83], v[64:67], off
	s_nop 1
	v_cvt_pk_bf16_f32 v64, v68, v69
	v_cvt_pk_bf16_f32 v65, v70, v71
	v_cvt_pk_bf16_f32 v66, v80, v81
	v_cvt_pk_bf16_f32 v67, v84, v85
	global_store_dwordx4 v[82:83], v[64:67], off offset:256
	s_nop 0
	s_waitcnt vmcnt(11)
	v_mov_b32_e32 v64, v181
	v_pk_mul_f32 v[62:63], v[62:63], v[64:65] op_sel_hi:[1,0]
	v_add_u32_e32 v66, 0x80, v142
	v_ashrrev_i32_e32 v67, 31, v66
	v_lshlrev_b64 v[66:67], 12, v[66:67]
	v_lshl_add_u64 v[66:67], v[144:145], 0, v[66:67]
	v_pk_mul_f32 v[60:61], v[60:61], v[64:65] op_sel_hi:[1,0]
	v_pk_mul_f32 v[58:59], v[58:59], v[64:65] op_sel_hi:[1,0]
	v_pk_mul_f32 v[56:57], v[56:57], v[64:65] op_sel_hi:[1,0]
	v_pk_mul_f32 v[54:55], v[54:55], v[64:65] op_sel_hi:[1,0]
	v_pk_mul_f32 v[52:53], v[52:53], v[64:65] op_sel_hi:[1,0]
	v_pk_mul_f32 v[68:69], v[50:51], v[64:65] op_sel_hi:[1,0]
	v_pk_mul_f32 v[64:65], v[48:49], v[64:65] op_sel_hi:[1,0]
	v_cvt_pk_bf16_f32 v48, v60, v61
	v_cvt_pk_bf16_f32 v49, v62, v63
	v_cvt_pk_bf16_f32 v50, v56, v57
	v_cvt_pk_bf16_f32 v51, v58, v59
	global_store_dwordx4 v[66:67], v[48:51], off
	s_nop 1
	v_cvt_pk_bf16_f32 v48, v52, v53
	v_cvt_pk_bf16_f32 v49, v54, v55
	v_cvt_pk_bf16_f32 v50, v64, v65
	v_cvt_pk_bf16_f32 v51, v68, v69
	global_store_dwordx4 v[66:67], v[48:51], off offset:256
	s_nop 0
	s_waitcnt vmcnt(12)
	v_mov_b32_e32 v48, v182
	v_pk_mul_f32 v[46:47], v[46:47], v[48:49] op_sel_hi:[1,0]
	v_add_u32_e32 v50, 0x90, v142
	v_ashrrev_i32_e32 v51, 31, v50
	v_lshlrev_b64 v[50:51], 12, v[50:51]
	v_lshl_add_u64 v[50:51], v[144:145], 0, v[50:51]
	v_pk_mul_f32 v[44:45], v[44:45], v[48:49] op_sel_hi:[1,0]
	v_pk_mul_f32 v[42:43], v[42:43], v[48:49] op_sel_hi:[1,0]
	v_pk_mul_f32 v[40:41], v[40:41], v[48:49] op_sel_hi:[1,0]
	v_pk_mul_f32 v[38:39], v[38:39], v[48:49] op_sel_hi:[1,0]
	v_pk_mul_f32 v[36:37], v[36:37], v[48:49] op_sel_hi:[1,0]
	v_pk_mul_f32 v[52:53], v[34:35], v[48:49] op_sel_hi:[1,0]
	v_pk_mul_f32 v[48:49], v[32:33], v[48:49] op_sel_hi:[1,0]
	v_cvt_pk_bf16_f32 v32, v44, v45
	v_cvt_pk_bf16_f32 v33, v46, v47
	v_cvt_pk_bf16_f32 v34, v40, v41
	v_cvt_pk_bf16_f32 v35, v42, v43
	global_store_dwordx4 v[50:51], v[32:35], off
	s_nop 1
	v_cvt_pk_bf16_f32 v32, v36, v37
	v_cvt_pk_bf16_f32 v33, v38, v39
	v_cvt_pk_bf16_f32 v34, v48, v49
	v_cvt_pk_bf16_f32 v35, v52, v53
	global_store_dwordx4 v[50:51], v[32:35], off offset:256
	s_nop 0
	s_waitcnt vmcnt(13)
	v_mov_b32_e32 v32, v183
	v_pk_mul_f32 v[30:31], v[30:31], v[32:33] op_sel_hi:[1,0]
	v_add_u32_e32 v34, 0xa0, v142
	v_ashrrev_i32_e32 v35, 31, v34
	v_lshlrev_b64 v[34:35], 12, v[34:35]
	v_lshl_add_u64 v[34:35], v[144:145], 0, v[34:35]
	v_pk_mul_f32 v[28:29], v[28:29], v[32:33] op_sel_hi:[1,0]
	v_pk_mul_f32 v[26:27], v[26:27], v[32:33] op_sel_hi:[1,0]
	v_pk_mul_f32 v[24:25], v[24:25], v[32:33] op_sel_hi:[1,0]
	v_pk_mul_f32 v[22:23], v[22:23], v[32:33] op_sel_hi:[1,0]
	v_pk_mul_f32 v[20:21], v[20:21], v[32:33] op_sel_hi:[1,0]
	v_pk_mul_f32 v[36:37], v[18:19], v[32:33] op_sel_hi:[1,0]
	v_pk_mul_f32 v[32:33], v[16:17], v[32:33] op_sel_hi:[1,0]
	v_cvt_pk_bf16_f32 v16, v28, v29
	v_cvt_pk_bf16_f32 v17, v30, v31
	v_cvt_pk_bf16_f32 v18, v24, v25
	v_cvt_pk_bf16_f32 v19, v26, v27
	global_store_dwordx4 v[34:35], v[16:19], off
	s_nop 1
	v_cvt_pk_bf16_f32 v16, v20, v21
	v_cvt_pk_bf16_f32 v17, v22, v23
	v_cvt_pk_bf16_f32 v18, v32, v33
	v_cvt_pk_bf16_f32 v19, v36, v37
	global_store_dwordx4 v[34:35], v[16:19], off offset:256
	s_nop 0
	s_waitcnt vmcnt(14)
	v_mov_b32_e32 v16, v184
	v_pk_mul_f32 v[14:15], v[14:15], v[16:17] op_sel_hi:[1,0]
	v_add_u32_e32 v18, 0xb0, v142
	v_ashrrev_i32_e32 v19, 31, v18
	v_lshlrev_b64 v[18:19], 12, v[18:19]
	v_lshl_add_u64 v[18:19], v[144:145], 0, v[18:19]
	v_pk_mul_f32 v[12:13], v[12:13], v[16:17] op_sel_hi:[1,0]
	v_pk_mul_f32 v[10:11], v[10:11], v[16:17] op_sel_hi:[1,0]
	v_pk_mul_f32 v[8:9], v[8:9], v[16:17] op_sel_hi:[1,0]
	v_pk_mul_f32 v[6:7], v[6:7], v[16:17] op_sel_hi:[1,0]
	v_pk_mul_f32 v[4:5], v[4:5], v[16:17] op_sel_hi:[1,0]
	v_pk_mul_f32 v[20:21], v[2:3], v[16:17] op_sel_hi:[1,0]
	v_pk_mul_f32 v[16:17], v[0:1], v[16:17] op_sel_hi:[1,0]
	v_cvt_pk_bf16_f32 v0, v12, v13
	v_cvt_pk_bf16_f32 v1, v14, v15
	v_cvt_pk_bf16_f32 v2, v8, v9
	v_cvt_pk_bf16_f32 v3, v10, v11
	global_store_dwordx4 v[18:19], v[0:3], off
	s_nop 1
	v_cvt_pk_bf16_f32 v0, v4, v5
	v_cvt_pk_bf16_f32 v1, v6, v7
	v_cvt_pk_bf16_f32 v2, v16, v17
	v_cvt_pk_bf16_f32 v3, v20, v21
	global_store_dwordx4 v[18:19], v[0:3], off offset:256
	s_cbranch_vccnz .LBB0_1171
	s_andn2_b64 vcc, exec, s[0:1]
	s_cbranch_vccnz .LBB0_1170
	s_barrier
	s_branch .LBB0_1170
